# GEMM prologue: per-row epilogue values (dinv, x last column) parked in LDS after stage 0 instead of draining all loads first
# speedup vs baseline: 1.0259x; 1.0012x over previous
_Z6k_gemmPKfPKDv8_DF16_S0_S0_PDF16_:
	s_load_dwordx2 s[8:9], s[0:1], 0x0
	s_load_dwordx2 s[10:11], s[0:1], 0x10
	s_load_dwordx2 s[12:13], s[0:1], 0x8
	s_load_dwordx4 s[4:7], s[0:1], 0x18
	s_mul_i32 s14, s2, 0xc4
	v_lshrrev_b32_e32 v1, 5, v0
	v_and_b32_e32 v89, 31, v0
	v_add_u32_e32 v2, s14, v1
	v_lshlrev_b32_e32 v154, 4, v89
	s_movk_i32 s15, 0x1664
	v_mad_u64_u32 v[150:151], s[0:1], v2, s15, v[154:155]
	s_lshl_b32 s16, s2, 2
	v_mul_u32_u24_e32 v245, 25, v1
	v_add_u32_e32 v245, s16, v245
	v_and_b32_e32 v245, 31, v245
	v_xor_b32_e32 v246, 16, v245
	v_lshlrev_b32_e32 v247, 2, v246
	v_sub_u32_e32 v244, v150, v247
	v_lshlrev_b32_e32 v247, 2, v245
	v_sub_u32_e32 v150, v150, v247
	v_add_u32_e32 v247, 24, v245
	v_lshrrev_b32_e32 v247, 2, v247
	v_sub_u32_e32 v247, v89, v247
	v_max_i32_e32 v247, 0, v247
	v_lshlrev_b32_e32 v247, 4, v247
	v_sub_u32_e32 v250, v150, v247
	v_add_u32_e32 v247, 24, v246
	v_lshrrev_b32_e32 v247, 2, v247
	v_sub_u32_e32 v247, v89, v247
	v_max_i32_e32 v247, 0, v247
	v_lshlrev_b32_e32 v247, 4, v247
	v_sub_u32_e32 v251, v244, v247
	s_movk_i32 s17, 0x1ee0
	v_mul_u32_u24_e32 v242, s17, v1
	v_add_u32_e32 v243, 0xffffff00, v242
	v_lshl_add_u32 v247, v89, 3, v242
	v_lshlrev_b32_e32 v248, 1, v245
	v_sub_u32_e32 v248, v247, v248
	v_add_u32_e32 v234, 64, v248
	v_add_u32_e32 v235, 0x42, v248
	v_add_u32_e32 v236, 0x44, v248
	v_add_u32_e32 v237, 0x46, v248
	v_lshlrev_b32_e32 v248, 1, v246
	v_sub_u32_e32 v248, v247, v248
	v_add_u32_e32 v238, 64, v248
	v_add_u32_e32 v239, 0x42, v248
	v_add_u32_e32 v240, 0x44, v248
	v_add_u32_e32 v241, 0x46, v248
	v_and_b32_e32 v247, 7, v89
	v_lshl_add_u32 v247, v247, 3, v242
	v_mov_b32_e32 v248, 0
	v_mov_b32_e32 v249, 0
	ds_write_b64 v247, v[248:249] offset:0
	ds_write_b64 v247, v[248:249] offset:608
	ds_write_b64 v247, v[248:249] offset:1216
	ds_write_b64 v247, v[248:249] offset:1824
	ds_write_b64 v247, v[248:249] offset:2432
	ds_write_b64 v247, v[248:249] offset:3040
	ds_write_b64 v247, v[248:249] offset:3648
	ds_write_b64 v247, v[248:249] offset:4256
	ds_write_b64 v247, v[248:249] offset:4864
	ds_write_b64 v247, v[248:249] offset:5472
	ds_write_b64 v247, v[248:249] offset:6080
	ds_write_b64 v247, v[248:249] offset:6688
	ds_write_b64 v247, v[248:249] offset:7296
	v_mov_b32_e32 v2, 2
	v_lshlrev_b32_sdwa v2, v2, v0 dst_sel:DWORD dst_unused:UNUSED_PAD src0_sel:DWORD src1_sel:BYTE_0
	v_mov_b32_e32 v3, 0
	s_waitcnt lgkmcnt(0)
	v_lshl_add_u64 v[4:5], s[4:5], 0, v[2:3]
	s_mov_b32 s0, 0x166000
	v_add_co_u32_e32 v4, vcc, s0, v4
	v_add_u32_e32 v6, 0x111514dc, v154
	s_nop 0
	v_addc_co_u32_e32 v5, vcc, 0, v5, vcc
	global_load_dword v90, v[4:5], off
	v_add_u32_e32 v4, 0x16640, v244
	v_min_u32_e32 v2, v150, v6
	v_min_u32_e32 v4, v4, v6
	global_load_dwordx4 v[82:85], v2, s[8:9] nt
	global_load_dwordx4 v[78:81], v4, s[8:9] nt
	v_add_u32_e32 v2, 0x2cc80, v150
	v_min_u32_e32 v2, v2, v6
	v_add_u32_e32 v4, 0x432c0, v244
	v_min_u32_e32 v4, v4, v6
	global_load_dwordx4 v[74:77], v2, s[8:9] nt
	global_load_dwordx4 v[70:73], v4, s[8:9] nt
	v_add_u32_e32 v2, 0x59900, v150
	v_min_u32_e32 v2, v2, v6
	v_add_u32_e32 v4, 0x6ff40, v244
	v_min_u32_e32 v4, v4, v6
	global_load_dwordx4 v[66:69], v2, s[8:9] nt
	global_load_dwordx4 v[54:57], v4, s[8:9] nt
	v_add_u32_e32 v2, 0x86580, v150
	v_min_u32_e32 v2, v2, v6
	v_add_u32_e32 v4, 0x9cbc0, v244
	v_min_u32_e32 v4, v4, v6
	global_load_dwordx4 v[62:65], v2, s[8:9] nt
	global_load_dwordx4 v[58:61], v4, s[8:9] nt
	v_add_u32_e32 v2, 0xb3200, v150
	v_min_u32_e32 v2, v2, v6
	v_add_u32_e32 v4, 0xc9840, v244
	v_min_u32_e32 v4, v4, v6
	global_load_dwordx4 v[46:49], v2, s[8:9] nt
	global_load_dwordx4 v[38:41], v4, s[8:9] nt
	v_add_u32_e32 v2, 0xdfe80, v150
	v_min_u32_e32 v2, v2, v6
	v_add_u32_e32 v4, 0xf64c0, v244
	s_movk_i32 s3, 0xc4
	v_or_b32_e32 v7, 0xc0, v1
	v_min_u32_e32 v4, v4, v6
	global_load_dwordx4 v[34:37], v2, s[8:9] nt
	global_load_dwordx4 v[14:17], v4, s[8:9] nt
	v_add_u32_e32 v2, 0x10cb00, v150
	v_min_u32_e32 v2, v2, v6
	v_cmp_gt_u32_e64 s[0:1], s3, v7
	v_bfe_u32 v87, v0, 4, 2
	v_and_b32_e32 v86, 15, v0
	v_cndmask_b32_e64 v2, 0, v2, s[0:1]
	global_load_dwordx4 v[10:13], v2, s[8:9] nt
	v_lshlrev_b32_e32 v2, 12, v87
	v_lshl_add_u64 v[4:5], s[12:13], 0, v[2:3]
	v_lshlrev_b32_e32 v2, 3, v0
	v_and_b32_e32 v2, 0xe00, v2
	v_lshl_add_u64 v[4:5], v[4:5], 0, v[2:3]
	v_lshlrev_b32_e32 v2, 4, v86
	v_lshl_add_u64 v[152:153], v[4:5], 0, v[2:3]
	s_movk_i32 s2, 0x4000
	v_add_co_u32_e32 v2, vcc, s2, v152
	s_mov_b32 s2, 0x8000
	s_nop 0
	v_addc_co_u32_e32 v3, vcc, 0, v153, vcc
	global_load_dwordx4 v[26:29], v[152:153], off sc1
	global_load_dwordx4 v[50:53], v[152:153], off offset:256 sc1
	global_load_dwordx4 v[18:21], v[2:3], off sc1
	global_load_dwordx4 v[42:45], v[2:3], off offset:256 sc1
	v_add_co_u32_e32 v2, vcc, s2, v152
	s_movk_i32 s2, 0xd0
	s_nop 0
	v_addc_co_u32_e32 v3, vcc, 0, v153, vcc
	v_add_co_u32_e32 v92, vcc, 0xc000, v152
	global_load_dwordx4 v[22:25], v[2:3], off sc1
	global_load_dwordx4 v[30:33], v[2:3], off offset:256 sc1
	v_addc_co_u32_e32 v93, vcc, 0, v153, vcc
	global_load_dwordx4 v[6:9], v[92:93], off sc1
	global_load_dwordx4 v[2:5], v[92:93], off offset:256 sc1
	v_cmp_gt_u32_e32 vcc, s2, v0
	v_add_u32_e32 v88, 0x111516dc, v154
	s_and_saveexec_b64 s[4:5], vcc
	s_cbranch_execz .LBB2_5
	v_cndmask_b32_e32 v91, 0, v0, vcc
	v_cmp_gt_u32_e32 vcc, s3, v91
	v_add_u32_e32 v91, s14, v91
	s_mov_b32 s2, 0xc350
	v_cmp_gt_i32_e64 s[2:3], s2, v91
	v_ashrrev_i32_e32 v92, 31, v91
	s_and_b64 s[2:3], vcc, s[2:3]
	v_cndmask_b32_e64 v93, 0, v92, s[2:3]
	v_mov_b32_e32 v92, 0xc34f
	v_cndmask_b32_e64 v92, v92, v91, s[2:3]
	v_mov_b64_e32 v[94:95], s[8:9]
	v_mad_i64_i32 v[94:95], s[12:13], v92, s15, v[94:95]
	v_add_co_u32_e32 v94, vcc, 0x1000, v94
	v_lshl_add_u64 v[92:93], v[92:93], 2, s[10:11]
	s_nop 0
	v_addc_co_u32_e32 v95, vcc, 0, v95, vcc
	global_load_dword v252, v[92:93], off
	global_load_dword v253, v[94:95], off offset:1632
	s_mov_b64 s[18:19], s[2:3]

.LBB2_7:
	s_or_b64 exec, exec, s[2:3]
	s_waitcnt vmcnt(21)
	v_add_u32_e32 v90, 0x200, v150
	v_min_u32_e32 v90, v90, v88
	global_load_dwordx4 v[110:113], v90, s[8:9] nt
	v_mul_u32_u24_e32 v1, 0x120, v1
	s_waitcnt vmcnt(21)
	v_cvt_pk_f16_f32 v85, v84, v85
	v_cvt_pk_f16_f32 v84, v82, v83
	v_lshl_add_u32 v1, v89, 3, v1
	s_movk_i32 s2, 0x120
	ds_write_b16 v234, v84 offset:0
	ds_write_b16_d16_hi v235, v84 offset:0
	ds_write_b16 v236, v85 offset:0
	ds_write_b16_d16_hi v237, v85 offset:0
	v_add_u32_e32 v82, 0x16840, v244
	v_min_u32_e32 v82, v82, v88
	global_load_dwordx4 v[114:117], v82, s[8:9] nt
	s_waitcnt vmcnt(21)
	v_cvt_pk_f16_f32 v81, v80, v81
	v_cvt_pk_f16_f32 v80, v78, v79
	ds_write_b16 v238, v80 offset:608
	ds_write_b16_d16_hi v239, v80 offset:608
	ds_write_b16 v240, v81 offset:608
	ds_write_b16_d16_hi v241, v81 offset:608
	v_add_u32_e32 v78, 0x2ce80, v150
	v_min_u32_e32 v78, v78, v88
	global_load_dwordx4 v[118:121], v78, s[8:9] nt
	s_waitcnt vmcnt(21)
	v_cvt_pk_f16_f32 v77, v76, v77
	v_cvt_pk_f16_f32 v76, v74, v75
	ds_write_b16 v234, v76 offset:1216
	ds_write_b16_d16_hi v235, v76 offset:1216
	ds_write_b16 v236, v77 offset:1216
	ds_write_b16_d16_hi v237, v77 offset:1216
	v_add_u32_e32 v74, 0x434c0, v244
	v_min_u32_e32 v74, v74, v88
	global_load_dwordx4 v[74:77], v74, s[8:9] nt
	s_waitcnt vmcnt(21)
	v_cvt_pk_f16_f32 v73, v72, v73
	v_cvt_pk_f16_f32 v72, v70, v71
	ds_write_b16 v238, v72 offset:1824
	ds_write_b16_d16_hi v239, v72 offset:1824
	ds_write_b16 v240, v73 offset:1824
	ds_write_b16_d16_hi v241, v73 offset:1824
	v_add_u32_e32 v70, 0x59b00, v150
	v_min_u32_e32 v70, v70, v88
	global_load_dwordx4 v[78:81], v70, s[8:9] nt
	s_waitcnt vmcnt(21)
	v_cvt_pk_f16_f32 v69, v68, v69
	v_cvt_pk_f16_f32 v68, v66, v67
	ds_write_b16 v234, v68 offset:2432
	ds_write_b16_d16_hi v235, v68 offset:2432
	ds_write_b16 v236, v69 offset:2432
	ds_write_b16_d16_hi v237, v69 offset:2432
	v_add_u32_e32 v66, 0x70140, v244
	v_min_u32_e32 v66, v66, v88
	global_load_dwordx4 v[82:85], v66, s[8:9] nt
	s_waitcnt vmcnt(21)
	v_cvt_pk_f16_f32 v57, v56, v57
	v_cvt_pk_f16_f32 v56, v54, v55
	ds_write_b16 v238, v56 offset:3040
	ds_write_b16_d16_hi v239, v56 offset:3040
	ds_write_b16 v240, v57 offset:3040
	ds_write_b16_d16_hi v241, v57 offset:3040
	v_add_u32_e32 v54, 0x86780, v150
	v_min_u32_e32 v54, v54, v88
	global_load_dwordx4 v[54:57], v54, s[8:9] nt
	s_waitcnt vmcnt(21)
	v_cvt_pk_f16_f32 v65, v64, v65
	v_cvt_pk_f16_f32 v64, v62, v63
	ds_write_b16 v234, v64 offset:3648
	ds_write_b16_d16_hi v235, v64 offset:3648
	ds_write_b16 v236, v65 offset:3648
	ds_write_b16_d16_hi v237, v65 offset:3648
	v_add_u32_e32 v62, 0x9cdc0, v244
	v_min_u32_e32 v62, v62, v88
	global_load_dwordx4 v[90:93], v62, s[8:9] nt
	s_waitcnt vmcnt(21)
	v_cvt_pk_f16_f32 v61, v60, v61
	v_cvt_pk_f16_f32 v60, v58, v59
	ds_write_b16 v238, v60 offset:4256
	ds_write_b16_d16_hi v239, v60 offset:4256
	ds_write_b16 v240, v61 offset:4256
	ds_write_b16_d16_hi v241, v61 offset:4256
	v_add_u32_e32 v58, 0xb3400, v150
	v_min_u32_e32 v58, v58, v88
	global_load_dwordx4 v[94:97], v58, s[8:9] nt
	s_waitcnt vmcnt(21)
	v_cvt_pk_f16_f32 v49, v48, v49
	v_cvt_pk_f16_f32 v48, v46, v47
	ds_write_b16 v234, v48 offset:4864
	ds_write_b16_d16_hi v235, v48 offset:4864
	ds_write_b16 v236, v49 offset:4864
	ds_write_b16_d16_hi v237, v49 offset:4864
	v_add_u32_e32 v46, 0xc9a40, v244
	v_min_u32_e32 v46, v46, v88
	global_load_dwordx4 v[98:101], v46, s[8:9] nt
	s_waitcnt vmcnt(21)
	v_cvt_pk_f16_f32 v41, v40, v41
	v_cvt_pk_f16_f32 v40, v38, v39
	ds_write_b16 v238, v40 offset:5472
	ds_write_b16_d16_hi v239, v40 offset:5472
	ds_write_b16 v240, v41 offset:5472
	ds_write_b16_d16_hi v241, v41 offset:5472
	v_add_u32_e32 v38, 0xe0080, v150
	v_min_u32_e32 v38, v38, v88
	global_load_dwordx4 v[102:105], v38, s[8:9] nt
	s_waitcnt vmcnt(21)
	v_cvt_pk_f16_f32 v37, v36, v37
	v_cvt_pk_f16_f32 v36, v34, v35
	ds_write_b16 v234, v36 offset:6080
	ds_write_b16_d16_hi v235, v36 offset:6080
	ds_write_b16 v236, v37 offset:6080
	ds_write_b16_d16_hi v237, v37 offset:6080
	v_add_u32_e32 v34, 0xf66c0, v244
	v_min_u32_e32 v34, v34, v88
	global_load_dwordx4 v[106:109], v34, s[8:9] nt
	s_waitcnt vmcnt(21)
	v_cvt_pk_f16_f32 v17, v16, v17
	v_cvt_pk_f16_f32 v16, v14, v15
	ds_write_b16 v238, v16 offset:6688
	ds_write_b16_d16_hi v239, v16 offset:6688
	ds_write_b16 v240, v17 offset:6688
	ds_write_b16_d16_hi v241, v17 offset:6688
	v_add_u32_e32 v14, 0x10cd00, v150
	v_min_u32_e32 v14, v14, v88
	v_cndmask_b32_e64 v14, 0, v14, s[0:1]
	global_load_dwordx4 v[46:49], v14, s[8:9] nt
	s_waitcnt vmcnt(21)
	v_cvt_pk_f16_f32 v13, v12, v13
	v_cvt_pk_f16_f32 v12, v10, v11
	ds_write_b16 v234, v12 offset:7296
	ds_write_b16_d16_hi v235, v12 offset:7296
	ds_write_b16 v236, v13 offset:7296
	ds_write_b16_d16_hi v237, v13 offset:7296
	s_movk_i32 s16, 0xd0
	v_cmp_gt_u32_e32 vcc, s16, v0
	s_and_saveexec_b64 s[4:5], vcc
	s_cbranch_execz .Ltailv_skip
	s_waitcnt vmcnt(13)
	v_cndmask_b32_e64 v255, 0, v252, s[18:19]
	v_cndmask_b32_e64 v254, 0, v253, s[18:19]
	v_mov_b32_e32 v252, 0x1ee00
	v_lshl_add_u32 v252, v0, 3, v252
	ds_write_b64 v252, v[254:255]
.Ltailv_skip:
	s_or_b64 exec, exec, s[4:5]
	s_waitcnt lgkmcnt(0)
	s_barrier
	v_sub_u32_e32 v245, v234, v243
	v_add_u32_e32 v246, 0xfffffdc0, v245
	v_min_u32_e32 v245, v245, v246
	v_add_u32_e32 v234, v242, v245
	v_sub_u32_e32 v245, v235, v243
	v_add_u32_e32 v246, 0xfffffdc0, v245
	v_min_u32_e32 v245, v245, v246
	v_add_u32_e32 v235, v242, v245
	v_sub_u32_e32 v245, v236, v243
	v_add_u32_e32 v246, 0xfffffdc0, v245
	v_min_u32_e32 v245, v245, v246
	v_add_u32_e32 v236, v242, v245
	v_sub_u32_e32 v245, v237, v243
	v_add_u32_e32 v246, 0xfffffdc0, v245
	v_min_u32_e32 v245, v245, v246
	v_add_u32_e32 v237, v242, v245
	v_sub_u32_e32 v245, v238, v243
	v_add_u32_e32 v246, 0xfffffdc0, v245
	v_min_u32_e32 v245, v245, v246
	v_add_u32_e32 v238, v242, v245
	v_sub_u32_e32 v245, v239, v243
	v_add_u32_e32 v246, 0xfffffdc0, v245
	v_min_u32_e32 v245, v245, v246
	v_add_u32_e32 v239, v242, v245
	v_sub_u32_e32 v245, v240, v243
	v_add_u32_e32 v246, 0xfffffdc0, v245
	v_min_u32_e32 v245, v245, v246
	v_add_u32_e32 v240, v242, v245
	v_sub_u32_e32 v245, v241, v243
	v_add_u32_e32 v246, 0xfffffdc0, v245
	v_min_u32_e32 v245, v245, v246
	v_add_u32_e32 v241, v242, v245
	s_mov_b32 s3, 0x10000
	v_add_co_u32_e32 v10, vcc, s3, v152
	s_mov_b32 s3, 0x14000
	s_nop 0
	v_addc_co_u32_e32 v11, vcc, 0, v153, vcc
	v_add_co_u32_e32 v58, vcc, s3, v152
	global_load_dwordx4 v[34:37], v[10:11], off sc1
	global_load_dwordx4 v[38:41], v[10:11], off offset:256 sc1
	v_addc_co_u32_e32 v59, vcc, 0, v153, vcc
	global_load_dwordx4 v[14:17], v[58:59], off sc1
	global_load_dwordx4 v[10:13], v[58:59], off offset:256 sc1
	v_lshlrev_b32_e32 v58, 4, v87
	v_add_u32_e32 v224, 0x111518dc, v154
	v_mad_u32_u24 v151, v86, s17, v58
	ds_read_b128 v[58:61], v151 offset:0
	v_add_u32_e32 v62, 0x400, v150
	s_waitcnt vmcnt(24) lgkmcnt(0)
	v_mfma_f32_16x16x32_f16 v[86:89], v[26:29], v[58:61], 0
	s_waitcnt vmcnt(23)
	v_mfma_f32_16x16x32_f16 v[122:125], v[50:53], v[58:61], 0
	v_min_u32_e32 v58, v62, v224
	global_load_dwordx4 v[58:61], v58, s[8:9] nt
	s_waitcnt vmcnt(17)
	v_cvt_pk_f16_f32 v63, v112, v113
	v_cvt_pk_f16_f32 v62, v110, v111
	v_add_u32_e32 v155, 0xea00, v1
	ds_write_b16 v234, v62 offset:0
	ds_write_b16_d16_hi v235, v62 offset:0
	ds_write_b16 v236, v63 offset:0
	ds_write_b16_d16_hi v237, v63 offset:0
	ds_read_b128 v[62:65], v151 offset:608
	ds_read_b128 v[66:69], v151 offset:1216
	s_waitcnt lgkmcnt(1)
	v_mfma_f32_16x16x32_f16 v[110:113], v[26:29], v[62:65], 0
	v_mfma_f32_16x16x32_f16 v[126:129], v[50:53], v[62:65], 0
	s_waitcnt lgkmcnt(0)
	v_mfma_f32_16x16x32_f16 v[130:133], v[26:29], v[66:69], 0
	v_mfma_f32_16x16x32_f16 v[134:137], v[50:53], v[66:69], 0
	ds_read_b128 v[62:65], v151 offset:1824
	ds_read_b128 v[66:69], v151 offset:2432
	s_waitcnt lgkmcnt(1)
	v_mfma_f32_16x16x32_f16 v[138:141], v[26:29], v[62:65], 0
	v_mfma_f32_16x16x32_f16 v[142:145], v[50:53], v[62:65], 0
	s_waitcnt lgkmcnt(0)
	v_mfma_f32_16x16x32_f16 v[146:149], v[26:29], v[66:69], 0
	v_mfma_f32_16x16x32_f16 v[156:159], v[50:53], v[66:69], 0
	v_add_u32_e32 v62, 0x16a40, v244
	v_min_u32_e32 v62, v62, v224
	global_load_dwordx4 v[62:65], v62, s[8:9] nt
	s_waitcnt vmcnt(17)
	v_cvt_pk_f16_f32 v67, v116, v117
	v_cvt_pk_f16_f32 v66, v114, v115
	ds_write_b16 v238, v66 offset:608
	ds_write_b16_d16_hi v239, v66 offset:608
	ds_write_b16 v240, v67 offset:608
	ds_write_b16_d16_hi v241, v67 offset:608
	ds_read_b128 v[66:69], v151 offset:3040
	ds_read_b128 v[70:73], v151 offset:4864
	s_waitcnt lgkmcnt(1)
	v_mfma_f32_16x16x32_f16 v[114:117], v[26:29], v[66:69], 0
	v_mfma_f32_16x16x32_f16 v[160:163], v[50:53], v[66:69], 0
	ds_read_b128 v[66:69], v151 offset:3648
	ds_read_b128 v[164:167], v151 offset:4256
	s_waitcnt lgkmcnt(1)
	v_mfma_f32_16x16x32_f16 v[168:171], v[26:29], v[66:69], 0
	v_mfma_f32_16x16x32_f16 v[172:175], v[50:53], v[66:69], 0
	s_waitcnt lgkmcnt(0)
	v_mfma_f32_16x16x32_f16 v[176:179], v[26:29], v[164:167], 0
	v_mfma_f32_16x16x32_f16 v[164:167], v[50:53], v[164:167], 0
	v_mfma_f32_16x16x32_f16 v[180:183], v[26:29], v[70:73], 0
	v_mfma_f32_16x16x32_f16 v[184:187], v[50:53], v[70:73], 0
	v_add_u32_e32 v66, 0x2d080, v150
	v_min_u32_e32 v66, v66, v224
	global_load_dwordx4 v[66:69], v66, s[8:9] nt
	s_waitcnt vmcnt(17)
	v_cvt_pk_f16_f32 v71, v120, v121
	v_cvt_pk_f16_f32 v70, v118, v119
	ds_write_b16 v234, v70 offset:1216
	ds_write_b16_d16_hi v235, v70 offset:1216
	ds_write_b16 v236, v71 offset:1216
	ds_write_b16_d16_hi v237, v71 offset:1216
	ds_read_b128 v[70:73], v151 offset:5472
	ds_read_b128 v[118:121], v151 offset:6080
	s_waitcnt lgkmcnt(1)
	v_mfma_f32_16x16x32_f16 v[188:191], v[26:29], v[70:73], 0
	v_mfma_f32_16x16x32_f16 v[192:195], v[50:53], v[70:73], 0
	ds_read_b128 v[70:73], v151 offset:6688
	ds_read_b128 v[200:203], v151 offset:7296
	s_waitcnt lgkmcnt(2)
	v_mfma_f32_16x16x32_f16 v[196:199], v[26:29], v[118:121], 0
	v_mfma_f32_16x16x32_f16 v[118:121], v[50:53], v[118:121], 0
	s_waitcnt lgkmcnt(1)
	v_mfma_f32_16x16x32_f16 v[204:207], v[26:29], v[70:73], 0
	v_mfma_f32_16x16x32_f16 v[208:211], v[50:53], v[70:73], 0
	s_waitcnt lgkmcnt(0)
	v_mfma_f32_16x16x32_f16 v[26:29], v[26:29], v[200:203], 0
	v_mfma_f32_16x16x32_f16 v[200:203], v[50:53], v[200:203], 0
	v_add_u32_e32 v50, 0x436c0, v244
	v_min_u32_e32 v50, v50, v224
	global_load_dwordx4 v[70:73], v50, s[8:9] nt
	s_waitcnt vmcnt(17)
	v_cvt_pk_f16_f32 v51, v76, v77
	v_cvt_pk_f16_f32 v50, v74, v75
	ds_write_b16 v238, v50 offset:1824
	ds_write_b16_d16_hi v239, v50 offset:1824
	ds_write_b16 v240, v51 offset:1824
	ds_write_b16_d16_hi v241, v51 offset:1824
	ds_read_b128 v[50:53], v151 offset:64
	ds_read_b128 v[74:77], v151 offset:672
	s_waitcnt lgkmcnt(1)
	v_mfma_f32_16x16x32_f16 v[86:89], v[18:21], v[50:53], v[86:89]
	v_mfma_f32_16x16x32_f16 v[122:125], v[42:45], v[50:53], v[122:125]
	s_waitcnt lgkmcnt(0)
	v_mfma_f32_16x16x32_f16 v[110:113], v[18:21], v[74:77], v[110:113]
	v_mfma_f32_16x16x32_f16 v[126:129], v[42:45], v[74:77], v[126:129]
	ds_read_b128 v[50:53], v151 offset:1280
	ds_read_b128 v[74:77], v151 offset:1888
	s_waitcnt lgkmcnt(1)
	v_mfma_f32_16x16x32_f16 v[130:133], v[18:21], v[50:53], v[130:133]
	v_mfma_f32_16x16x32_f16 v[134:137], v[42:45], v[50:53], v[134:137]
	s_waitcnt lgkmcnt(0)
	v_mfma_f32_16x16x32_f16 v[138:141], v[18:21], v[74:77], v[138:141]
	v_mfma_f32_16x16x32_f16 v[142:145], v[42:45], v[74:77], v[142:145]
	v_add_u32_e32 v50, 0x59d00, v150
	v_min_u32_e32 v50, v50, v224
	global_load_dwordx4 v[74:77], v50, s[8:9] nt
	s_waitcnt vmcnt(17)
	v_cvt_pk_f16_f32 v51, v80, v81
	v_cvt_pk_f16_f32 v50, v78, v79
	ds_write_b16 v234, v50 offset:2432
	ds_write_b16_d16_hi v235, v50 offset:2432
	ds_write_b16 v236, v51 offset:2432
	ds_write_b16_d16_hi v237, v51 offset:2432
	ds_read_b128 v[50:53], v151 offset:2496
	ds_read_b128 v[78:81], v151 offset:3104
	s_waitcnt lgkmcnt(1)
	v_mfma_f32_16x16x32_f16 v[146:149], v[18:21], v[50:53], v[146:149]
	v_mfma_f32_16x16x32_f16 v[156:159], v[42:45], v[50:53], v[156:159]
	s_waitcnt lgkmcnt(0)
	v_mfma_f32_16x16x32_f16 v[114:117], v[18:21], v[78:81], v[114:117]
	v_mfma_f32_16x16x32_f16 v[160:163], v[42:45], v[78:81], v[160:163]
	ds_read_b128 v[50:53], v151 offset:3712
	ds_read_b128 v[78:81], v151 offset:4320
	s_waitcnt lgkmcnt(1)
	v_mfma_f32_16x16x32_f16 v[168:171], v[18:21], v[50:53], v[168:171]
	v_mfma_f32_16x16x32_f16 v[172:175], v[42:45], v[50:53], v[172:175]
	s_waitcnt lgkmcnt(0)
	v_mfma_f32_16x16x32_f16 v[176:179], v[18:21], v[78:81], v[176:179]
	v_mfma_f32_16x16x32_f16 v[164:167], v[42:45], v[78:81], v[164:167]
	v_add_u32_e32 v50, 0x70340, v244
	v_min_u32_e32 v50, v50, v224
	global_load_dwordx4 v[78:81], v50, s[8:9] nt
	s_waitcnt vmcnt(17)
	v_cvt_pk_f16_f32 v51, v84, v85
	v_cvt_pk_f16_f32 v50, v82, v83
	ds_write_b16 v238, v50 offset:3040
	ds_write_b16_d16_hi v239, v50 offset:3040
	ds_write_b16 v240, v51 offset:3040
	ds_write_b16_d16_hi v241, v51 offset:3040
	ds_read_b128 v[50:53], v151 offset:4928
	ds_read_b128 v[82:85], v151 offset:5536
	s_waitcnt lgkmcnt(1)
	v_mfma_f32_16x16x32_f16 v[180:183], v[18:21], v[50:53], v[180:183]
	v_mfma_f32_16x16x32_f16 v[184:187], v[42:45], v[50:53], v[184:187]
	s_waitcnt lgkmcnt(0)
	v_mfma_f32_16x16x32_f16 v[188:191], v[18:21], v[82:85], v[188:191]
	v_mfma_f32_16x16x32_f16 v[192:195], v[42:45], v[82:85], v[192:195]
	ds_read_b128 v[50:53], v151 offset:6144
	ds_read_b128 v[82:85], v151 offset:6752
	s_waitcnt lgkmcnt(1)
	v_mfma_f32_16x16x32_f16 v[196:199], v[18:21], v[50:53], v[196:199]
	v_mfma_f32_16x16x32_f16 v[118:121], v[42:45], v[50:53], v[118:121]
	s_waitcnt lgkmcnt(0)
	v_mfma_f32_16x16x32_f16 v[204:207], v[18:21], v[82:85], v[204:207]
	v_mfma_f32_16x16x32_f16 v[208:211], v[42:45], v[82:85], v[208:211]
	v_add_u32_e32 v50, 0x86980, v150
	v_min_u32_e32 v50, v50, v224
	global_load_dwordx4 v[82:85], v50, s[8:9] nt
	s_waitcnt vmcnt(17)
	v_cvt_pk_f16_f32 v51, v56, v57
	v_cvt_pk_f16_f32 v50, v54, v55
	ds_write_b16 v234, v50 offset:3648
	ds_write_b16_d16_hi v235, v50 offset:3648
	ds_write_b16 v236, v51 offset:3648
	ds_write_b16_d16_hi v237, v51 offset:3648
	ds_read_b128 v[212:215], v151 offset:7360
	s_mov_b32 s2, 0x18000
	s_waitcnt lgkmcnt(0)
	v_mfma_f32_16x16x32_f16 v[216:219], v[18:21], v[212:215], v[26:29]
	v_add_co_u32_e32 v18, vcc, s2, v152
	s_mov_b32 s2, 0x1c000
	s_nop 0
	v_addc_co_u32_e32 v19, vcc, 0, v153, vcc
	global_load_dwordx4 v[50:53], v[18:19], off sc1
	global_load_dwordx4 v[54:57], v[18:19], off offset:256 sc1
	v_add_co_u32_e32 v18, vcc, s2, v152
	v_mfma_f32_16x16x32_f16 v[42:45], v[42:45], v[212:215], v[200:203]
	s_nop 0
	v_addc_co_u32_e32 v19, vcc, 0, v153, vcc
	global_load_dwordx4 v[26:29], v[18:19], off sc1
	s_nop 0
	global_load_dwordx4 v[18:21], v[18:19], off offset:256 sc1
	ds_read_b128 v[200:203], v151 offset:128
	ds_read_b128 v[212:215], v151 offset:736
	s_waitcnt lgkmcnt(1)
	v_mfma_f32_16x16x32_f16 v[220:223], v[22:25], v[200:203], v[86:89]
	s_nop 2
	ds_read_b128 v[86:89], v151 offset:1344
	v_mfma_f32_16x16x32_f16 v[122:125], v[30:33], v[200:203], v[122:125]
	s_waitcnt lgkmcnt(1)
	v_mfma_f32_16x16x32_f16 v[110:113], v[22:25], v[212:215], v[110:113]
	v_mfma_f32_16x16x32_f16 v[126:129], v[30:33], v[212:215], v[126:129]
	s_waitcnt lgkmcnt(0)
	v_mfma_f32_16x16x32_f16 v[130:133], v[22:25], v[86:89], v[130:133]
	v_mfma_f32_16x16x32_f16 v[134:137], v[30:33], v[86:89], v[134:137]
	v_add_u32_e32 v86, 0x9cfc0, v244
	v_min_u32_e32 v86, v86, v224
	global_load_dwordx4 v[86:89], v86, s[8:9] nt
	s_waitcnt vmcnt(21)
	v_cvt_pk_f16_f32 v93, v92, v93
	v_cvt_pk_f16_f32 v92, v90, v91
	ds_write_b16 v238, v92 offset:4256
	ds_write_b16_d16_hi v239, v92 offset:4256
	ds_write_b16 v240, v93 offset:4256
	ds_write_b16_d16_hi v241, v93 offset:4256
	ds_read_b128 v[90:93], v151 offset:1952
	ds_read_b128 v[200:203], v151 offset:2560
	s_waitcnt lgkmcnt(1)
	v_mfma_f32_16x16x32_f16 v[138:141], v[22:25], v[90:93], v[138:141]
	v_mfma_f32_16x16x32_f16 v[142:145], v[30:33], v[90:93], v[142:145]
	s_waitcnt lgkmcnt(0)
	v_mfma_f32_16x16x32_f16 v[146:149], v[22:25], v[200:203], v[146:149]
	v_mfma_f32_16x16x32_f16 v[156:159], v[30:33], v[200:203], v[156:159]
	ds_read_b128 v[90:93], v151 offset:3168
	ds_read_b128 v[200:203], v151 offset:3776
	s_waitcnt lgkmcnt(1)
	v_mfma_f32_16x16x32_f16 v[114:117], v[22:25], v[90:93], v[114:117]
	v_mfma_f32_16x16x32_f16 v[160:163], v[30:33], v[90:93], v[160:163]
	s_waitcnt lgkmcnt(0)
	v_mfma_f32_16x16x32_f16 v[168:171], v[22:25], v[200:203], v[168:171]
	v_mfma_f32_16x16x32_f16 v[172:175], v[30:33], v[200:203], v[172:175]
	v_add_u32_e32 v90, 0xb3600, v150
	v_min_u32_e32 v90, v90, v224
	global_load_dwordx4 v[90:93], v90, s[8:9] nt
	s_waitcnt vmcnt(21)
	v_cvt_pk_f16_f32 v97, v96, v97
	v_cvt_pk_f16_f32 v96, v94, v95
	ds_write_b16 v234, v96 offset:4864
	ds_write_b16_d16_hi v235, v96 offset:4864
	ds_write_b16 v236, v97 offset:4864
	ds_write_b16_d16_hi v237, v97 offset:4864
	ds_read_b128 v[94:97], v151 offset:4384
	ds_read_b128 v[200:203], v151 offset:6208
	s_waitcnt lgkmcnt(1)
	v_mfma_f32_16x16x32_f16 v[176:179], v[22:25], v[94:97], v[176:179]
	v_mfma_f32_16x16x32_f16 v[164:167], v[30:33], v[94:97], v[164:167]
	ds_read_b128 v[94:97], v151 offset:4992
	ds_read_b128 v[212:215], v151 offset:5600
	s_waitcnt lgkmcnt(1)
	v_mfma_f32_16x16x32_f16 v[180:183], v[22:25], v[94:97], v[180:183]
	v_mfma_f32_16x16x32_f16 v[184:187], v[30:33], v[94:97], v[184:187]
	s_waitcnt lgkmcnt(0)
	v_mfma_f32_16x16x32_f16 v[188:191], v[22:25], v[212:215], v[188:191]
	v_mfma_f32_16x16x32_f16 v[192:195], v[30:33], v[212:215], v[192:195]
	v_mfma_f32_16x16x32_f16 v[196:199], v[22:25], v[200:203], v[196:199]
	v_mfma_f32_16x16x32_f16 v[118:121], v[30:33], v[200:203], v[118:121]
	v_add_u32_e32 v94, 0xc9c40, v244
	v_min_u32_e32 v94, v94, v224
	global_load_dwordx4 v[94:97], v94, s[8:9] nt
	s_waitcnt vmcnt(21)
	v_cvt_pk_f16_f32 v101, v100, v101
	v_cvt_pk_f16_f32 v100, v98, v99
	ds_write_b16 v238, v100 offset:5472
	ds_write_b16_d16_hi v239, v100 offset:5472
	ds_write_b16 v240, v101 offset:5472
	ds_write_b16_d16_hi v241, v101 offset:5472
	ds_read_b128 v[98:101], v151 offset:6816
	ds_read_b128 v[200:203], v151 offset:7424
	s_waitcnt lgkmcnt(1)
	v_mfma_f32_16x16x32_f16 v[204:207], v[22:25], v[98:101], v[204:207]
	v_mfma_f32_16x16x32_f16 v[208:211], v[30:33], v[98:101], v[208:211]
	s_waitcnt lgkmcnt(0)
	v_mfma_f32_16x16x32_f16 v[30:33], v[30:33], v[200:203], v[42:45]
	s_nop 2
	ds_read_b128 v[42:45], v151 offset:192
	ds_read_b128 v[98:101], v151 offset:800
	v_mfma_f32_16x16x32_f16 v[22:25], v[22:25], v[200:203], v[216:219]
	s_waitcnt lgkmcnt(1)
	v_mfma_f32_16x16x32_f16 v[200:203], v[6:9], v[42:45], v[220:223]
	v_mfma_f32_16x16x32_f16 v[122:125], v[2:5], v[42:45], v[122:125]
	s_waitcnt lgkmcnt(0)
	v_mfma_f32_16x16x32_f16 v[212:215], v[6:9], v[98:101], v[110:113]
	v_mfma_f32_16x16x32_f16 v[126:129], v[2:5], v[98:101], v[126:129]
	v_add_u32_e32 v42, 0xe0280, v150
	v_min_u32_e32 v42, v42, v224
	global_load_dwordx4 v[98:101], v42, s[8:9] nt
	s_waitcnt vmcnt(21)
	v_cvt_pk_f16_f32 v43, v104, v105
	v_cvt_pk_f16_f32 v42, v102, v103
	ds_write_b16 v234, v42 offset:6080
	ds_write_b16_d16_hi v235, v42 offset:6080
	ds_write_b16 v236, v43 offset:6080
	ds_write_b16_d16_hi v237, v43 offset:6080
	ds_read_b128 v[42:45], v151 offset:1408
	ds_read_b128 v[102:105], v151 offset:2016
	s_waitcnt lgkmcnt(1)
	v_mfma_f32_16x16x32_f16 v[130:133], v[6:9], v[42:45], v[130:133]
	v_mfma_f32_16x16x32_f16 v[134:137], v[2:5], v[42:45], v[134:137]
	s_waitcnt lgkmcnt(0)
	v_mfma_f32_16x16x32_f16 v[138:141], v[6:9], v[102:105], v[138:141]
	v_mfma_f32_16x16x32_f16 v[142:145], v[2:5], v[102:105], v[142:145]
	ds_read_b128 v[42:45], v151 offset:2624
	ds_read_b128 v[102:105], v151 offset:3232
	s_waitcnt lgkmcnt(1)
	v_mfma_f32_16x16x32_f16 v[146:149], v[6:9], v[42:45], v[146:149]
	v_mfma_f32_16x16x32_f16 v[216:219], v[2:5], v[42:45], v[156:159]
	s_waitcnt lgkmcnt(0)
	v_mfma_f32_16x16x32_f16 v[220:223], v[6:9], v[102:105], v[114:117]
	v_mfma_f32_16x16x32_f16 v[158:161], v[2:5], v[102:105], v[160:163]
	v_add_u32_e32 v42, 0xf68c0, v244
	v_min_u32_e32 v42, v42, v224
	global_load_dwordx4 v[102:105], v42, s[8:9] nt
	s_waitcnt vmcnt(21)
	v_cvt_pk_f16_f32 v43, v108, v109
	v_cvt_pk_f16_f32 v42, v106, v107
	ds_write_b16 v238, v42 offset:6688
	ds_write_b16_d16_hi v239, v42 offset:6688
	ds_write_b16 v240, v43 offset:6688
	ds_write_b16_d16_hi v241, v43 offset:6688
	ds_read_b128 v[42:45], v151 offset:3840
	ds_read_b128 v[106:109], v151 offset:4448
	s_waitcnt lgkmcnt(1)
	v_mfma_f32_16x16x32_f16 v[168:171], v[6:9], v[42:45], v[168:171]
	v_mfma_f32_16x16x32_f16 v[172:175], v[2:5], v[42:45], v[172:175]
	s_waitcnt lgkmcnt(0)
	v_mfma_f32_16x16x32_f16 v[176:179], v[6:9], v[106:109], v[176:179]
	v_mfma_f32_16x16x32_f16 v[162:165], v[2:5], v[106:109], v[164:167]
	ds_read_b128 v[42:45], v151 offset:5056
	ds_read_b128 v[106:109], v151 offset:5664
	s_waitcnt lgkmcnt(1)
	v_mfma_f32_16x16x32_f16 v[180:183], v[6:9], v[42:45], v[180:183]
	v_mfma_f32_16x16x32_f16 v[184:187], v[2:5], v[42:45], v[184:187]
	s_waitcnt lgkmcnt(0)
	v_mfma_f32_16x16x32_f16 v[188:191], v[6:9], v[106:109], v[188:191]
	v_mfma_f32_16x16x32_f16 v[192:195], v[2:5], v[106:109], v[192:195]
	v_add_u32_e32 v42, 0x10cf00, v150
	v_min_u32_e32 v42, v42, v224
	v_cndmask_b32_e64 v42, 0, v42, s[0:1]
	global_load_dwordx4 v[106:109], v42, s[8:9] nt
	s_waitcnt vmcnt(21)
	v_cvt_pk_f16_f32 v43, v48, v49
	v_cvt_pk_f16_f32 v42, v46, v47
	ds_write_b16 v234, v42 offset:7296
	ds_write_b16_d16_hi v235, v42 offset:7296
	ds_write_b16 v236, v43 offset:7296
	ds_write_b16_d16_hi v237, v43 offset:7296
	ds_read_b128 v[42:45], v151 offset:6272
	ds_read_b128 v[46:49], v151 offset:6880
	ds_read_b128 v[110:113], v151 offset:7488
	s_mov_b32 s2, 0x20000
	v_add_co_u32_e32 v114, vcc, s2, v152
	s_mov_b32 s2, 0x24000
	s_nop 0
	v_addc_co_u32_e32 v115, vcc, 0, v153, vcc
	s_waitcnt lgkmcnt(2)
	v_mfma_f32_16x16x32_f16 v[196:199], v[6:9], v[42:45], v[196:199]
	s_waitcnt lgkmcnt(0)
	s_barrier
	v_sub_u32_e32 v245, v234, v243
	v_add_u32_e32 v246, 0xfffffdc0, v245
	v_min_u32_e32 v245, v245, v246
	v_add_u32_e32 v234, v242, v245
	v_sub_u32_e32 v245, v235, v243
	v_add_u32_e32 v246, 0xfffffdc0, v245
	v_min_u32_e32 v245, v245, v246
	v_add_u32_e32 v235, v242, v245
	v_sub_u32_e32 v245, v236, v243
	v_add_u32_e32 v246, 0xfffffdc0, v245
	v_min_u32_e32 v245, v245, v246
	v_add_u32_e32 v236, v242, v245
	v_sub_u32_e32 v245, v237, v243
	v_add_u32_e32 v246, 0xfffffdc0, v245
	v_min_u32_e32 v245, v245, v246
	v_add_u32_e32 v237, v242, v245
	v_sub_u32_e32 v245, v238, v243
	v_add_u32_e32 v246, 0xfffffdc0, v245
	v_min_u32_e32 v245, v245, v246
	v_add_u32_e32 v238, v242, v245
	v_sub_u32_e32 v245, v239, v243
	v_add_u32_e32 v246, 0xfffffdc0, v245
	v_min_u32_e32 v245, v245, v246
	v_add_u32_e32 v239, v242, v245
	v_sub_u32_e32 v245, v240, v243
	v_add_u32_e32 v246, 0xfffffdc0, v245
	v_min_u32_e32 v245, v245, v246
	v_add_u32_e32 v240, v242, v245
	v_sub_u32_e32 v245, v241, v243
	v_add_u32_e32 v246, 0xfffffdc0, v245
	v_min_u32_e32 v245, v245, v246
	v_add_u32_e32 v241, v242, v245
	v_mfma_f32_16x16x32_f16 v[204:207], v[6:9], v[46:49], v[204:207]
	v_mfma_f32_16x16x32_f16 v[228:231], v[6:9], v[110:113], v[22:25]
	v_add_co_u32_e32 v6, vcc, s2, v152
	s_nop 1
	v_addc_co_u32_e32 v7, vcc, 0, v153, vcc
	v_mfma_f32_16x16x32_f16 v[224:227], v[2:5], v[42:45], v[118:121]
	v_mfma_f32_16x16x32_f16 v[208:211], v[2:5], v[46:49], v[208:211]
	global_load_dwordx4 v[42:45], v[114:115], off sc1
	global_load_dwordx4 v[46:49], v[114:115], off offset:256 sc1
	global_load_dwordx4 v[22:25], v[6:7], off sc1
	s_nop 0
	global_load_dwordx4 v[6:9], v[6:7], off offset:256 sc1
	v_mfma_f32_16x16x32_f16 v[2:5], v[2:5], v[110:113], v[30:33]
	v_add_u32_e32 v157, 0x11151adc, v154
	s_nop 1
	ds_read_b128 v[30:33], v151 offset:256
	v_add_u32_e32 v156, 0xea00, v151
	v_add_u32_e32 v110, 0x600, v150
	s_waitcnt vmcnt(24) lgkmcnt(0)
	v_mfma_f32_16x16x32_f16 v[200:203], v[34:37], v[30:33], v[200:203]
	s_waitcnt vmcnt(23)
	v_mfma_f32_16x16x32_f16 v[30:33], v[38:41], v[30:33], v[122:125]
	v_min_u32_e32 v110, v110, v157
	global_load_dwordx4 v[110:113], v110, s[8:9] nt
	s_waitcnt vmcnt(21)
	v_cvt_pk_f16_f32 v61, v60, v61
	v_cvt_pk_f16_f32 v60, v58, v59
	ds_write_b16 v234, v60 offset:0
	ds_write_b16_d16_hi v235, v60 offset:0
	ds_write_b16 v236, v61 offset:0
	ds_write_b16_d16_hi v237, v61 offset:0
	ds_read_b128 v[58:61], v151 offset:864
	ds_read_b128 v[114:117], v151 offset:1472
	s_waitcnt lgkmcnt(1)
	v_mfma_f32_16x16x32_f16 v[122:125], v[34:37], v[58:61], v[212:215]
	v_mfma_f32_16x16x32_f16 v[58:61], v[38:41], v[58:61], v[126:129]
	s_waitcnt lgkmcnt(0)
	v_mfma_f32_16x16x32_f16 v[126:129], v[34:37], v[114:117], v[130:133]
	v_mfma_f32_16x16x32_f16 v[130:133], v[38:41], v[114:117], v[134:137]
	ds_read_b128 v[114:117], v151 offset:2080
	ds_read_b128 v[118:121], v151 offset:2688
	s_waitcnt lgkmcnt(1)
	v_mfma_f32_16x16x32_f16 v[134:137], v[34:37], v[114:117], v[138:141]
	v_mfma_f32_16x16x32_f16 v[138:141], v[38:41], v[114:117], v[142:145]
	s_waitcnt lgkmcnt(0)
	v_mfma_f32_16x16x32_f16 v[142:145], v[34:37], v[118:121], v[146:149]
	v_mfma_f32_16x16x32_f16 v[146:149], v[38:41], v[118:121], v[216:219]
	v_add_u32_e32 v114, 0x16c40, v244
	v_min_u32_e32 v114, v114, v157
	global_load_dwordx4 v[114:117], v114, s[8:9] nt
	s_waitcnt vmcnt(21)
	v_cvt_pk_f16_f32 v65, v64, v65
	v_cvt_pk_f16_f32 v64, v62, v63
	ds_write_b16 v238, v64 offset:608
	ds_write_b16_d16_hi v239, v64 offset:608
	ds_write_b16 v240, v65 offset:608
	ds_write_b16_d16_hi v241, v65 offset:608
	ds_read_b128 v[62:65], v151 offset:3296
	ds_read_b128 v[118:121], v151 offset:5120
	s_waitcnt lgkmcnt(1)
	v_mfma_f32_16x16x32_f16 v[212:215], v[34:37], v[62:65], v[220:223]
	v_mfma_f32_16x16x32_f16 v[62:65], v[38:41], v[62:65], v[158:161]
	s_nop 2
	ds_read_b128 v[158:161], v151 offset:3904
	ds_read_b128 v[216:219], v151 offset:4512
	s_waitcnt lgkmcnt(1)
	v_mfma_f32_16x16x32_f16 v[166:169], v[34:37], v[158:161], v[168:171]
	v_mfma_f32_16x16x32_f16 v[158:161], v[38:41], v[158:161], v[172:175]
	s_waitcnt lgkmcnt(0)
	v_mfma_f32_16x16x32_f16 v[170:173], v[34:37], v[216:219], v[176:179]
	v_mfma_f32_16x16x32_f16 v[162:165], v[38:41], v[216:219], v[162:165]
	v_mfma_f32_16x16x32_f16 v[174:177], v[34:37], v[118:121], v[180:183]
	v_mfma_f32_16x16x32_f16 v[178:181], v[38:41], v[118:121], v[184:187]
	v_add_u32_e32 v118, 0x2d280, v150
	v_min_u32_e32 v118, v118, v157
	global_load_dwordx4 v[118:121], v118, s[8:9] nt
	s_waitcnt vmcnt(21)
	v_cvt_pk_f16_f32 v69, v68, v69
	v_cvt_pk_f16_f32 v68, v66, v67
	ds_write_b16 v234, v68 offset:1216
	ds_write_b16_d16_hi v235, v68 offset:1216
	ds_write_b16 v236, v69 offset:1216
	ds_write_b16_d16_hi v237, v69 offset:1216
	ds_read_b128 v[66:69], v151 offset:5728
	ds_read_b128 v[182:185], v151 offset:6336
	s_waitcnt lgkmcnt(1)
	v_mfma_f32_16x16x32_f16 v[186:189], v[34:37], v[66:69], v[188:191]
	v_mfma_f32_16x16x32_f16 v[190:193], v[38:41], v[66:69], v[192:195]
	ds_read_b128 v[66:69], v151 offset:6944
	ds_read_b128 v[216:219], v151 offset:7552
	s_waitcnt lgkmcnt(2)
	v_mfma_f32_16x16x32_f16 v[194:197], v[34:37], v[182:185], v[196:199]
	v_mfma_f32_16x16x32_f16 v[182:185], v[38:41], v[182:185], v[224:227]
	s_waitcnt lgkmcnt(1)
	v_mfma_f32_16x16x32_f16 v[204:207], v[34:37], v[66:69], v[204:207]
	v_mfma_f32_16x16x32_f16 v[208:211], v[38:41], v[66:69], v[208:211]
	s_waitcnt lgkmcnt(0)
	v_mfma_f32_16x16x32_f16 v[220:223], v[34:37], v[216:219], v[228:231]
	v_mfma_f32_16x16x32_f16 v[2:5], v[38:41], v[216:219], v[2:5]
	v_add_u32_e32 v34, 0x438c0, v244
	v_min_u32_e32 v34, v34, v157
	global_load_dwordx4 v[34:37], v34, s[8:9] nt
	s_waitcnt vmcnt(21)
	v_cvt_pk_f16_f32 v39, v72, v73
	v_cvt_pk_f16_f32 v38, v70, v71
	ds_write_b16 v238, v38 offset:1824
	ds_write_b16_d16_hi v239, v38 offset:1824
	ds_write_b16 v240, v39 offset:1824
	ds_write_b16_d16_hi v241, v39 offset:1824
	ds_read_b128 v[38:41], v151 offset:320
	ds_read_b128 v[66:69], v151 offset:928
	s_waitcnt lgkmcnt(1)
	v_mfma_f32_16x16x32_f16 v[198:201], v[14:17], v[38:41], v[200:203]
	v_mfma_f32_16x16x32_f16 v[38:41], v[10:13], v[38:41], v[30:33]
	s_waitcnt lgkmcnt(0)
	v_mfma_f32_16x16x32_f16 v[216:219], v[10:13], v[66:69], v[58:61]
	s_nop 0
	ds_read_b128 v[30:33], v151 offset:1536
	s_nop 0
	ds_read_b128 v[58:61], v151 offset:2144
	v_mfma_f32_16x16x32_f16 v[122:125], v[14:17], v[66:69], v[122:125]
	s_waitcnt lgkmcnt(1)
	v_mfma_f32_16x16x32_f16 v[126:129], v[14:17], v[30:33], v[126:129]
	v_mfma_f32_16x16x32_f16 v[130:133], v[10:13], v[30:33], v[130:133]
	s_waitcnt lgkmcnt(0)
	v_mfma_f32_16x16x32_f16 v[134:137], v[14:17], v[58:61], v[134:137]
	v_mfma_f32_16x16x32_f16 v[138:141], v[10:13], v[58:61], v[138:141]
	v_add_u32_e32 v30, 0x59f00, v150
	v_min_u32_e32 v30, v30, v157
	global_load_dwordx4 v[66:69], v30, s[8:9] nt
	s_waitcnt vmcnt(21)
	v_cvt_pk_f16_f32 v31, v76, v77
	v_cvt_pk_f16_f32 v30, v74, v75
	ds_write_b16 v234, v30 offset:2432
	ds_write_b16_d16_hi v235, v30 offset:2432
	ds_write_b16 v236, v31 offset:2432
	ds_write_b16_d16_hi v237, v31 offset:2432
	ds_read_b128 v[30:33], v151 offset:2752
	ds_read_b128 v[58:61], v151 offset:3360
	s_waitcnt lgkmcnt(1)
	v_mfma_f32_16x16x32_f16 v[142:145], v[14:17], v[30:33], v[142:145]
	v_mfma_f32_16x16x32_f16 v[146:149], v[10:13], v[30:33], v[146:149]
	s_waitcnt lgkmcnt(0)
	v_mfma_f32_16x16x32_f16 v[212:215], v[14:17], v[58:61], v[212:215]
	v_mfma_f32_16x16x32_f16 v[224:227], v[10:13], v[58:61], v[62:65]
	ds_read_b128 v[30:33], v151 offset:3968
	ds_read_b128 v[58:61], v151 offset:4576
	s_waitcnt lgkmcnt(1)
	v_mfma_f32_16x16x32_f16 v[166:169], v[14:17], v[30:33], v[166:169]
	v_mfma_f32_16x16x32_f16 v[158:161], v[10:13], v[30:33], v[158:161]
	s_waitcnt lgkmcnt(0)
	v_mfma_f32_16x16x32_f16 v[170:173], v[14:17], v[58:61], v[170:173]
	v_mfma_f32_16x16x32_f16 v[162:165], v[10:13], v[58:61], v[162:165]
	v_add_u32_e32 v30, 0x70540, v244
	v_min_u32_e32 v30, v30, v157
	global_load_dwordx4 v[70:73], v30, s[8:9] nt
	s_waitcnt vmcnt(21)
	v_cvt_pk_f16_f32 v31, v80, v81
	v_cvt_pk_f16_f32 v30, v78, v79
	ds_write_b16 v238, v30 offset:3040
	ds_write_b16_d16_hi v239, v30 offset:3040
	ds_write_b16 v240, v31 offset:3040
	ds_write_b16_d16_hi v241, v31 offset:3040
	ds_read_b128 v[30:33], v151 offset:5184
	ds_read_b128 v[58:61], v151 offset:5792
	s_waitcnt lgkmcnt(1)
	v_mfma_f32_16x16x32_f16 v[174:177], v[14:17], v[30:33], v[174:177]
	v_mfma_f32_16x16x32_f16 v[178:181], v[10:13], v[30:33], v[178:181]
	s_waitcnt lgkmcnt(0)
	v_mfma_f32_16x16x32_f16 v[186:189], v[14:17], v[58:61], v[186:189]
	v_mfma_f32_16x16x32_f16 v[190:193], v[10:13], v[58:61], v[190:193]
	ds_read_b128 v[30:33], v151 offset:6400
	ds_read_b128 v[58:61], v151 offset:7008
	s_waitcnt lgkmcnt(1)
	v_mfma_f32_16x16x32_f16 v[194:197], v[14:17], v[30:33], v[194:197]
	v_mfma_f32_16x16x32_f16 v[182:185], v[10:13], v[30:33], v[182:185]
	s_waitcnt lgkmcnt(0)
	v_mfma_f32_16x16x32_f16 v[202:205], v[14:17], v[58:61], v[204:207]
	v_mfma_f32_16x16x32_f16 v[206:209], v[10:13], v[58:61], v[208:211]
	v_add_u32_e32 v30, 0x86b80, v150
	v_min_u32_e32 v30, v30, v157
	global_load_dwordx4 v[74:77], v30, s[8:9] nt
	s_waitcnt vmcnt(21)
	v_cvt_pk_f16_f32 v31, v84, v85
	v_cvt_pk_f16_f32 v30, v82, v83
	ds_write_b16 v234, v30 offset:3648
	ds_write_b16_d16_hi v235, v30 offset:3648
	ds_write_b16 v236, v31 offset:3648
	ds_write_b16_d16_hi v237, v31 offset:3648
	ds_read_b128 v[78:81], v151 offset:7616
	s_mov_b32 s2, 0x28000
	s_waitcnt lgkmcnt(0)
	v_mfma_f32_16x16x32_f16 v[220:223], v[14:17], v[78:81], v[220:223]
	v_add_co_u32_e32 v14, vcc, s2, v152
	s_mov_b32 s2, 0x2c000
	s_nop 0
	v_addc_co_u32_e32 v15, vcc, 0, v153, vcc
	global_load_dwordx4 v[58:61], v[14:15], off sc1
	global_load_dwordx4 v[62:65], v[14:15], off offset:256 sc1
	v_add_co_u32_e32 v14, vcc, s2, v152
	v_mfma_f32_16x16x32_f16 v[2:5], v[10:13], v[78:81], v[2:5]
	s_nop 0
	v_addc_co_u32_e32 v15, vcc, 0, v153, vcc
	global_load_dwordx4 v[30:33], v[14:15], off sc1
	s_nop 0
	global_load_dwordx4 v[14:17], v[14:15], off offset:256 sc1
	ds_read_b128 v[10:13], v151 offset:384
	ds_read_b128 v[78:81], v151 offset:992
	s_waitcnt vmcnt(24) lgkmcnt(1)
	v_mfma_f32_16x16x32_f16 v[198:201], v[50:53], v[10:13], v[198:201]
	s_waitcnt vmcnt(23)
	v_mfma_f32_16x16x32_f16 v[10:13], v[54:57], v[10:13], v[38:41]
	s_waitcnt lgkmcnt(0)
	v_mfma_f32_16x16x32_f16 v[38:41], v[50:53], v[78:81], v[122:125]
	v_mfma_f32_16x16x32_f16 v[122:125], v[54:57], v[78:81], v[216:219]
	ds_read_b128 v[78:81], v151 offset:1600
	s_waitcnt lgkmcnt(0)
	v_mfma_f32_16x16x32_f16 v[126:129], v[50:53], v[78:81], v[126:129]
	v_mfma_f32_16x16x32_f16 v[130:133], v[54:57], v[78:81], v[130:133]
	v_add_u32_e32 v78, 0x9d1c0, v244
	v_min_u32_e32 v78, v78, v157
	global_load_dwordx4 v[78:81], v78, s[8:9] nt
	s_waitcnt vmcnt(21)
	v_cvt_pk_f16_f32 v83, v88, v89
	v_cvt_pk_f16_f32 v82, v86, v87
	ds_write_b16 v238, v82 offset:4256
	ds_write_b16_d16_hi v239, v82 offset:4256
	ds_write_b16 v240, v83 offset:4256
	ds_write_b16_d16_hi v241, v83 offset:4256
	ds_read_b128 v[82:85], v151 offset:2208
	ds_read_b128 v[86:89], v151 offset:2816
	s_waitcnt lgkmcnt(1)
	v_mfma_f32_16x16x32_f16 v[134:137], v[50:53], v[82:85], v[134:137]
	v_mfma_f32_16x16x32_f16 v[138:141], v[54:57], v[82:85], v[138:141]
	s_waitcnt lgkmcnt(0)
	v_mfma_f32_16x16x32_f16 v[142:145], v[50:53], v[86:89], v[142:145]
	v_mfma_f32_16x16x32_f16 v[146:149], v[54:57], v[86:89], v[146:149]
	ds_read_b128 v[82:85], v151 offset:3424
	ds_read_b128 v[86:89], v151 offset:4032
	s_waitcnt lgkmcnt(1)
	v_mfma_f32_16x16x32_f16 v[210:213], v[50:53], v[82:85], v[212:215]
	v_mfma_f32_16x16x32_f16 v[214:217], v[54:57], v[82:85], v[224:227]
	s_waitcnt lgkmcnt(0)
	v_mfma_f32_16x16x32_f16 v[166:169], v[50:53], v[86:89], v[166:169]
	v_mfma_f32_16x16x32_f16 v[158:161], v[54:57], v[86:89], v[158:161]
	v_add_u32_e32 v82, 0xb3800, v150
	v_min_u32_e32 v82, v82, v157
	global_load_dwordx4 v[82:85], v82, s[8:9] nt
	s_waitcnt vmcnt(21)
	v_cvt_pk_f16_f32 v87, v92, v93
	v_cvt_pk_f16_f32 v86, v90, v91
	ds_write_b16 v234, v86 offset:4864
	ds_write_b16_d16_hi v235, v86 offset:4864
	ds_write_b16 v236, v87 offset:4864
	ds_write_b16_d16_hi v237, v87 offset:4864
	ds_read_b128 v[86:89], v151 offset:4640
	ds_read_b128 v[90:93], v151 offset:6464
	s_waitcnt lgkmcnt(1)
	v_mfma_f32_16x16x32_f16 v[170:173], v[50:53], v[86:89], v[170:173]
	v_mfma_f32_16x16x32_f16 v[162:165], v[54:57], v[86:89], v[162:165]
	ds_read_b128 v[86:89], v151 offset:5248
	ds_read_b128 v[224:227], v151 offset:5856
	s_waitcnt lgkmcnt(1)
	v_mfma_f32_16x16x32_f16 v[174:177], v[50:53], v[86:89], v[174:177]
	v_mfma_f32_16x16x32_f16 v[178:181], v[54:57], v[86:89], v[178:181]
	s_waitcnt lgkmcnt(0)
	v_mfma_f32_16x16x32_f16 v[186:189], v[50:53], v[224:227], v[186:189]
	v_mfma_f32_16x16x32_f16 v[190:193], v[54:57], v[224:227], v[190:193]
	v_mfma_f32_16x16x32_f16 v[194:197], v[50:53], v[90:93], v[194:197]
	v_mfma_f32_16x16x32_f16 v[182:185], v[54:57], v[90:93], v[182:185]
	v_add_u32_e32 v86, 0xc9e40, v244
	v_min_u32_e32 v86, v86, v157
	global_load_dwordx4 v[86:89], v86, s[8:9] nt
	s_waitcnt vmcnt(21)
	v_cvt_pk_f16_f32 v91, v96, v97
	v_cvt_pk_f16_f32 v90, v94, v95
	ds_write_b16 v238, v90 offset:5472
	ds_write_b16_d16_hi v239, v90 offset:5472
	ds_write_b16 v240, v91 offset:5472
	ds_write_b16_d16_hi v241, v91 offset:5472
	ds_read_b128 v[90:93], v151 offset:7072
	ds_read_b128 v[94:97], v151 offset:7680
	s_waitcnt lgkmcnt(1)
	v_mfma_f32_16x16x32_f16 v[202:205], v[50:53], v[90:93], v[202:205]
	v_mfma_f32_16x16x32_f16 v[206:209], v[54:57], v[90:93], v[206:209]
	s_waitcnt lgkmcnt(0)
	v_mfma_f32_16x16x32_f16 v[218:221], v[50:53], v[94:97], v[220:223]
	v_mfma_f32_16x16x32_f16 v[54:57], v[54:57], v[94:97], v[2:5]
	s_nop 2
	ds_read_b128 v[2:5], v151 offset:448
	ds_read_b128 v[50:53], v151 offset:1056
	s_waitcnt lgkmcnt(1)
	v_mfma_f32_16x16x32_f16 v[198:201], v[26:29], v[2:5], v[198:201]
	v_mfma_f32_16x16x32_f16 v[222:225], v[18:21], v[2:5], v[10:13]
	s_waitcnt lgkmcnt(0)
	v_mfma_f32_16x16x32_f16 v[226:229], v[26:29], v[50:53], v[38:41]
	v_mfma_f32_16x16x32_f16 v[122:125], v[18:21], v[50:53], v[122:125]
	v_add_u32_e32 v2, 0xe0480, v150
	v_min_u32_e32 v2, v2, v157
	global_load_dwordx4 v[90:93], v2, s[8:9] nt
	s_waitcnt vmcnt(21)
	v_cvt_pk_f16_f32 v3, v100, v101
	v_cvt_pk_f16_f32 v2, v98, v99
	ds_write_b16 v234, v2 offset:6080
	ds_write_b16_d16_hi v235, v2 offset:6080
	ds_write_b16 v236, v3 offset:6080
	ds_write_b16_d16_hi v237, v3 offset:6080
	ds_read_b128 v[2:5], v151 offset:1664
	ds_read_b128 v[10:13], v151 offset:2272
	s_waitcnt lgkmcnt(1)
	v_mfma_f32_16x16x32_f16 v[126:129], v[26:29], v[2:5], v[126:129]
	v_mfma_f32_16x16x32_f16 v[130:133], v[18:21], v[2:5], v[130:133]
	s_waitcnt lgkmcnt(0)
	v_mfma_f32_16x16x32_f16 v[134:137], v[26:29], v[10:13], v[134:137]
	v_mfma_f32_16x16x32_f16 v[138:141], v[18:21], v[10:13], v[138:141]
	ds_read_b128 v[2:5], v151 offset:2880
	ds_read_b128 v[10:13], v151 offset:3488
	s_waitcnt lgkmcnt(1)
	v_mfma_f32_16x16x32_f16 v[142:145], v[26:29], v[2:5], v[142:145]
	v_mfma_f32_16x16x32_f16 v[146:149], v[18:21], v[2:5], v[146:149]
	s_waitcnt lgkmcnt(0)
	v_mfma_f32_16x16x32_f16 v[210:213], v[26:29], v[10:13], v[210:213]
	v_mfma_f32_16x16x32_f16 v[214:217], v[18:21], v[10:13], v[214:217]
	v_add_u32_e32 v2, 0xf6ac0, v244
	v_min_u32_e32 v2, v2, v157
	global_load_dwordx4 v[94:97], v2, s[8:9] nt
	s_waitcnt vmcnt(21)
	v_cvt_pk_f16_f32 v3, v104, v105
	v_cvt_pk_f16_f32 v2, v102, v103
	ds_write_b16 v238, v2 offset:6688
	ds_write_b16_d16_hi v239, v2 offset:6688
	ds_write_b16 v240, v3 offset:6688
	ds_write_b16_d16_hi v241, v3 offset:6688
	ds_read_b128 v[2:5], v151 offset:4096
	ds_read_b128 v[10:13], v151 offset:4704
	s_waitcnt lgkmcnt(1)
	v_mfma_f32_16x16x32_f16 v[166:169], v[26:29], v[2:5], v[166:169]
	v_mfma_f32_16x16x32_f16 v[158:161], v[18:21], v[2:5], v[158:161]
	s_waitcnt lgkmcnt(0)
	v_mfma_f32_16x16x32_f16 v[170:173], v[26:29], v[10:13], v[170:173]
	v_mfma_f32_16x16x32_f16 v[162:165], v[18:21], v[10:13], v[162:165]
	ds_read_b128 v[2:5], v151 offset:5312
	ds_read_b128 v[10:13], v151 offset:5920
	s_waitcnt lgkmcnt(1)
	v_mfma_f32_16x16x32_f16 v[174:177], v[26:29], v[2:5], v[174:177]
	v_mfma_f32_16x16x32_f16 v[178:181], v[18:21], v[2:5], v[178:181]
	s_waitcnt lgkmcnt(0)
	v_mfma_f32_16x16x32_f16 v[186:189], v[26:29], v[10:13], v[186:189]
	v_mfma_f32_16x16x32_f16 v[190:193], v[18:21], v[10:13], v[190:193]
	v_add_u32_e32 v2, 0x10d100, v150
	v_min_u32_e32 v2, v2, v157
	v_cndmask_b32_e64 v2, 0, v2, s[0:1]
	global_load_dwordx4 v[98:101], v2, s[8:9] nt
	s_waitcnt vmcnt(21)
	v_cvt_pk_f16_f32 v3, v108, v109
	v_cvt_pk_f16_f32 v2, v106, v107
	ds_write_b16 v234, v2 offset:7296
	ds_write_b16_d16_hi v235, v2 offset:7296
	ds_write_b16 v236, v3 offset:7296
	ds_write_b16_d16_hi v237, v3 offset:7296
	ds_read_b128 v[2:5], v151 offset:6528
	ds_read_b128 v[10:13], v151 offset:7136
	s_mov_b32 s2, 0x30000
	ds_read_b128 v[102:105], v151 offset:7744
	s_waitcnt lgkmcnt(0)
	v_mfma_f32_16x16x32_f16 v[194:197], v[26:29], v[2:5], v[194:197]
	s_barrier
	v_sub_u32_e32 v245, v234, v243
	v_add_u32_e32 v246, 0xfffffdc0, v245
	v_min_u32_e32 v245, v245, v246
	v_add_u32_e32 v234, v242, v245
	v_sub_u32_e32 v245, v235, v243
	v_add_u32_e32 v246, 0xfffffdc0, v245
	v_min_u32_e32 v245, v245, v246
	v_add_u32_e32 v235, v242, v245
	v_sub_u32_e32 v245, v236, v243
	v_add_u32_e32 v246, 0xfffffdc0, v245
	v_min_u32_e32 v245, v245, v246
	v_add_u32_e32 v236, v242, v245
	v_sub_u32_e32 v245, v237, v243
	v_add_u32_e32 v246, 0xfffffdc0, v245
	v_min_u32_e32 v245, v245, v246
	v_add_u32_e32 v237, v242, v245
	v_sub_u32_e32 v245, v238, v243
	v_add_u32_e32 v246, 0xfffffdc0, v245
	v_min_u32_e32 v245, v245, v246
	v_add_u32_e32 v238, v242, v245
	v_sub_u32_e32 v245, v239, v243
	v_add_u32_e32 v246, 0xfffffdc0, v245
	v_min_u32_e32 v245, v245, v246
	v_add_u32_e32 v239, v242, v245
	v_sub_u32_e32 v245, v240, v243
	v_add_u32_e32 v246, 0xfffffdc0, v245
	v_min_u32_e32 v245, v245, v246
	v_add_u32_e32 v240, v242, v245
	v_sub_u32_e32 v245, v241, v243
	v_add_u32_e32 v246, 0xfffffdc0, v245
	v_min_u32_e32 v245, v245, v246
	v_add_u32_e32 v241, v242, v245
	v_mfma_f32_16x16x32_f16 v[182:185], v[18:21], v[2:5], v[182:185]
	v_add_co_u32_e32 v2, vcc, s2, v152
	s_mov_b32 s2, 0x34000
	s_nop 0
	v_addc_co_u32_e32 v3, vcc, 0, v153, vcc
	global_load_dwordx4 v[38:41], v[2:3], off sc1
	global_load_dwordx4 v[50:53], v[2:3], off offset:256 sc1
	v_add_co_u32_e32 v2, vcc, s2, v152
	v_mfma_f32_16x16x32_f16 v[202:205], v[26:29], v[10:13], v[202:205]
	s_nop 0
	v_addc_co_u32_e32 v3, vcc, 0, v153, vcc
	v_mfma_f32_16x16x32_f16 v[206:209], v[18:21], v[10:13], v[206:209]
	global_load_dwordx4 v[10:13], v[2:3], off sc1
	s_nop 0
	global_load_dwordx4 v[2:5], v[2:3], off offset:256 sc1
	v_mfma_f32_16x16x32_f16 v[26:29], v[26:29], v[102:105], v[218:221]
	v_mfma_f32_16x16x32_f16 v[18:21], v[18:21], v[102:105], v[54:57]
	v_add_u32_e32 v157, 0x11151cdc, v154
	s_nop 1
	ds_read_b128 v[54:57], v151 offset:512
	v_add_u32_e32 v102, 0x800, v150
	s_waitcnt vmcnt(24) lgkmcnt(0)
	v_mfma_f32_16x16x32_f16 v[198:201], v[42:45], v[54:57], v[198:201]
	s_waitcnt vmcnt(23)
	v_mfma_f32_16x16x32_f16 v[54:57], v[46:49], v[54:57], v[222:225]
	v_min_u32_e32 v102, v102, v157
	global_load_dwordx4 v[102:105], v102, s[8:9] nt
	s_waitcnt vmcnt(21)
	v_cvt_pk_f16_f32 v107, v112, v113
	v_cvt_pk_f16_f32 v106, v110, v111
	ds_write_b16 v234, v106 offset:0
	ds_write_b16_d16_hi v235, v106 offset:0
	ds_write_b16 v236, v107 offset:0
	ds_write_b16_d16_hi v237, v107 offset:0
	ds_read_b128 v[106:109], v151 offset:1120
	ds_read_b128 v[110:113], v151 offset:1728
	s_waitcnt lgkmcnt(1)
	v_mfma_f32_16x16x32_f16 v[218:221], v[42:45], v[106:109], v[226:229]
	v_mfma_f32_16x16x32_f16 v[122:125], v[46:49], v[106:109], v[122:125]
	s_waitcnt lgkmcnt(0)
	v_mfma_f32_16x16x32_f16 v[126:129], v[42:45], v[110:113], v[126:129]
	v_mfma_f32_16x16x32_f16 v[130:133], v[46:49], v[110:113], v[130:133]
	ds_read_b128 v[106:109], v151 offset:2336
	ds_read_b128 v[110:113], v151 offset:2944
	s_waitcnt lgkmcnt(1)
	v_mfma_f32_16x16x32_f16 v[134:137], v[42:45], v[106:109], v[134:137]
	v_mfma_f32_16x16x32_f16 v[138:141], v[46:49], v[106:109], v[138:141]
	s_waitcnt lgkmcnt(0)
	v_mfma_f32_16x16x32_f16 v[142:145], v[42:45], v[110:113], v[142:145]
	v_mfma_f32_16x16x32_f16 v[146:149], v[46:49], v[110:113], v[146:149]
	v_add_u32_e32 v106, 0x16e40, v244
	v_min_u32_e32 v106, v106, v157
	global_load_dwordx4 v[106:109], v106, s[8:9] nt
	s_waitcnt vmcnt(21)
	v_cvt_pk_f16_f32 v111, v116, v117
	v_cvt_pk_f16_f32 v110, v114, v115
	ds_write_b16 v238, v110 offset:608
	ds_write_b16_d16_hi v239, v110 offset:608
	ds_write_b16 v240, v111 offset:608
	ds_write_b16_d16_hi v241, v111 offset:608
	ds_read_b128 v[110:113], v151 offset:3552
	ds_read_b128 v[114:117], v151 offset:5376
	s_waitcnt lgkmcnt(1)
	v_mfma_f32_16x16x32_f16 v[210:213], v[42:45], v[110:113], v[210:213]
	v_mfma_f32_16x16x32_f16 v[214:217], v[46:49], v[110:113], v[214:217]
	ds_read_b128 v[110:113], v151 offset:4160
	ds_read_b128 v[222:225], v151 offset:4768
	s_waitcnt lgkmcnt(1)
	v_mfma_f32_16x16x32_f16 v[166:169], v[42:45], v[110:113], v[166:169]
	v_mfma_f32_16x16x32_f16 v[158:161], v[46:49], v[110:113], v[158:161]
	s_waitcnt lgkmcnt(0)
	v_mfma_f32_16x16x32_f16 v[170:173], v[42:45], v[222:225], v[170:173]
	v_mfma_f32_16x16x32_f16 v[162:165], v[46:49], v[222:225], v[162:165]
	v_mfma_f32_16x16x32_f16 v[174:177], v[42:45], v[114:117], v[174:177]
	v_mfma_f32_16x16x32_f16 v[178:181], v[46:49], v[114:117], v[178:181]
	v_add_u32_e32 v110, 0x2d480, v150
	v_min_u32_e32 v110, v110, v157
	global_load_dwordx4 v[110:113], v110, s[8:9] nt
	s_waitcnt vmcnt(21)
	v_cvt_pk_f16_f32 v115, v120, v121
	v_cvt_pk_f16_f32 v114, v118, v119
	ds_write_b16 v234, v114 offset:1216
	ds_write_b16_d16_hi v235, v114 offset:1216
	ds_write_b16 v236, v115 offset:1216
	ds_write_b16_d16_hi v237, v115 offset:1216
	ds_read_b128 v[114:117], v151 offset:5984
	ds_read_b128 v[118:121], v151 offset:6592
	s_waitcnt lgkmcnt(1)
	v_mfma_f32_16x16x32_f16 v[186:189], v[42:45], v[114:117], v[186:189]
	v_mfma_f32_16x16x32_f16 v[190:193], v[46:49], v[114:117], v[190:193]
	s_waitcnt lgkmcnt(0)
	v_mfma_f32_16x16x32_f16 v[194:197], v[42:45], v[118:121], v[194:197]
	v_mfma_f32_16x16x32_f16 v[182:185], v[46:49], v[118:121], v[182:185]
	ds_read_b128 v[114:117], v151 offset:7200
	ds_read_b128 v[118:121], v151 offset:7808
	s_waitcnt lgkmcnt(1)
	v_mfma_f32_16x16x32_f16 v[202:205], v[42:45], v[114:117], v[202:205]
	v_mfma_f32_16x16x32_f16 v[206:209], v[46:49], v[114:117], v[206:209]
	s_waitcnt lgkmcnt(0)
	v_mfma_f32_16x16x32_f16 v[26:29], v[42:45], v[118:121], v[26:29]
	v_mfma_f32_16x16x32_f16 v[42:45], v[46:49], v[118:121], v[18:21]
	s_nop 2
	v_add_u32_e32 v18, 0x43ac0, v244
	v_min_u32_e32 v18, v18, v157
	global_load_dwordx4 v[114:117], v18, s[8:9] nt
	s_waitcnt vmcnt(21)
	v_cvt_pk_f16_f32 v19, v36, v37
	v_cvt_pk_f16_f32 v18, v34, v35
	ds_write_b16 v238, v18 offset:1824
	ds_write_b16_d16_hi v239, v18 offset:1824
	ds_write_b16 v240, v19 offset:1824
	ds_write_b16_d16_hi v241, v19 offset:1824
	ds_read_b128 v[18:21], v151 offset:0
	ds_read_b128 v[34:37], v151 offset:608
	s_waitcnt lgkmcnt(1)
	v_mfma_f32_16x16x32_f16 v[46:49], v[22:25], v[18:21], v[198:201]
	v_mfma_f32_16x16x32_f16 v[198:201], v[6:9], v[18:21], v[54:57]
	s_waitcnt lgkmcnt(0)
	v_mfma_f32_16x16x32_f16 v[218:221], v[22:25], v[34:37], v[218:221]
	v_mfma_f32_16x16x32_f16 v[222:225], v[6:9], v[34:37], v[122:125]
	ds_read_b128 v[18:21], v151 offset:1216
	ds_read_b128 v[34:37], v151 offset:1824
	s_waitcnt lgkmcnt(1)
	v_mfma_f32_16x16x32_f16 v[126:129], v[22:25], v[18:21], v[126:129]
	v_mfma_f32_16x16x32_f16 v[130:133], v[6:9], v[18:21], v[130:133]
	s_waitcnt lgkmcnt(0)
	v_mfma_f32_16x16x32_f16 v[134:137], v[22:25], v[34:37], v[134:137]
	v_mfma_f32_16x16x32_f16 v[138:141], v[6:9], v[34:37], v[138:141]
	v_add_u32_e32 v18, 0x5a100, v150
	v_min_u32_e32 v18, v18, v157
	global_load_dwordx4 v[118:121], v18, s[8:9] nt
	s_waitcnt vmcnt(21)
	v_cvt_pk_f16_f32 v19, v68, v69
	v_cvt_pk_f16_f32 v18, v66, v67
	ds_write_b16 v234, v18 offset:2432
	ds_write_b16_d16_hi v235, v18 offset:2432
	ds_write_b16 v236, v19 offset:2432
	ds_write_b16_d16_hi v237, v19 offset:2432
	ds_read_b128 v[18:21], v151 offset:2432
	ds_read_b128 v[34:37], v151 offset:3040
	s_waitcnt lgkmcnt(1)
	v_mfma_f32_16x16x32_f16 v[142:145], v[22:25], v[18:21], v[142:145]
	v_mfma_f32_16x16x32_f16 v[146:149], v[6:9], v[18:21], v[146:149]
	s_waitcnt lgkmcnt(0)
	v_mfma_f32_16x16x32_f16 v[210:213], v[22:25], v[34:37], v[210:213]
	v_mfma_f32_16x16x32_f16 v[214:217], v[6:9], v[34:37], v[214:217]
	ds_read_b128 v[18:21], v151 offset:3648
	ds_read_b128 v[34:37], v151 offset:4256
	s_waitcnt lgkmcnt(1)
	v_mfma_f32_16x16x32_f16 v[166:169], v[22:25], v[18:21], v[166:169]
	v_mfma_f32_16x16x32_f16 v[158:161], v[6:9], v[18:21], v[158:161]
	s_waitcnt lgkmcnt(0)
	v_mfma_f32_16x16x32_f16 v[170:173], v[22:25], v[34:37], v[170:173]
	v_mfma_f32_16x16x32_f16 v[162:165], v[6:9], v[34:37], v[162:165]
	v_add_u32_e32 v18, 0x70740, v244
	v_min_u32_e32 v18, v18, v157
	global_load_dwordx4 v[122:125], v18, s[8:9] nt
	s_waitcnt vmcnt(21)
	v_cvt_pk_f16_f32 v19, v72, v73
	v_cvt_pk_f16_f32 v18, v70, v71
	ds_write_b16 v238, v18 offset:3040
	ds_write_b16_d16_hi v239, v18 offset:3040
	ds_write_b16 v240, v19 offset:3040
	ds_write_b16_d16_hi v241, v19 offset:3040
	ds_read_b128 v[18:21], v151 offset:4864
	ds_read_b128 v[34:37], v151 offset:5472
	s_waitcnt lgkmcnt(1)
	v_mfma_f32_16x16x32_f16 v[174:177], v[22:25], v[18:21], v[174:177]
	v_mfma_f32_16x16x32_f16 v[178:181], v[6:9], v[18:21], v[178:181]
	s_waitcnt lgkmcnt(0)
	v_mfma_f32_16x16x32_f16 v[186:189], v[22:25], v[34:37], v[186:189]
	v_mfma_f32_16x16x32_f16 v[190:193], v[6:9], v[34:37], v[190:193]
	ds_read_b128 v[18:21], v151 offset:6080
	ds_read_b128 v[34:37], v151 offset:6688
	s_waitcnt lgkmcnt(1)
	v_mfma_f32_16x16x32_f16 v[194:197], v[22:25], v[18:21], v[194:197]
	v_mfma_f32_16x16x32_f16 v[182:185], v[6:9], v[18:21], v[182:185]
	s_waitcnt lgkmcnt(0)
	v_mfma_f32_16x16x32_f16 v[202:205], v[22:25], v[34:37], v[202:205]
	v_mfma_f32_16x16x32_f16 v[206:209], v[6:9], v[34:37], v[206:209]
	v_add_u32_e32 v18, 0x86d80, v150
	v_min_u32_e32 v18, v18, v157
	global_load_dwordx4 v[70:73], v18, s[8:9] nt
	s_waitcnt vmcnt(21)
	v_cvt_pk_f16_f32 v19, v76, v77
	v_cvt_pk_f16_f32 v18, v74, v75
	ds_write_b16 v234, v18 offset:3648
	ds_write_b16_d16_hi v235, v18 offset:3648
	ds_write_b16 v236, v19 offset:3648
	ds_write_b16_d16_hi v237, v19 offset:3648
	s_mov_b32 s2, 0x38000
	v_add_co_u32_e32 v18, vcc, s2, v152
	s_mov_b32 s2, 0x3c000
	s_nop 0
	v_addc_co_u32_e32 v19, vcc, 0, v153, vcc
	ds_read_b128 v[74:77], v151 offset:7296
	global_load_dwordx4 v[54:57], v[18:19], off sc1
	global_load_dwordx4 v[66:69], v[18:19], off offset:256 sc1
	v_add_co_u32_e32 v18, vcc, s2, v152
	s_waitcnt lgkmcnt(0)
	v_mfma_f32_16x16x32_f16 v[22:25], v[22:25], v[74:77], v[26:29]
	v_addc_co_u32_e32 v19, vcc, 0, v153, vcc
	global_load_dwordx4 v[34:37], v[18:19], off sc1
	s_nop 0
	global_load_dwordx4 v[18:21], v[18:19], off offset:256 sc1
	v_mfma_f32_16x16x32_f16 v[6:9], v[6:9], v[74:77], v[42:45]
	ds_read_b128 v[26:29], v151 offset:64
	s_nop 1
	ds_read_b128 v[42:45], v151 offset:672
	s_waitcnt vmcnt(24) lgkmcnt(1)
	v_mfma_f32_16x16x32_f16 v[46:49], v[58:61], v[26:29], v[46:49]
	s_waitcnt vmcnt(23)
	v_mfma_f32_16x16x32_f16 v[26:29], v[62:65], v[26:29], v[198:201]
	s_nop 2
	ds_read_b128 v[198:201], v151 offset:1280
	s_waitcnt lgkmcnt(1)
	v_mfma_f32_16x16x32_f16 v[74:77], v[58:61], v[42:45], v[218:221]
	v_mfma_f32_16x16x32_f16 v[42:45], v[62:65], v[42:45], v[222:225]
	s_waitcnt lgkmcnt(0)
	v_mfma_f32_16x16x32_f16 v[218:221], v[58:61], v[198:201], v[126:129]
	v_mfma_f32_16x16x32_f16 v[130:133], v[62:65], v[198:201], v[130:133]
	s_nop 1
	v_add_u32_e32 v126, 0x9d3c0, v244
	v_min_u32_e32 v126, v126, v157
	global_load_dwordx4 v[126:129], v126, s[8:9] nt
	s_waitcnt vmcnt(21)
	v_cvt_pk_f16_f32 v81, v80, v81
	v_cvt_pk_f16_f32 v80, v78, v79
	ds_write_b16 v238, v80 offset:4256
	ds_write_b16_d16_hi v239, v80 offset:4256
	ds_write_b16 v240, v81 offset:4256
	ds_write_b16_d16_hi v241, v81 offset:4256
	ds_read_b128 v[78:81], v151 offset:1888
	ds_read_b128 v[198:201], v151 offset:2496
	s_waitcnt lgkmcnt(1)
	v_mfma_f32_16x16x32_f16 v[134:137], v[58:61], v[78:81], v[134:137]
	v_mfma_f32_16x16x32_f16 v[138:141], v[62:65], v[78:81], v[138:141]
	s_waitcnt lgkmcnt(0)
	v_mfma_f32_16x16x32_f16 v[142:145], v[58:61], v[198:201], v[142:145]
	v_mfma_f32_16x16x32_f16 v[146:149], v[62:65], v[198:201], v[146:149]
	ds_read_b128 v[78:81], v151 offset:3104
	ds_read_b128 v[198:201], v151 offset:3712
	s_waitcnt lgkmcnt(1)
	v_mfma_f32_16x16x32_f16 v[210:213], v[58:61], v[78:81], v[210:213]
	v_mfma_f32_16x16x32_f16 v[214:217], v[62:65], v[78:81], v[214:217]
	s_waitcnt lgkmcnt(0)
	v_mfma_f32_16x16x32_f16 v[166:169], v[58:61], v[198:201], v[166:169]
	v_mfma_f32_16x16x32_f16 v[158:161], v[62:65], v[198:201], v[158:161]
	v_add_u32_e32 v78, 0xb3a00, v150
	v_min_u32_e32 v78, v78, v157
	global_load_dwordx4 v[78:81], v78, s[8:9] nt
	s_waitcnt vmcnt(21)
	v_cvt_pk_f16_f32 v85, v84, v85
	v_cvt_pk_f16_f32 v84, v82, v83
	ds_write_b16 v234, v84 offset:4864
	ds_write_b16_d16_hi v235, v84 offset:4864
	ds_write_b16 v236, v85 offset:4864
	ds_write_b16_d16_hi v237, v85 offset:4864
	ds_read_b128 v[82:85], v151 offset:4320
	ds_read_b128 v[198:201], v151 offset:6144
	s_waitcnt lgkmcnt(1)
	v_mfma_f32_16x16x32_f16 v[170:173], v[58:61], v[82:85], v[170:173]
	v_mfma_f32_16x16x32_f16 v[162:165], v[62:65], v[82:85], v[162:165]
	ds_read_b128 v[82:85], v151 offset:4928
	ds_read_b128 v[222:225], v151 offset:5536
	s_waitcnt lgkmcnt(1)
	v_mfma_f32_16x16x32_f16 v[174:177], v[58:61], v[82:85], v[174:177]
	v_mfma_f32_16x16x32_f16 v[178:181], v[62:65], v[82:85], v[178:181]
	s_waitcnt lgkmcnt(0)
	v_mfma_f32_16x16x32_f16 v[186:189], v[58:61], v[222:225], v[186:189]
	v_mfma_f32_16x16x32_f16 v[190:193], v[62:65], v[222:225], v[190:193]
	v_mfma_f32_16x16x32_f16 v[194:197], v[58:61], v[198:201], v[194:197]
	v_mfma_f32_16x16x32_f16 v[182:185], v[62:65], v[198:201], v[182:185]
	v_add_u32_e32 v82, 0xca040, v244
	v_min_u32_e32 v82, v82, v157
	global_load_dwordx4 v[82:85], v82, s[8:9] nt
	s_waitcnt vmcnt(21)
	v_cvt_pk_f16_f32 v89, v88, v89
	v_cvt_pk_f16_f32 v88, v86, v87
	ds_write_b16 v238, v88 offset:5472
	ds_write_b16_d16_hi v239, v88 offset:5472
	ds_write_b16 v240, v89 offset:5472
	ds_write_b16_d16_hi v241, v89 offset:5472
	ds_read_b128 v[86:89], v151 offset:6752
	ds_read_b128 v[198:201], v151 offset:7360
	s_waitcnt lgkmcnt(1)
	v_mfma_f32_16x16x32_f16 v[202:205], v[58:61], v[86:89], v[202:205]
	s_waitcnt lgkmcnt(0)
	v_mfma_f32_16x16x32_f16 v[22:25], v[58:61], v[198:201], v[22:25]
	v_mfma_f32_16x16x32_f16 v[198:201], v[62:65], v[198:201], v[6:9]
	s_nop 2
	ds_read_b128 v[6:9], v151 offset:128
	ds_read_b128 v[58:61], v151 offset:736
	v_mfma_f32_16x16x32_f16 v[206:209], v[62:65], v[86:89], v[206:209]
	s_waitcnt lgkmcnt(1)
	v_mfma_f32_16x16x32_f16 v[222:225], v[30:33], v[6:9], v[46:49]
	v_mfma_f32_16x16x32_f16 v[226:229], v[14:17], v[6:9], v[26:29]
	s_waitcnt lgkmcnt(0)
	v_mfma_f32_16x16x32_f16 v[74:77], v[30:33], v[58:61], v[74:77]
	v_mfma_f32_16x16x32_f16 v[230:233], v[14:17], v[58:61], v[42:45]
	v_add_u32_e32 v6, 0xe0680, v150
	v_min_u32_e32 v6, v6, v157
	global_load_dwordx4 v[58:61], v6, s[8:9] nt
	s_waitcnt vmcnt(21)
	v_cvt_pk_f16_f32 v7, v92, v93
	v_cvt_pk_f16_f32 v6, v90, v91
	ds_write_b16 v234, v6 offset:6080
	ds_write_b16_d16_hi v235, v6 offset:6080
	ds_write_b16 v236, v7 offset:6080
	ds_write_b16_d16_hi v237, v7 offset:6080
	ds_read_b128 v[6:9], v151 offset:1344
	ds_read_b128 v[26:29], v151 offset:1952
	s_waitcnt lgkmcnt(1)
	v_mfma_f32_16x16x32_f16 v[90:93], v[30:33], v[6:9], v[218:221]
	v_mfma_f32_16x16x32_f16 v[130:133], v[14:17], v[6:9], v[130:133]
	s_waitcnt lgkmcnt(0)
	v_mfma_f32_16x16x32_f16 v[134:137], v[30:33], v[26:29], v[134:137]
	v_mfma_f32_16x16x32_f16 v[138:141], v[14:17], v[26:29], v[138:141]
	ds_read_b128 v[6:9], v151 offset:2560
	ds_read_b128 v[26:29], v151 offset:3168
	s_waitcnt lgkmcnt(1)
	v_mfma_f32_16x16x32_f16 v[142:145], v[30:33], v[6:9], v[142:145]
	v_mfma_f32_16x16x32_f16 v[146:149], v[14:17], v[6:9], v[146:149]
	s_waitcnt lgkmcnt(0)
	v_mfma_f32_16x16x32_f16 v[210:213], v[30:33], v[26:29], v[210:213]
	v_mfma_f32_16x16x32_f16 v[214:217], v[14:17], v[26:29], v[214:217]
	v_add_u32_e32 v6, 0xf6cc0, v244
	v_min_u32_e32 v6, v6, v157
	global_load_dwordx4 v[62:65], v6, s[8:9] nt
	s_waitcnt vmcnt(21)
	v_cvt_pk_f16_f32 v7, v96, v97
	v_cvt_pk_f16_f32 v6, v94, v95
	ds_write_b16 v238, v6 offset:6688
	ds_write_b16_d16_hi v239, v6 offset:6688
	ds_write_b16 v240, v7 offset:6688
	ds_write_b16_d16_hi v241, v7 offset:6688
	ds_read_b128 v[6:9], v151 offset:3776
	ds_read_b128 v[26:29], v151 offset:4384
	s_waitcnt lgkmcnt(1)
	v_mfma_f32_16x16x32_f16 v[94:97], v[30:33], v[6:9], v[166:169]
	v_mfma_f32_16x16x32_f16 v[158:161], v[14:17], v[6:9], v[158:161]
	s_waitcnt lgkmcnt(0)
	v_mfma_f32_16x16x32_f16 v[166:169], v[30:33], v[26:29], v[170:173]
	v_mfma_f32_16x16x32_f16 v[162:165], v[14:17], v[26:29], v[162:165]
	ds_read_b128 v[6:9], v151 offset:4992
	ds_read_b128 v[26:29], v151 offset:5600
	s_waitcnt lgkmcnt(1)
	v_mfma_f32_16x16x32_f16 v[170:173], v[30:33], v[6:9], v[174:177]
	v_mfma_f32_16x16x32_f16 v[174:177], v[14:17], v[6:9], v[178:181]
	s_waitcnt lgkmcnt(0)
	v_mfma_f32_16x16x32_f16 v[178:181], v[30:33], v[26:29], v[186:189]
	v_mfma_f32_16x16x32_f16 v[186:189], v[14:17], v[26:29], v[190:193]
	v_add_u32_e32 v6, 0x10d300, v150
	v_min_u32_e32 v6, v6, v157
	v_cndmask_b32_e64 v6, 0, v6, s[0:1]
	global_load_dwordx4 v[86:89], v6, s[8:9] nt
	s_waitcnt vmcnt(21)
	v_cvt_pk_f16_f32 v7, v100, v101
	v_cvt_pk_f16_f32 v6, v98, v99
	ds_write_b16 v234, v6 offset:7296
	ds_write_b16_d16_hi v235, v6 offset:7296
	ds_write_b16 v236, v7 offset:7296
	ds_write_b16_d16_hi v237, v7 offset:7296
	ds_read_b128 v[6:9], v151 offset:6208
	ds_read_b128 v[26:29], v151 offset:6816
	s_mov_b32 s2, 0x40000
	ds_read_b128 v[190:193], v151 offset:7424
	s_waitcnt lgkmcnt(0)
	v_mfma_f32_16x16x32_f16 v[98:101], v[30:33], v[6:9], v[194:197]
	s_barrier
	v_sub_u32_e32 v245, v234, v243
	v_add_u32_e32 v246, 0xfffffdc0, v245
	v_min_u32_e32 v245, v245, v246
	v_add_u32_e32 v234, v242, v245
	v_sub_u32_e32 v245, v235, v243
	v_add_u32_e32 v246, 0xfffffdc0, v245
	v_min_u32_e32 v245, v245, v246
	v_add_u32_e32 v235, v242, v245
	v_sub_u32_e32 v245, v236, v243
	v_add_u32_e32 v246, 0xfffffdc0, v245
	v_min_u32_e32 v245, v245, v246
	v_add_u32_e32 v236, v242, v245
	v_sub_u32_e32 v245, v237, v243
	v_add_u32_e32 v246, 0xfffffdc0, v245
	v_min_u32_e32 v245, v245, v246
	v_add_u32_e32 v237, v242, v245
	v_sub_u32_e32 v245, v238, v243
	v_add_u32_e32 v246, 0xfffffdc0, v245
	v_min_u32_e32 v245, v245, v246
	v_add_u32_e32 v238, v242, v245
	v_sub_u32_e32 v245, v239, v243
	v_add_u32_e32 v246, 0xfffffdc0, v245
	v_min_u32_e32 v245, v245, v246
	v_add_u32_e32 v239, v242, v245
	v_sub_u32_e32 v245, v240, v243
	v_add_u32_e32 v246, 0xfffffdc0, v245
	v_min_u32_e32 v245, v245, v246
	v_add_u32_e32 v240, v242, v245
	v_sub_u32_e32 v245, v241, v243
	v_add_u32_e32 v246, 0xfffffdc0, v245
	v_min_u32_e32 v245, v245, v246
	v_add_u32_e32 v241, v242, v245
	v_mfma_f32_16x16x32_f16 v[182:185], v[14:17], v[6:9], v[182:185]
	v_add_co_u32_e32 v6, vcc, s2, v152
	s_mov_b32 s2, 0x44000
	s_nop 0
	v_addc_co_u32_e32 v7, vcc, 0, v153, vcc
	global_load_dwordx4 v[42:45], v[6:7], off sc1
	global_load_dwordx4 v[46:49], v[6:7], off offset:256 sc1
	v_add_co_u32_e32 v6, vcc, s2, v152
	v_mfma_f32_16x16x32_f16 v[194:197], v[30:33], v[26:29], v[202:205]
	s_nop 0
	v_addc_co_u32_e32 v7, vcc, 0, v153, vcc
	v_mfma_f32_16x16x32_f16 v[202:205], v[14:17], v[26:29], v[206:209]
	global_load_dwordx4 v[26:29], v[6:7], off sc1
	s_nop 0
	global_load_dwordx4 v[6:9], v[6:7], off offset:256 sc1
	v_mfma_f32_16x16x32_f16 v[22:25], v[30:33], v[190:193], v[22:25]
	v_mfma_f32_16x16x32_f16 v[30:33], v[14:17], v[190:193], v[198:201]
	v_add_u32_e32 v157, 0x11151edc, v154
	ds_read_b128 v[14:17], v151 offset:192
	v_add_u32_e32 v206, 0xa00, v150
	s_waitcnt vmcnt(24) lgkmcnt(0)
	v_mfma_f32_16x16x32_f16 v[190:193], v[38:41], v[14:17], v[222:225]
	s_waitcnt vmcnt(23)
	v_mfma_f32_16x16x32_f16 v[198:201], v[50:53], v[14:17], v[226:229]
	v_min_u32_e32 v14, v206, v157
	global_load_dwordx4 v[14:17], v14, s[8:9] nt
	s_waitcnt vmcnt(21)
	v_cvt_pk_f16_f32 v105, v104, v105
	v_cvt_pk_f16_f32 v104, v102, v103
	ds_write_b16 v234, v104 offset:0
	ds_write_b16_d16_hi v235, v104 offset:0
	ds_write_b16 v236, v105 offset:0
	ds_write_b16_d16_hi v237, v105 offset:0
	ds_read_b128 v[102:105], v151 offset:800
	ds_read_b128 v[206:209], v151 offset:1408
	s_waitcnt lgkmcnt(1)
	v_mfma_f32_16x16x32_f16 v[74:77], v[38:41], v[102:105], v[74:77]
	s_waitcnt lgkmcnt(0)
	v_mfma_f32_16x16x32_f16 v[218:221], v[38:41], v[206:209], v[90:93]
	v_mfma_f32_16x16x32_f16 v[130:133], v[50:53], v[206:209], v[130:133]
	s_nop 1
	ds_read_b128 v[90:93], v151 offset:2016
	ds_read_b128 v[206:209], v151 offset:2624
	v_mfma_f32_16x16x32_f16 v[102:105], v[50:53], v[102:105], v[230:233]
	s_waitcnt lgkmcnt(1)
	v_mfma_f32_16x16x32_f16 v[134:137], v[38:41], v[90:93], v[134:137]
	v_mfma_f32_16x16x32_f16 v[138:141], v[50:53], v[90:93], v[138:141]
	s_waitcnt lgkmcnt(0)
	v_mfma_f32_16x16x32_f16 v[142:145], v[38:41], v[206:209], v[142:145]
	v_mfma_f32_16x16x32_f16 v[146:149], v[50:53], v[206:209], v[146:149]
	v_add_u32_e32 v90, 0x17040, v244
	v_min_u32_e32 v90, v90, v157
	global_load_dwordx4 v[90:93], v90, s[8:9] nt
	s_waitcnt vmcnt(21)
	v_cvt_pk_f16_f32 v109, v108, v109
	v_cvt_pk_f16_f32 v108, v106, v107
	ds_write_b16 v238, v108 offset:608
	ds_write_b16_d16_hi v239, v108 offset:608
	ds_write_b16 v240, v109 offset:608
	ds_write_b16_d16_hi v241, v109 offset:608
	ds_read_b128 v[106:109], v151 offset:3232
	ds_read_b128 v[206:209], v151 offset:5056
	s_waitcnt lgkmcnt(1)
	v_mfma_f32_16x16x32_f16 v[210:213], v[38:41], v[106:109], v[210:213]
	v_mfma_f32_16x16x32_f16 v[106:109], v[50:53], v[106:109], v[214:217]
	s_nop 2
	ds_read_b128 v[214:217], v151 offset:3840
	ds_read_b128 v[222:225], v151 offset:4448
	s_waitcnt lgkmcnt(1)
	v_mfma_f32_16x16x32_f16 v[226:229], v[38:41], v[214:217], v[94:97]
	v_mfma_f32_16x16x32_f16 v[158:161], v[50:53], v[214:217], v[158:161]
	s_waitcnt lgkmcnt(0)
	v_mfma_f32_16x16x32_f16 v[166:169], v[38:41], v[222:225], v[166:169]
	v_mfma_f32_16x16x32_f16 v[162:165], v[50:53], v[222:225], v[162:165]
	v_mfma_f32_16x16x32_f16 v[170:173], v[38:41], v[206:209], v[170:173]
	v_mfma_f32_16x16x32_f16 v[174:177], v[50:53], v[206:209], v[174:177]
	v_add_u32_e32 v94, 0x2d680, v150
	v_min_u32_e32 v94, v94, v157
	global_load_dwordx4 v[94:97], v94, s[8:9] nt
	s_waitcnt vmcnt(21)
	v_cvt_pk_f16_f32 v113, v112, v113
	v_cvt_pk_f16_f32 v112, v110, v111
	ds_write_b16 v234, v112 offset:1216
	ds_write_b16_d16_hi v235, v112 offset:1216
	ds_write_b16 v236, v113 offset:1216
	ds_write_b16_d16_hi v237, v113 offset:1216
	ds_read_b128 v[110:113], v151 offset:5664
	ds_read_b128 v[206:209], v151 offset:6272
	s_waitcnt lgkmcnt(1)
	v_mfma_f32_16x16x32_f16 v[178:181], v[38:41], v[110:113], v[178:181]
	v_mfma_f32_16x16x32_f16 v[110:113], v[50:53], v[110:113], v[186:189]
	s_waitcnt lgkmcnt(0)
	v_mfma_f32_16x16x32_f16 v[186:189], v[38:41], v[206:209], v[98:101]
	v_mfma_f32_16x16x32_f16 v[182:185], v[50:53], v[206:209], v[182:185]
	s_nop 1
	ds_read_b128 v[98:101], v151 offset:6880
	ds_read_b128 v[206:209], v151 offset:7488
	s_waitcnt lgkmcnt(1)
	v_mfma_f32_16x16x32_f16 v[194:197], v[38:41], v[98:101], v[194:197]
	v_mfma_f32_16x16x32_f16 v[202:205], v[50:53], v[98:101], v[202:205]
	s_waitcnt lgkmcnt(0)
	v_mfma_f32_16x16x32_f16 v[22:25], v[38:41], v[206:209], v[22:25]
	v_mfma_f32_16x16x32_f16 v[30:33], v[50:53], v[206:209], v[30:33]
	v_add_u32_e32 v38, 0x43cc0, v244
	v_min_u32_e32 v38, v38, v157
	global_load_dwordx4 v[98:101], v38, s[8:9] nt
	s_waitcnt vmcnt(21)
	v_cvt_pk_f16_f32 v39, v116, v117
	v_cvt_pk_f16_f32 v38, v114, v115
	ds_write_b16 v238, v38 offset:1824
	ds_write_b16_d16_hi v239, v38 offset:1824
	ds_write_b16 v240, v39 offset:1824
	ds_write_b16_d16_hi v241, v39 offset:1824
	ds_read_b128 v[38:41], v151 offset:256
	ds_read_b128 v[50:53], v151 offset:864
	s_waitcnt lgkmcnt(1)
	v_mfma_f32_16x16x32_f16 v[114:117], v[10:13], v[38:41], v[190:193]
	v_mfma_f32_16x16x32_f16 v[190:193], v[2:5], v[38:41], v[198:201]
	s_waitcnt lgkmcnt(0)
	v_mfma_f32_16x16x32_f16 v[198:201], v[10:13], v[50:53], v[74:77]
	ds_read_b128 v[38:41], v151 offset:1472
	s_nop 1
	ds_read_b128 v[74:77], v151 offset:2080
	v_mfma_f32_16x16x32_f16 v[50:53], v[2:5], v[50:53], v[102:105]
	s_waitcnt lgkmcnt(1)
	v_mfma_f32_16x16x32_f16 v[206:209], v[10:13], v[38:41], v[218:221]
	v_mfma_f32_16x16x32_f16 v[130:133], v[2:5], v[38:41], v[130:133]
	s_waitcnt lgkmcnt(0)
	v_mfma_f32_16x16x32_f16 v[134:137], v[10:13], v[74:77], v[134:137]
	v_mfma_f32_16x16x32_f16 v[138:141], v[2:5], v[74:77], v[138:141]
	v_add_u32_e32 v38, 0x5a300, v150
	v_min_u32_e32 v38, v38, v157
	global_load_dwordx4 v[102:105], v38, s[8:9] nt
	s_waitcnt vmcnt(21)
	v_cvt_pk_f16_f32 v39, v120, v121
	v_cvt_pk_f16_f32 v38, v118, v119
	ds_write_b16 v234, v38 offset:2432
	ds_write_b16_d16_hi v235, v38 offset:2432
	ds_write_b16 v236, v39 offset:2432
	ds_write_b16_d16_hi v237, v39 offset:2432
	ds_read_b128 v[38:41], v151 offset:2688
	ds_read_b128 v[74:77], v151 offset:3296
	s_waitcnt lgkmcnt(1)
	v_mfma_f32_16x16x32_f16 v[118:121], v[10:13], v[38:41], v[142:145]
	v_mfma_f32_16x16x32_f16 v[142:145], v[2:5], v[38:41], v[146:149]
	s_waitcnt lgkmcnt(0)
	v_mfma_f32_16x16x32_f16 v[146:149], v[10:13], v[74:77], v[210:213]
	v_mfma_f32_16x16x32_f16 v[210:213], v[2:5], v[74:77], v[106:109]
	ds_read_b128 v[38:41], v151 offset:3904
	ds_read_b128 v[74:77], v151 offset:4512
	s_waitcnt lgkmcnt(1)
	v_mfma_f32_16x16x32_f16 v[214:217], v[10:13], v[38:41], v[226:229]
	v_mfma_f32_16x16x32_f16 v[158:161], v[2:5], v[38:41], v[158:161]
	s_waitcnt lgkmcnt(0)
	v_mfma_f32_16x16x32_f16 v[166:169], v[10:13], v[74:77], v[166:169]
	v_mfma_f32_16x16x32_f16 v[162:165], v[2:5], v[74:77], v[162:165]
	v_add_u32_e32 v38, 0x70940, v244
	v_min_u32_e32 v38, v38, v157
	global_load_dwordx4 v[106:109], v38, s[8:9] nt
	s_waitcnt vmcnt(21)
	v_cvt_pk_f16_f32 v39, v124, v125
	v_cvt_pk_f16_f32 v38, v122, v123
	ds_write_b16 v238, v38 offset:3040
	ds_write_b16_d16_hi v239, v38 offset:3040
	ds_write_b16 v240, v39 offset:3040
	ds_write_b16_d16_hi v241, v39 offset:3040
	ds_read_b128 v[38:41], v151 offset:5120
	ds_read_b128 v[74:77], v151 offset:5728
	s_waitcnt lgkmcnt(1)
	v_mfma_f32_16x16x32_f16 v[122:125], v[10:13], v[38:41], v[170:173]
	v_mfma_f32_16x16x32_f16 v[170:173], v[2:5], v[38:41], v[174:177]
	s_waitcnt lgkmcnt(0)
	v_mfma_f32_16x16x32_f16 v[174:177], v[10:13], v[74:77], v[178:181]
	v_mfma_f32_16x16x32_f16 v[178:181], v[2:5], v[74:77], v[110:113]
	ds_read_b128 v[38:41], v151 offset:6336
	ds_read_b128 v[74:77], v151 offset:6944
	s_waitcnt lgkmcnt(1)
	v_mfma_f32_16x16x32_f16 v[186:189], v[10:13], v[38:41], v[186:189]
	v_mfma_f32_16x16x32_f16 v[182:185], v[2:5], v[38:41], v[182:185]
	s_waitcnt lgkmcnt(0)
	v_mfma_f32_16x16x32_f16 v[194:197], v[10:13], v[74:77], v[194:197]
	v_mfma_f32_16x16x32_f16 v[202:205], v[2:5], v[74:77], v[202:205]
	v_add_u32_e32 v38, 0x86f80, v150
	v_min_u32_e32 v38, v38, v157
	global_load_dwordx4 v[110:113], v38, s[8:9] nt
	s_waitcnt vmcnt(21)
	v_cvt_pk_f16_f32 v39, v72, v73
	v_cvt_pk_f16_f32 v38, v70, v71
	ds_write_b16 v234, v38 offset:3648
	ds_write_b16_d16_hi v235, v38 offset:3648
	ds_write_b16 v236, v39 offset:3648
	ds_write_b16_d16_hi v237, v39 offset:3648
	ds_read_b128 v[218:221], v151 offset:7552
	s_mov_b32 s2, 0x48000
	s_waitcnt lgkmcnt(0)
	v_mfma_f32_16x16x32_f16 v[10:13], v[10:13], v[218:221], v[22:25]
	s_nop 2
	v_add_co_u32_e32 v22, vcc, s2, v152
	s_mov_b32 s2, 0x4c000
	s_nop 0
	v_addc_co_u32_e32 v23, vcc, 0, v153, vcc
	global_load_dwordx4 v[70:73], v[22:23], off sc1
	global_load_dwordx4 v[74:77], v[22:23], off offset:256 sc1
	v_add_co_u32_e32 v22, vcc, s2, v152
	v_mfma_f32_16x16x32_f16 v[30:33], v[2:5], v[218:221], v[30:33]
	s_nop 0
	v_addc_co_u32_e32 v23, vcc, 0, v153, vcc
	global_load_dwordx4 v[38:41], v[22:23], off sc1
	s_nop 0
	global_load_dwordx4 v[22:25], v[22:23], off offset:256 sc1
	ds_read_b128 v[2:5], v151 offset:320
	ds_read_b128 v[218:221], v151 offset:928
	s_waitcnt vmcnt(24) lgkmcnt(1)
	v_mfma_f32_16x16x32_f16 v[222:225], v[54:57], v[2:5], v[114:117]
	s_waitcnt vmcnt(23)
	v_mfma_f32_16x16x32_f16 v[190:193], v[66:69], v[2:5], v[190:193]
	ds_read_b128 v[2:5], v151 offset:1536
	s_waitcnt lgkmcnt(1)
	v_mfma_f32_16x16x32_f16 v[198:201], v[54:57], v[218:221], v[198:201]
	v_mfma_f32_16x16x32_f16 v[50:53], v[66:69], v[218:221], v[50:53]
	s_waitcnt lgkmcnt(0)
	v_mfma_f32_16x16x32_f16 v[206:209], v[54:57], v[2:5], v[206:209]
	v_mfma_f32_16x16x32_f16 v[130:133], v[66:69], v[2:5], v[130:133]
	v_add_u32_e32 v2, 0x9d5c0, v244
	v_min_u32_e32 v2, v2, v157
	global_load_dwordx4 v[2:5], v2, s[8:9] nt
	s_waitcnt vmcnt(21)
	v_cvt_pk_f16_f32 v115, v128, v129
	v_cvt_pk_f16_f32 v114, v126, v127
	ds_write_b16 v238, v114 offset:4256
	ds_write_b16_d16_hi v239, v114 offset:4256
	ds_write_b16 v240, v115 offset:4256
	ds_write_b16_d16_hi v241, v115 offset:4256
	ds_read_b128 v[114:117], v151 offset:2144
	ds_read_b128 v[126:129], v151 offset:2752
	s_waitcnt lgkmcnt(1)
	v_mfma_f32_16x16x32_f16 v[134:137], v[54:57], v[114:117], v[134:137]
	v_mfma_f32_16x16x32_f16 v[138:141], v[66:69], v[114:117], v[138:141]
	s_waitcnt lgkmcnt(0)
	v_mfma_f32_16x16x32_f16 v[118:121], v[54:57], v[126:129], v[118:121]
	v_mfma_f32_16x16x32_f16 v[126:129], v[66:69], v[126:129], v[142:145]
	ds_read_b128 v[114:117], v151 offset:3360
	s_nop 1
	ds_read_b128 v[142:145], v151 offset:3968
	s_waitcnt lgkmcnt(1)
	v_mfma_f32_16x16x32_f16 v[146:149], v[54:57], v[114:117], v[146:149]
	v_mfma_f32_16x16x32_f16 v[210:213], v[66:69], v[114:117], v[210:213]
	s_waitcnt lgkmcnt(0)
	v_mfma_f32_16x16x32_f16 v[214:217], v[54:57], v[142:145], v[214:217]
	v_mfma_f32_16x16x32_f16 v[142:145], v[66:69], v[142:145], v[158:161]
	v_add_u32_e32 v114, 0xb3c00, v150
	v_min_u32_e32 v114, v114, v157
	global_load_dwordx4 v[114:117], v114, s[8:9] nt
	s_waitcnt vmcnt(21)
	v_cvt_pk_f16_f32 v81, v80, v81
	v_cvt_pk_f16_f32 v80, v78, v79
	ds_write_b16 v234, v80 offset:4864
	ds_write_b16_d16_hi v235, v80 offset:4864
	ds_write_b16 v236, v81 offset:4864
	ds_write_b16_d16_hi v237, v81 offset:4864
	ds_read_b128 v[78:81], v151 offset:4576
	ds_read_b128 v[158:161], v151 offset:6400
	s_waitcnt lgkmcnt(1)
	v_mfma_f32_16x16x32_f16 v[166:169], v[54:57], v[78:81], v[166:169]
	v_mfma_f32_16x16x32_f16 v[162:165], v[66:69], v[78:81], v[162:165]
	ds_read_b128 v[78:81], v151 offset:5184
	ds_read_b128 v[218:221], v151 offset:5792
	s_waitcnt lgkmcnt(1)
	v_mfma_f32_16x16x32_f16 v[122:125], v[54:57], v[78:81], v[122:125]
	v_mfma_f32_16x16x32_f16 v[170:173], v[66:69], v[78:81], v[170:173]
	s_waitcnt lgkmcnt(0)
	v_mfma_f32_16x16x32_f16 v[174:177], v[54:57], v[218:221], v[174:177]
	v_mfma_f32_16x16x32_f16 v[178:181], v[66:69], v[218:221], v[178:181]
	v_mfma_f32_16x16x32_f16 v[186:189], v[54:57], v[158:161], v[186:189]
	v_mfma_f32_16x16x32_f16 v[158:161], v[66:69], v[158:161], v[182:185]
	v_add_u32_e32 v78, 0xca240, v244
	v_min_u32_e32 v78, v78, v157
	global_load_dwordx4 v[78:81], v78, s[8:9] nt
	s_waitcnt vmcnt(21)
	v_cvt_pk_f16_f32 v85, v84, v85
	v_cvt_pk_f16_f32 v84, v82, v83
	ds_write_b16 v238, v84 offset:5472
	ds_write_b16_d16_hi v239, v84 offset:5472
	ds_write_b16 v240, v85 offset:5472
	ds_write_b16_d16_hi v241, v85 offset:5472
	ds_read_b128 v[82:85], v151 offset:7008
	ds_read_b128 v[182:185], v151 offset:7616
	s_waitcnt lgkmcnt(1)
	v_mfma_f32_16x16x32_f16 v[194:197], v[54:57], v[82:85], v[194:197]
	s_waitcnt lgkmcnt(0)
	v_mfma_f32_16x16x32_f16 v[10:13], v[54:57], v[182:185], v[10:13]
	v_mfma_f32_16x16x32_f16 v[182:185], v[66:69], v[182:185], v[30:33]
	s_nop 2
	ds_read_b128 v[30:33], v151 offset:384
	ds_read_b128 v[54:57], v151 offset:992
	v_mfma_f32_16x16x32_f16 v[202:205], v[66:69], v[82:85], v[202:205]
	s_waitcnt lgkmcnt(1)
	v_mfma_f32_16x16x32_f16 v[218:221], v[34:37], v[30:33], v[222:225]
	v_mfma_f32_16x16x32_f16 v[190:193], v[18:21], v[30:33], v[190:193]
	s_waitcnt lgkmcnt(0)
	v_mfma_f32_16x16x32_f16 v[198:201], v[34:37], v[54:57], v[198:201]
	v_mfma_f32_16x16x32_f16 v[222:225], v[18:21], v[54:57], v[50:53]
	v_add_u32_e32 v30, 0xe0880, v150
	v_min_u32_e32 v30, v30, v157
	global_load_dwordx4 v[66:69], v30, s[8:9] nt
	s_waitcnt vmcnt(21)
	v_cvt_pk_f16_f32 v31, v60, v61
	v_cvt_pk_f16_f32 v30, v58, v59
	ds_write_b16 v234, v30 offset:6080
	ds_write_b16_d16_hi v235, v30 offset:6080
	ds_write_b16 v236, v31 offset:6080
	ds_write_b16_d16_hi v237, v31 offset:6080
	ds_read_b128 v[30:33], v151 offset:1600
	ds_read_b128 v[50:53], v151 offset:2208
	s_waitcnt lgkmcnt(1)
	v_mfma_f32_16x16x32_f16 v[58:61], v[34:37], v[30:33], v[206:209]
	v_mfma_f32_16x16x32_f16 v[130:133], v[18:21], v[30:33], v[130:133]
	s_waitcnt lgkmcnt(0)
	v_mfma_f32_16x16x32_f16 v[134:137], v[34:37], v[50:53], v[134:137]
	v_mfma_f32_16x16x32_f16 v[138:141], v[18:21], v[50:53], v[138:141]
	ds_read_b128 v[30:33], v151 offset:2816
	ds_read_b128 v[50:53], v151 offset:3424
	s_waitcnt lgkmcnt(1)
	v_mfma_f32_16x16x32_f16 v[206:209], v[34:37], v[30:33], v[118:121]
	v_mfma_f32_16x16x32_f16 v[126:129], v[18:21], v[30:33], v[126:129]
	s_waitcnt lgkmcnt(0)
	v_mfma_f32_16x16x32_f16 v[146:149], v[34:37], v[50:53], v[146:149]
	v_mfma_f32_16x16x32_f16 v[210:213], v[18:21], v[50:53], v[210:213]
	v_add_u32_e32 v30, 0xf6ec0, v244
	v_min_u32_e32 v30, v30, v157
	global_load_dwordx4 v[82:85], v30, s[8:9] nt
	s_waitcnt vmcnt(21)
	v_cvt_pk_f16_f32 v31, v64, v65
	v_cvt_pk_f16_f32 v30, v62, v63
	ds_write_b16 v238, v30 offset:6688
	ds_write_b16_d16_hi v239, v30 offset:6688
	ds_write_b16 v240, v31 offset:6688
	ds_write_b16_d16_hi v241, v31 offset:6688
	ds_read_b128 v[30:33], v151 offset:4032
	ds_read_b128 v[50:53], v151 offset:4640
	s_waitcnt lgkmcnt(1)
	v_mfma_f32_16x16x32_f16 v[62:65], v[34:37], v[30:33], v[214:217]
	v_mfma_f32_16x16x32_f16 v[142:145], v[18:21], v[30:33], v[142:145]
	s_waitcnt lgkmcnt(0)
	v_mfma_f32_16x16x32_f16 v[166:169], v[34:37], v[50:53], v[166:169]
	v_mfma_f32_16x16x32_f16 v[162:165], v[18:21], v[50:53], v[162:165]
	ds_read_b128 v[30:33], v151 offset:5248
	ds_read_b128 v[50:53], v151 offset:5856
	s_waitcnt lgkmcnt(1)
	v_mfma_f32_16x16x32_f16 v[214:217], v[34:37], v[30:33], v[122:125]
	v_mfma_f32_16x16x32_f16 v[170:173], v[18:21], v[30:33], v[170:173]
	s_waitcnt lgkmcnt(0)
	v_mfma_f32_16x16x32_f16 v[174:177], v[34:37], v[50:53], v[174:177]
	v_mfma_f32_16x16x32_f16 v[178:181], v[18:21], v[50:53], v[178:181]
	v_add_u32_e32 v30, 0x10d500, v150
	v_min_u32_e32 v30, v30, v157
	v_cndmask_b32_e64 v30, 0, v30, s[0:1]
	global_load_dwordx4 v[118:121], v30, s[8:9] nt
	s_waitcnt vmcnt(21)
	v_cvt_pk_f16_f32 v31, v88, v89
	v_cvt_pk_f16_f32 v30, v86, v87
	ds_write_b16 v234, v30 offset:7296
	ds_write_b16_d16_hi v235, v30 offset:7296
	ds_write_b16 v236, v31 offset:7296
	ds_write_b16_d16_hi v237, v31 offset:7296
	ds_read_b128 v[30:33], v151 offset:6464
	ds_read_b128 v[50:53], v151 offset:7072
	ds_read_b128 v[122:125], v151 offset:7680
	s_mov_b32 s2, 0x50000
	s_waitcnt lgkmcnt(0)
	v_mfma_f32_16x16x32_f16 v[86:89], v[34:37], v[30:33], v[186:189]
	s_barrier
	v_sub_u32_e32 v245, v234, v243
	v_add_u32_e32 v246, 0xfffffdc0, v245
	v_min_u32_e32 v245, v245, v246
	v_add_u32_e32 v234, v242, v245
	v_sub_u32_e32 v245, v235, v243
	v_add_u32_e32 v246, 0xfffffdc0, v245
	v_min_u32_e32 v245, v245, v246
	v_add_u32_e32 v235, v242, v245
	v_sub_u32_e32 v245, v236, v243
	v_add_u32_e32 v246, 0xfffffdc0, v245
	v_min_u32_e32 v245, v245, v246
	v_add_u32_e32 v236, v242, v245
	v_sub_u32_e32 v245, v237, v243
	v_add_u32_e32 v246, 0xfffffdc0, v245
	v_min_u32_e32 v245, v245, v246
	v_add_u32_e32 v237, v242, v245
	v_sub_u32_e32 v245, v238, v243
	v_add_u32_e32 v246, 0xfffffdc0, v245
	v_min_u32_e32 v245, v245, v246
	v_add_u32_e32 v238, v242, v245
	v_sub_u32_e32 v245, v239, v243
	v_add_u32_e32 v246, 0xfffffdc0, v245
	v_min_u32_e32 v245, v245, v246
	v_add_u32_e32 v239, v242, v245
	v_sub_u32_e32 v245, v240, v243
	v_add_u32_e32 v246, 0xfffffdc0, v245
	v_min_u32_e32 v245, v245, v246
	v_add_u32_e32 v240, v242, v245
	v_sub_u32_e32 v245, v241, v243
	v_add_u32_e32 v246, 0xfffffdc0, v245
	v_min_u32_e32 v245, v245, v246
	v_add_u32_e32 v241, v242, v245
	v_mfma_f32_16x16x32_f16 v[158:161], v[18:21], v[30:33], v[158:161]
	v_add_co_u32_e32 v30, vcc, s2, v152
	s_mov_b32 s2, 0x54000
	s_nop 0
	v_addc_co_u32_e32 v31, vcc, 0, v153, vcc
	v_mfma_f32_16x16x32_f16 v[186:189], v[34:37], v[50:53], v[194:197]
	v_mfma_f32_16x16x32_f16 v[34:37], v[34:37], v[122:125], v[10:13]
	s_nop 2
	v_add_co_u32_e32 v10, vcc, s2, v152
	v_mfma_f32_16x16x32_f16 v[194:197], v[18:21], v[50:53], v[202:205]
	s_nop 0
	v_addc_co_u32_e32 v11, vcc, 0, v153, vcc
	global_load_dwordx4 v[50:53], v[30:31], off sc1
	global_load_dwordx4 v[54:57], v[30:31], off offset:256 sc1
	s_nop 0
	global_load_dwordx4 v[30:33], v[10:11], off sc1
	s_nop 0
	global_load_dwordx4 v[10:13], v[10:11], off offset:256 sc1
	v_mfma_f32_16x16x32_f16 v[182:185], v[18:21], v[122:125], v[182:185]
	v_add_u32_e32 v157, 0x111520dc, v154
	ds_read_b128 v[18:21], v151 offset:448
	v_add_u32_e32 v122, 0xc00, v150
	s_waitcnt vmcnt(24) lgkmcnt(0)
	v_mfma_f32_16x16x32_f16 v[202:205], v[42:45], v[18:21], v[218:221]
	s_waitcnt vmcnt(23)
	v_mfma_f32_16x16x32_f16 v[190:193], v[46:49], v[18:21], v[190:193]
	v_min_u32_e32 v18, v122, v157
	global_load_dwordx4 v[18:21], v18, s[8:9] nt
	s_waitcnt vmcnt(21)
	v_cvt_pk_f16_f32 v17, v16, v17
	v_cvt_pk_f16_f32 v16, v14, v15
	ds_write_b16 v234, v16 offset:0
	ds_write_b16_d16_hi v235, v16 offset:0
	ds_write_b16 v236, v17 offset:0
	ds_write_b16_d16_hi v237, v17 offset:0
	ds_read_b128 v[14:17], v151 offset:1056
	ds_read_b128 v[122:125], v151 offset:1664
	s_waitcnt lgkmcnt(1)
	v_mfma_f32_16x16x32_f16 v[198:201], v[42:45], v[14:17], v[198:201]
	s_waitcnt lgkmcnt(0)
	v_mfma_f32_16x16x32_f16 v[58:61], v[42:45], v[122:125], v[58:61]
	v_mfma_f32_16x16x32_f16 v[218:221], v[46:49], v[122:125], v[130:133]
	ds_read_b128 v[122:125], v151 offset:2272
	s_nop 1
	ds_read_b128 v[130:133], v151 offset:2880
	v_mfma_f32_16x16x32_f16 v[14:17], v[46:49], v[14:17], v[222:225]
	s_waitcnt lgkmcnt(1)
	v_mfma_f32_16x16x32_f16 v[134:137], v[42:45], v[122:125], v[134:137]
	v_mfma_f32_16x16x32_f16 v[138:141], v[46:49], v[122:125], v[138:141]
	s_waitcnt lgkmcnt(0)
	v_mfma_f32_16x16x32_f16 v[206:209], v[42:45], v[130:133], v[206:209]
	v_mfma_f32_16x16x32_f16 v[222:225], v[46:49], v[130:133], v[126:129]
	v_add_u32_e32 v122, 0x17240, v244
	v_min_u32_e32 v122, v122, v157
	global_load_dwordx4 v[122:125], v122, s[8:9] nt
	s_waitcnt vmcnt(21)
	v_cvt_pk_f16_f32 v93, v92, v93
	v_cvt_pk_f16_f32 v92, v90, v91
	ds_write_b16 v238, v92 offset:608
	ds_write_b16_d16_hi v239, v92 offset:608
	ds_write_b16 v240, v93 offset:608
	ds_write_b16_d16_hi v241, v93 offset:608
	ds_read_b128 v[90:93], v151 offset:3488
	ds_read_b128 v[126:129], v151 offset:5312
	s_waitcnt lgkmcnt(1)
	v_mfma_f32_16x16x32_f16 v[146:149], v[42:45], v[90:93], v[146:149]
	v_mfma_f32_16x16x32_f16 v[90:93], v[46:49], v[90:93], v[210:213]
	ds_read_b128 v[130:133], v151 offset:4096
	s_nop 1
	ds_read_b128 v[210:213], v151 offset:4704
	s_waitcnt lgkmcnt(1)
	v_mfma_f32_16x16x32_f16 v[62:65], v[42:45], v[130:133], v[62:65]
	v_mfma_f32_16x16x32_f16 v[142:145], v[46:49], v[130:133], v[142:145]
	s_waitcnt lgkmcnt(0)
	v_mfma_f32_16x16x32_f16 v[166:169], v[42:45], v[210:213], v[166:169]
	v_mfma_f32_16x16x32_f16 v[162:165], v[46:49], v[210:213], v[162:165]
	v_mfma_f32_16x16x32_f16 v[210:213], v[42:45], v[126:129], v[214:217]
	v_mfma_f32_16x16x32_f16 v[170:173], v[46:49], v[126:129], v[170:173]
	v_add_u32_e32 v126, 0x2d880, v150
	v_min_u32_e32 v126, v126, v157
	global_load_dwordx4 v[126:129], v126, s[8:9] nt
	s_waitcnt vmcnt(21)
	v_cvt_pk_f16_f32 v97, v96, v97
	v_cvt_pk_f16_f32 v96, v94, v95
	ds_write_b16 v234, v96 offset:1216
	ds_write_b16_d16_hi v235, v96 offset:1216
	ds_write_b16 v236, v97 offset:1216
	ds_write_b16_d16_hi v237, v97 offset:1216
	ds_read_b128 v[94:97], v151 offset:5920
	ds_read_b128 v[130:133], v151 offset:6528
	s_waitcnt lgkmcnt(1)
	v_mfma_f32_16x16x32_f16 v[174:177], v[42:45], v[94:97], v[174:177]
	v_mfma_f32_16x16x32_f16 v[94:97], v[46:49], v[94:97], v[178:181]
	s_waitcnt lgkmcnt(0)
	v_mfma_f32_16x16x32_f16 v[86:89], v[42:45], v[130:133], v[86:89]
	v_mfma_f32_16x16x32_f16 v[158:161], v[46:49], v[130:133], v[158:161]
	ds_read_b128 v[130:133], v151 offset:7136
	ds_read_b128 v[178:181], v151 offset:7744
	s_waitcnt lgkmcnt(1)
	v_mfma_f32_16x16x32_f16 v[186:189], v[42:45], v[130:133], v[186:189]
	v_mfma_f32_16x16x32_f16 v[194:197], v[46:49], v[130:133], v[194:197]
	s_waitcnt lgkmcnt(0)
	v_mfma_f32_16x16x32_f16 v[34:37], v[42:45], v[178:181], v[34:37]
	v_mfma_f32_16x16x32_f16 v[42:45], v[46:49], v[178:181], v[182:185]
	v_add_u32_e32 v46, 0x43ec0, v244
	v_min_u32_e32 v46, v46, v157
	global_load_dwordx4 v[130:133], v46, s[8:9] nt
	s_waitcnt vmcnt(21)
	v_cvt_pk_f16_f32 v47, v100, v101
	v_cvt_pk_f16_f32 v46, v98, v99
	ds_write_b16 v238, v46 offset:1824
	ds_write_b16_d16_hi v239, v46 offset:1824
	ds_write_b16 v240, v47 offset:1824
	ds_write_b16_d16_hi v241, v47 offset:1824
	ds_read_b128 v[46:49], v151 offset:512
	ds_read_b128 v[98:101], v151 offset:1120
	s_waitcnt lgkmcnt(1)
	v_mfma_f32_16x16x32_f16 v[178:181], v[26:29], v[46:49], v[202:205]
	v_mfma_f32_16x16x32_f16 v[46:49], v[6:9], v[46:49], v[190:193]
	s_waitcnt lgkmcnt(0)
	v_mfma_f32_16x16x32_f16 v[182:185], v[26:29], v[98:101], v[198:201]
	v_mfma_f32_16x16x32_f16 v[98:101], v[6:9], v[98:101], v[14:17]
	s_nop 2
	ds_read_b128 v[14:17], v151 offset:1728
	ds_read_b128 v[190:193], v151 offset:2336
	s_waitcnt lgkmcnt(1)
	v_mfma_f32_16x16x32_f16 v[198:201], v[26:29], v[14:17], v[58:61]
	v_mfma_f32_16x16x32_f16 v[202:205], v[6:9], v[14:17], v[218:221]
	s_waitcnt lgkmcnt(0)
	v_mfma_f32_16x16x32_f16 v[214:217], v[26:29], v[190:193], v[134:137]
	v_mfma_f32_16x16x32_f16 v[190:193], v[6:9], v[190:193], v[138:141]
	v_add_u32_e32 v14, 0x5a500, v150
	v_min_u32_e32 v14, v14, v157
	global_load_dwordx4 v[134:137], v14, s[8:9] nt
	s_waitcnt vmcnt(21)
	v_cvt_pk_f16_f32 v15, v104, v105
	v_cvt_pk_f16_f32 v14, v102, v103
	ds_write_b16 v234, v14 offset:2432
	ds_write_b16_d16_hi v235, v14 offset:2432
	ds_write_b16 v236, v15 offset:2432
	ds_write_b16_d16_hi v237, v15 offset:2432
	ds_read_b128 v[14:17], v151 offset:2944
	ds_read_b128 v[58:61], v151 offset:3552
	s_waitcnt lgkmcnt(1)
	v_mfma_f32_16x16x32_f16 v[102:105], v[26:29], v[14:17], v[206:209]
	v_mfma_f32_16x16x32_f16 v[206:209], v[6:9], v[14:17], v[222:225]
	s_waitcnt lgkmcnt(0)
	v_mfma_f32_16x16x32_f16 v[218:221], v[26:29], v[58:61], v[146:149]
	v_mfma_f32_16x16x32_f16 v[90:93], v[6:9], v[58:61], v[90:93]
	ds_read_b128 v[14:17], v151 offset:4160
	ds_read_b128 v[58:61], v151 offset:4768
	s_waitcnt lgkmcnt(1)
	v_mfma_f32_16x16x32_f16 v[222:225], v[26:29], v[14:17], v[62:65]
	v_mfma_f32_16x16x32_f16 v[226:229], v[6:9], v[14:17], v[142:145]
	s_waitcnt lgkmcnt(0)
	v_mfma_f32_16x16x32_f16 v[166:169], v[26:29], v[58:61], v[166:169]
	v_mfma_f32_16x16x32_f16 v[162:165], v[6:9], v[58:61], v[162:165]
	v_add_u32_e32 v14, 0x70b40, v244
	v_min_u32_e32 v14, v14, v157
	global_load_dwordx4 v[138:141], v14, s[8:9] nt
	s_waitcnt vmcnt(21)
	v_cvt_pk_f16_f32 v15, v108, v109
	v_cvt_pk_f16_f32 v14, v106, v107
	ds_write_b16 v238, v14 offset:3040
	ds_write_b16_d16_hi v239, v14 offset:3040
	ds_write_b16 v240, v15 offset:3040
	ds_write_b16_d16_hi v241, v15 offset:3040
	ds_read_b128 v[14:17], v151 offset:5376
	ds_read_b128 v[58:61], v151 offset:5984
	s_waitcnt lgkmcnt(1)
	v_mfma_f32_16x16x32_f16 v[106:109], v[26:29], v[14:17], v[210:213]
	v_mfma_f32_16x16x32_f16 v[170:173], v[6:9], v[14:17], v[170:173]
	s_waitcnt lgkmcnt(0)
	v_mfma_f32_16x16x32_f16 v[174:177], v[26:29], v[58:61], v[174:177]
	v_mfma_f32_16x16x32_f16 v[94:97], v[6:9], v[58:61], v[94:97]
	ds_read_b128 v[14:17], v151 offset:6592
	ds_read_b128 v[58:61], v151 offset:7200
	s_waitcnt lgkmcnt(1)
	v_mfma_f32_16x16x32_f16 v[86:89], v[26:29], v[14:17], v[86:89]
	v_mfma_f32_16x16x32_f16 v[158:161], v[6:9], v[14:17], v[158:161]
	s_waitcnt lgkmcnt(0)
	v_mfma_f32_16x16x32_f16 v[186:189], v[26:29], v[58:61], v[186:189]
	v_mfma_f32_16x16x32_f16 v[194:197], v[6:9], v[58:61], v[194:197]
	v_add_u32_e32 v14, 0x87180, v150
	v_min_u32_e32 v14, v14, v157
	global_load_dwordx4 v[142:145], v14, s[8:9] nt
	s_waitcnt vmcnt(21)
	v_cvt_pk_f16_f32 v15, v112, v113
	v_cvt_pk_f16_f32 v14, v110, v111
	ds_write_b16 v234, v14 offset:3648
	ds_write_b16_d16_hi v235, v14 offset:3648
	ds_write_b16 v236, v15 offset:3648
	ds_write_b16_d16_hi v237, v15 offset:3648
	ds_read_b128 v[110:113], v151 offset:7808
	s_mov_b32 s2, 0x58000
	v_add_co_u32_e32 v14, vcc, s2, v152
	s_mov_b32 s2, 0x5c000
	s_nop 0
	v_addc_co_u32_e32 v15, vcc, 0, v153, vcc
	global_load_dwordx4 v[58:61], v[14:15], off sc1
	global_load_dwordx4 v[62:65], v[14:15], off offset:256 sc1
	v_add_co_u32_e32 v14, vcc, s2, v152
	s_waitcnt lgkmcnt(0)
	v_mfma_f32_16x16x32_f16 v[26:29], v[26:29], v[110:113], v[34:37]
	v_addc_co_u32_e32 v15, vcc, 0, v153, vcc
	s_nop 1
	global_load_dwordx4 v[34:37], v[14:15], off sc1
	s_nop 0
	global_load_dwordx4 v[14:17], v[14:15], off offset:256 sc1
	v_mfma_f32_16x16x32_f16 v[42:45], v[6:9], v[110:113], v[42:45]
	ds_read_b128 v[6:9], v151 offset:0
	ds_read_b128 v[110:113], v151 offset:608
	s_waitcnt vmcnt(24) lgkmcnt(1)
	v_mfma_f32_16x16x32_f16 v[178:181], v[70:73], v[6:9], v[178:181]
	s_waitcnt vmcnt(23)
	v_mfma_f32_16x16x32_f16 v[46:49], v[74:77], v[6:9], v[46:49]
	ds_read_b128 v[6:9], v151 offset:1216
	s_waitcnt lgkmcnt(1)
	v_mfma_f32_16x16x32_f16 v[182:185], v[70:73], v[110:113], v[182:185]
	v_mfma_f32_16x16x32_f16 v[98:101], v[74:77], v[110:113], v[98:101]
	s_waitcnt lgkmcnt(0)
	v_mfma_f32_16x16x32_f16 v[198:201], v[70:73], v[6:9], v[198:201]
	v_mfma_f32_16x16x32_f16 v[202:205], v[74:77], v[6:9], v[202:205]
	v_add_u32_e32 v6, 0x9d7c0, v244
	v_min_u32_e32 v6, v6, v157
	global_load_dwordx4 v[146:149], v6, s[8:9] nt
	s_waitcnt vmcnt(21)
	v_cvt_pk_f16_f32 v5, v4, v5
	v_cvt_pk_f16_f32 v4, v2, v3
	ds_write_b16 v238, v4 offset:4256
	ds_write_b16_d16_hi v239, v4 offset:4256
	ds_write_b16 v240, v5 offset:4256
	ds_write_b16_d16_hi v241, v5 offset:4256
	ds_read_b128 v[2:5], v151 offset:1824
	ds_read_b128 v[6:9], v151 offset:2432
	s_waitcnt lgkmcnt(1)
	v_mfma_f32_16x16x32_f16 v[210:213], v[70:73], v[2:5], v[214:217]
	v_mfma_f32_16x16x32_f16 v[2:5], v[74:77], v[2:5], v[190:193]
	s_waitcnt lgkmcnt(0)
	v_mfma_f32_16x16x32_f16 v[102:105], v[70:73], v[6:9], v[102:105]
	v_mfma_f32_16x16x32_f16 v[190:193], v[74:77], v[6:9], v[206:209]
	ds_read_b128 v[6:9], v151 offset:3040
	ds_read_b128 v[110:113], v151 offset:3648
	s_waitcnt lgkmcnt(1)
	v_mfma_f32_16x16x32_f16 v[206:209], v[70:73], v[6:9], v[218:221]
	v_mfma_f32_16x16x32_f16 v[90:93], v[74:77], v[6:9], v[90:93]
	s_waitcnt lgkmcnt(0)
	v_mfma_f32_16x16x32_f16 v[214:217], v[70:73], v[110:113], v[222:225]
	v_mfma_f32_16x16x32_f16 v[218:221], v[74:77], v[110:113], v[226:229]
	v_add_u32_e32 v6, 0xb3e00, v150
	v_min_u32_e32 v6, v6, v157
	global_load_dwordx4 v[110:113], v6, s[8:9] nt
	s_waitcnt vmcnt(21)
	v_cvt_pk_f16_f32 v7, v116, v117
	v_cvt_pk_f16_f32 v6, v114, v115
	ds_write_b16 v234, v6 offset:4864
	ds_write_b16_d16_hi v235, v6 offset:4864
	ds_write_b16 v236, v7 offset:4864
	ds_write_b16_d16_hi v237, v7 offset:4864
	ds_read_b128 v[6:9], v151 offset:4256
	ds_read_b128 v[114:117], v151 offset:6080
	s_waitcnt lgkmcnt(1)
	v_mfma_f32_16x16x32_f16 v[166:169], v[70:73], v[6:9], v[166:169]
	v_mfma_f32_16x16x32_f16 v[162:165], v[74:77], v[6:9], v[162:165]
	ds_read_b128 v[6:9], v151 offset:4864
	ds_read_b128 v[222:225], v151 offset:5472
	s_waitcnt lgkmcnt(2)
	v_mfma_f32_16x16x32_f16 v[86:89], v[70:73], v[114:117], v[86:89]
	v_mfma_f32_16x16x32_f16 v[114:117], v[74:77], v[114:117], v[158:161]
	s_waitcnt lgkmcnt(1)
	v_mfma_f32_16x16x32_f16 v[106:109], v[70:73], v[6:9], v[106:109]
	v_mfma_f32_16x16x32_f16 v[170:173], v[74:77], v[6:9], v[170:173]
	s_waitcnt lgkmcnt(0)
	v_mfma_f32_16x16x32_f16 v[174:177], v[70:73], v[222:225], v[174:177]
	v_mfma_f32_16x16x32_f16 v[94:97], v[74:77], v[222:225], v[94:97]
	v_add_u32_e32 v6, 0xca440, v244
	v_min_u32_e32 v6, v6, v157
	global_load_dwordx4 v[6:9], v6, s[8:9] nt
	s_waitcnt vmcnt(21)
	v_cvt_pk_f16_f32 v81, v80, v81
	v_cvt_pk_f16_f32 v80, v78, v79
	ds_write_b16 v238, v80 offset:5472
	ds_write_b16_d16_hi v239, v80 offset:5472
	ds_write_b16 v240, v81 offset:5472
	ds_write_b16_d16_hi v241, v81 offset:5472
	ds_read_b128 v[78:81], v151 offset:6688
	ds_read_b128 v[158:161], v151 offset:7296
	s_waitcnt lgkmcnt(1)
	v_mfma_f32_16x16x32_f16 v[186:189], v[70:73], v[78:81], v[186:189]
	s_waitcnt lgkmcnt(0)
	v_mfma_f32_16x16x32_f16 v[26:29], v[70:73], v[158:161], v[26:29]
	v_mfma_f32_16x16x32_f16 v[158:161], v[74:77], v[158:161], v[42:45]
	s_nop 2
	ds_read_b128 v[42:45], v151 offset:64
	ds_read_b128 v[70:73], v151 offset:672
	v_mfma_f32_16x16x32_f16 v[194:197], v[74:77], v[78:81], v[194:197]
	s_waitcnt lgkmcnt(1)
	v_mfma_f32_16x16x32_f16 v[178:181], v[38:41], v[42:45], v[178:181]
	v_mfma_f32_16x16x32_f16 v[222:225], v[22:25], v[42:45], v[46:49]
	s_waitcnt lgkmcnt(0)
	v_mfma_f32_16x16x32_f16 v[182:185], v[38:41], v[70:73], v[182:185]
	v_mfma_f32_16x16x32_f16 v[98:101], v[22:25], v[70:73], v[98:101]
	v_add_u32_e32 v42, 0xe0a80, v150
	v_min_u32_e32 v42, v42, v157
	global_load_dwordx4 v[70:73], v42, s[8:9] nt
	s_waitcnt vmcnt(21)
	v_cvt_pk_f16_f32 v43, v68, v69
	v_cvt_pk_f16_f32 v42, v66, v67
	ds_write_b16 v234, v42 offset:6080
	ds_write_b16_d16_hi v235, v42 offset:6080
	ds_write_b16 v236, v43 offset:6080
	ds_write_b16_d16_hi v237, v43 offset:6080
	ds_read_b128 v[42:45], v151 offset:1280
	ds_read_b128 v[46:49], v151 offset:1888
	s_waitcnt lgkmcnt(1)
	v_mfma_f32_16x16x32_f16 v[66:69], v[38:41], v[42:45], v[198:201]
	v_mfma_f32_16x16x32_f16 v[198:201], v[22:25], v[42:45], v[202:205]
	s_waitcnt lgkmcnt(0)
	v_mfma_f32_16x16x32_f16 v[202:205], v[38:41], v[46:49], v[210:213]
	v_mfma_f32_16x16x32_f16 v[210:213], v[22:25], v[46:49], v[2:5]
	s_nop 2
	ds_read_b128 v[2:5], v151 offset:2496
	ds_read_b128 v[42:45], v151 offset:3104
	s_waitcnt lgkmcnt(1)
	v_mfma_f32_16x16x32_f16 v[102:105], v[38:41], v[2:5], v[102:105]
	v_mfma_f32_16x16x32_f16 v[190:193], v[22:25], v[2:5], v[190:193]
	s_waitcnt lgkmcnt(0)
	v_mfma_f32_16x16x32_f16 v[206:209], v[38:41], v[42:45], v[206:209]
	v_mfma_f32_16x16x32_f16 v[90:93], v[22:25], v[42:45], v[90:93]
	v_add_u32_e32 v2, 0xf70c0, v244
	v_min_u32_e32 v2, v2, v157
	global_load_dwordx4 v[74:77], v2, s[8:9] nt
	s_waitcnt vmcnt(21)
	v_cvt_pk_f16_f32 v3, v84, v85
	v_cvt_pk_f16_f32 v2, v82, v83
	ds_write_b16 v238, v2 offset:6688
	ds_write_b16_d16_hi v239, v2 offset:6688
	ds_write_b16 v240, v3 offset:6688
	ds_write_b16_d16_hi v241, v3 offset:6688
	ds_read_b128 v[2:5], v151 offset:3712
	ds_read_b128 v[42:45], v151 offset:4320
	s_waitcnt lgkmcnt(1)
	v_mfma_f32_16x16x32_f16 v[214:217], v[38:41], v[2:5], v[214:217]
	v_mfma_f32_16x16x32_f16 v[218:221], v[22:25], v[2:5], v[218:221]
	s_waitcnt lgkmcnt(0)
	v_mfma_f32_16x16x32_f16 v[166:169], v[38:41], v[42:45], v[166:169]
	v_mfma_f32_16x16x32_f16 v[162:165], v[22:25], v[42:45], v[162:165]
	ds_read_b128 v[2:5], v151 offset:4928
	ds_read_b128 v[42:45], v151 offset:5536
	s_waitcnt lgkmcnt(1)
	v_mfma_f32_16x16x32_f16 v[106:109], v[38:41], v[2:5], v[106:109]
	v_mfma_f32_16x16x32_f16 v[170:173], v[22:25], v[2:5], v[170:173]
	s_waitcnt lgkmcnt(0)
	v_mfma_f32_16x16x32_f16 v[174:177], v[38:41], v[42:45], v[174:177]
	v_mfma_f32_16x16x32_f16 v[94:97], v[22:25], v[42:45], v[94:97]
	v_add_u32_e32 v2, 0x10d700, v150
	v_min_u32_e32 v2, v2, v157
	v_cndmask_b32_e64 v2, 0, v2, s[0:1]
	global_load_dwordx4 v[78:81], v2, s[8:9] nt
	s_waitcnt vmcnt(21)
	v_cvt_pk_f16_f32 v3, v120, v121
	v_cvt_pk_f16_f32 v2, v118, v119
	ds_write_b16 v234, v2 offset:7296
	ds_write_b16_d16_hi v235, v2 offset:7296
	ds_write_b16 v236, v3 offset:7296
	ds_write_b16_d16_hi v237, v3 offset:7296
	ds_read_b128 v[2:5], v151 offset:6144
	ds_read_b128 v[42:45], v151 offset:6752
	ds_read_b128 v[82:85], v151 offset:7360
	s_mov_b32 s2, 0x60000
	s_waitcnt lgkmcnt(0)
	v_mfma_f32_16x16x32_f16 v[118:121], v[38:41], v[2:5], v[86:89]
	s_barrier
	v_sub_u32_e32 v245, v234, v243
	v_add_u32_e32 v246, 0xfffffdc0, v245
	v_min_u32_e32 v245, v245, v246
	v_add_u32_e32 v234, v242, v245
	v_sub_u32_e32 v245, v235, v243
	v_add_u32_e32 v246, 0xfffffdc0, v245
	v_min_u32_e32 v245, v245, v246
	v_add_u32_e32 v235, v242, v245
	v_sub_u32_e32 v245, v236, v243
	v_add_u32_e32 v246, 0xfffffdc0, v245
	v_min_u32_e32 v245, v245, v246
	v_add_u32_e32 v236, v242, v245
	v_sub_u32_e32 v245, v237, v243
	v_add_u32_e32 v246, 0xfffffdc0, v245
	v_min_u32_e32 v245, v245, v246
	v_add_u32_e32 v237, v242, v245
	v_sub_u32_e32 v245, v238, v243
	v_add_u32_e32 v246, 0xfffffdc0, v245
	v_min_u32_e32 v245, v245, v246
	v_add_u32_e32 v238, v242, v245
	v_sub_u32_e32 v245, v239, v243
	v_add_u32_e32 v246, 0xfffffdc0, v245
	v_min_u32_e32 v245, v245, v246
	v_add_u32_e32 v239, v242, v245
	v_sub_u32_e32 v245, v240, v243
	v_add_u32_e32 v246, 0xfffffdc0, v245
	v_min_u32_e32 v245, v245, v246
	v_add_u32_e32 v240, v242, v245
	v_sub_u32_e32 v245, v241, v243
	v_add_u32_e32 v246, 0xfffffdc0, v245
	v_min_u32_e32 v245, v245, v246
	v_add_u32_e32 v241, v242, v245
	v_mfma_f32_16x16x32_f16 v[114:117], v[22:25], v[2:5], v[114:117]
	v_add_co_u32_e32 v2, vcc, s2, v152
	s_mov_b32 s2, 0x64000
	s_nop 0
	v_addc_co_u32_e32 v3, vcc, 0, v153, vcc
	v_mfma_f32_16x16x32_f16 v[186:189], v[38:41], v[42:45], v[186:189]
	v_mfma_f32_16x16x32_f16 v[194:197], v[22:25], v[42:45], v[194:197]
	global_load_dwordx4 v[42:45], v[2:3], off sc1
	global_load_dwordx4 v[46:49], v[2:3], off offset:256 sc1
	v_add_co_u32_e32 v2, vcc, s2, v152
	v_mfma_f32_16x16x32_f16 v[38:41], v[38:41], v[82:85], v[26:29]
	s_nop 0
	v_addc_co_u32_e32 v3, vcc, 0, v153, vcc
	s_nop 0
	global_load_dwordx4 v[26:29], v[2:3], off sc1
	s_nop 0
	global_load_dwordx4 v[2:5], v[2:3], off offset:256 sc1
	v_mfma_f32_16x16x32_f16 v[22:25], v[22:25], v[82:85], v[158:161]
	v_add_u32_e32 v157, 0x111522dc, v154
	ds_read_b128 v[82:85], v151 offset:128
	v_add_u32_e32 v86, 0xe00, v150
	s_waitcnt vmcnt(24) lgkmcnt(0)
	v_mfma_f32_16x16x32_f16 v[158:161], v[50:53], v[82:85], v[178:181]
	s_waitcnt vmcnt(23)
	v_mfma_f32_16x16x32_f16 v[178:181], v[54:57], v[82:85], v[222:225]
	v_min_u32_e32 v82, v86, v157
	global_load_dwordx4 v[82:85], v82, s[8:9] nt
	s_waitcnt vmcnt(21)
	v_cvt_pk_f16_f32 v21, v20, v21
	v_cvt_pk_f16_f32 v20, v18, v19
	ds_write_b16 v234, v20 offset:0
	ds_write_b16_d16_hi v235, v20 offset:0
	ds_write_b16 v236, v21 offset:0
	ds_write_b16_d16_hi v237, v21 offset:0
	ds_read_b128 v[18:21], v151 offset:736
	ds_read_b128 v[86:89], v151 offset:1344
	s_waitcnt lgkmcnt(1)
	v_mfma_f32_16x16x32_f16 v[182:185], v[50:53], v[18:21], v[182:185]
	v_mfma_f32_16x16x32_f16 v[18:21], v[54:57], v[18:21], v[98:101]
	s_waitcnt lgkmcnt(0)
	v_mfma_f32_16x16x32_f16 v[66:69], v[50:53], v[86:89], v[66:69]
	v_mfma_f32_16x16x32_f16 v[98:101], v[54:57], v[86:89], v[198:201]
	ds_read_b128 v[86:89], v151 offset:1952
	s_nop 1
	ds_read_b128 v[198:201], v151 offset:2560
	s_waitcnt lgkmcnt(1)
	v_mfma_f32_16x16x32_f16 v[202:205], v[50:53], v[86:89], v[202:205]
	v_mfma_f32_16x16x32_f16 v[210:213], v[54:57], v[86:89], v[210:213]
	s_waitcnt lgkmcnt(0)
	v_mfma_f32_16x16x32_f16 v[102:105], v[50:53], v[198:201], v[102:105]
	v_mfma_f32_16x16x32_f16 v[190:193], v[54:57], v[198:201], v[190:193]
	v_add_u32_e32 v86, 0x17440, v244
	v_min_u32_e32 v86, v86, v157
	global_load_dwordx4 v[86:89], v86, s[8:9] nt
	s_waitcnt vmcnt(21)
	v_cvt_pk_f16_f32 v125, v124, v125
	v_cvt_pk_f16_f32 v124, v122, v123
	ds_write_b16 v238, v124 offset:608
	ds_write_b16_d16_hi v239, v124 offset:608
	ds_write_b16 v240, v125 offset:608
	ds_write_b16_d16_hi v241, v125 offset:608
	ds_read_b128 v[122:125], v151 offset:3168
	ds_read_b128 v[198:201], v151 offset:4992
	s_waitcnt lgkmcnt(1)
	v_mfma_f32_16x16x32_f16 v[206:209], v[50:53], v[122:125], v[206:209]
	v_mfma_f32_16x16x32_f16 v[122:125], v[54:57], v[122:125], v[90:93]
	s_nop 2
	ds_read_b128 v[90:93], v151 offset:3776
	ds_read_b128 v[222:225], v151 offset:4384
	s_waitcnt lgkmcnt(1)
	v_mfma_f32_16x16x32_f16 v[214:217], v[50:53], v[90:93], v[214:217]
	v_mfma_f32_16x16x32_f16 v[218:221], v[54:57], v[90:93], v[218:221]
	s_waitcnt lgkmcnt(0)
	v_mfma_f32_16x16x32_f16 v[166:169], v[50:53], v[222:225], v[166:169]
	v_mfma_f32_16x16x32_f16 v[162:165], v[54:57], v[222:225], v[162:165]
	v_mfma_f32_16x16x32_f16 v[106:109], v[50:53], v[198:201], v[106:109]
	v_mfma_f32_16x16x32_f16 v[170:173], v[54:57], v[198:201], v[170:173]
	v_add_u32_e32 v90, 0x2da80, v150
	v_min_u32_e32 v90, v90, v157
	global_load_dwordx4 v[90:93], v90, s[8:9] nt
	s_waitcnt vmcnt(21)
	v_cvt_pk_f16_f32 v129, v128, v129
	v_cvt_pk_f16_f32 v128, v126, v127
	ds_write_b16 v234, v128 offset:1216
	ds_write_b16_d16_hi v235, v128 offset:1216
	ds_write_b16 v236, v129 offset:1216
	ds_write_b16_d16_hi v237, v129 offset:1216
	ds_read_b128 v[126:129], v151 offset:5600
	ds_read_b128 v[198:201], v151 offset:6208
	s_waitcnt lgkmcnt(1)
	v_mfma_f32_16x16x32_f16 v[174:177], v[50:53], v[126:129], v[174:177]
	v_mfma_f32_16x16x32_f16 v[126:129], v[54:57], v[126:129], v[94:97]
	s_waitcnt lgkmcnt(0)
	v_mfma_f32_16x16x32_f16 v[118:121], v[50:53], v[198:201], v[118:121]
	v_mfma_f32_16x16x32_f16 v[114:117], v[54:57], v[198:201], v[114:117]
	ds_read_b128 v[94:97], v151 offset:6816
	ds_read_b128 v[198:201], v151 offset:7424
	s_waitcnt lgkmcnt(1)
	v_mfma_f32_16x16x32_f16 v[186:189], v[50:53], v[94:97], v[186:189]
	v_mfma_f32_16x16x32_f16 v[194:197], v[54:57], v[94:97], v[194:197]
	s_waitcnt lgkmcnt(0)
	v_mfma_f32_16x16x32_f16 v[38:41], v[50:53], v[198:201], v[38:41]
	v_mfma_f32_16x16x32_f16 v[22:25], v[54:57], v[198:201], v[22:25]
	v_add_u32_e32 v50, 0x440c0, v244
	v_min_u32_e32 v50, v50, v157
	global_load_dwordx4 v[94:97], v50, s[8:9] nt
	s_waitcnt vmcnt(21)
	v_cvt_pk_f16_f32 v51, v132, v133
	v_cvt_pk_f16_f32 v50, v130, v131
	ds_write_b16 v238, v50 offset:1824
	ds_write_b16_d16_hi v239, v50 offset:1824
	ds_write_b16 v240, v51 offset:1824
	ds_write_b16_d16_hi v241, v51 offset:1824
	ds_read_b128 v[50:53], v151 offset:192
	ds_read_b128 v[54:57], v151 offset:800
	s_waitcnt lgkmcnt(1)
	v_mfma_f32_16x16x32_f16 v[130:133], v[30:33], v[50:53], v[158:161]
	v_mfma_f32_16x16x32_f16 v[50:53], v[10:13], v[50:53], v[178:181]
	s_waitcnt lgkmcnt(0)
	v_mfma_f32_16x16x32_f16 v[158:161], v[30:33], v[54:57], v[182:185]
	v_mfma_f32_16x16x32_f16 v[178:181], v[10:13], v[54:57], v[18:21]
	s_nop 2
	ds_read_b128 v[18:21], v151 offset:1408
	ds_read_b128 v[54:57], v151 offset:2016
	s_waitcnt lgkmcnt(1)
	v_mfma_f32_16x16x32_f16 v[182:185], v[30:33], v[18:21], v[66:69]
	v_mfma_f32_16x16x32_f16 v[198:201], v[10:13], v[18:21], v[98:101]
	s_waitcnt lgkmcnt(0)
	v_mfma_f32_16x16x32_f16 v[202:205], v[30:33], v[54:57], v[202:205]
	v_mfma_f32_16x16x32_f16 v[210:213], v[10:13], v[54:57], v[210:213]
	v_add_u32_e32 v18, 0x5a700, v150
	v_min_u32_e32 v18, v18, v157
	global_load_dwordx4 v[98:101], v18, s[8:9] nt
	s_waitcnt vmcnt(21)
	v_cvt_pk_f16_f32 v19, v136, v137
	v_cvt_pk_f16_f32 v18, v134, v135
	ds_write_b16 v234, v18 offset:2432
	ds_write_b16_d16_hi v235, v18 offset:2432
	ds_write_b16 v236, v19 offset:2432
	ds_write_b16_d16_hi v237, v19 offset:2432
	ds_read_b128 v[18:21], v151 offset:2624
	ds_read_b128 v[54:57], v151 offset:3232
	s_waitcnt lgkmcnt(1)
	v_mfma_f32_16x16x32_f16 v[134:137], v[30:33], v[18:21], v[102:105]
	v_mfma_f32_16x16x32_f16 v[190:193], v[10:13], v[18:21], v[190:193]
	s_waitcnt lgkmcnt(0)
	v_mfma_f32_16x16x32_f16 v[206:209], v[30:33], v[54:57], v[206:209]
	v_mfma_f32_16x16x32_f16 v[122:125], v[10:13], v[54:57], v[122:125]
	ds_read_b128 v[18:21], v151 offset:3840
	ds_read_b128 v[54:57], v151 offset:4448
	s_waitcnt lgkmcnt(1)
	v_mfma_f32_16x16x32_f16 v[214:217], v[30:33], v[18:21], v[214:217]
	v_mfma_f32_16x16x32_f16 v[218:221], v[10:13], v[18:21], v[218:221]
	s_waitcnt lgkmcnt(0)
	v_mfma_f32_16x16x32_f16 v[166:169], v[30:33], v[54:57], v[166:169]
	v_mfma_f32_16x16x32_f16 v[162:165], v[10:13], v[54:57], v[162:165]
	v_add_u32_e32 v18, 0x70d40, v244
	v_min_u32_e32 v18, v18, v157
	global_load_dwordx4 v[102:105], v18, s[8:9] nt
	s_waitcnt vmcnt(21)
	v_cvt_pk_f16_f32 v19, v140, v141
	v_cvt_pk_f16_f32 v18, v138, v139
	ds_write_b16 v238, v18 offset:3040
	ds_write_b16_d16_hi v239, v18 offset:3040
	ds_write_b16 v240, v19 offset:3040
	ds_write_b16_d16_hi v241, v19 offset:3040
	ds_read_b128 v[18:21], v151 offset:5056
	ds_read_b128 v[54:57], v151 offset:5664
	s_waitcnt lgkmcnt(1)
	v_mfma_f32_16x16x32_f16 v[138:141], v[30:33], v[18:21], v[106:109]
	v_mfma_f32_16x16x32_f16 v[170:173], v[10:13], v[18:21], v[170:173]
	s_waitcnt lgkmcnt(0)
	v_mfma_f32_16x16x32_f16 v[174:177], v[30:33], v[54:57], v[174:177]
	v_mfma_f32_16x16x32_f16 v[126:129], v[10:13], v[54:57], v[126:129]
	ds_read_b128 v[18:21], v151 offset:6272
	ds_read_b128 v[54:57], v151 offset:6880
	s_waitcnt lgkmcnt(1)
	v_mfma_f32_16x16x32_f16 v[118:121], v[30:33], v[18:21], v[118:121]
	v_mfma_f32_16x16x32_f16 v[222:225], v[10:13], v[18:21], v[114:117]
	s_waitcnt lgkmcnt(0)
	v_mfma_f32_16x16x32_f16 v[186:189], v[30:33], v[54:57], v[186:189]
	v_mfma_f32_16x16x32_f16 v[194:197], v[10:13], v[54:57], v[194:197]
	v_add_u32_e32 v18, 0x87380, v150
	v_min_u32_e32 v18, v18, v157
	global_load_dwordx4 v[106:109], v18, s[8:9] nt
	s_waitcnt vmcnt(21)
	v_cvt_pk_f16_f32 v19, v144, v145
	v_cvt_pk_f16_f32 v18, v142, v143
	ds_write_b16 v234, v18 offset:3648
	ds_write_b16_d16_hi v235, v18 offset:3648
	ds_write_b16 v236, v19 offset:3648
	ds_write_b16_d16_hi v237, v19 offset:3648
	ds_read_b128 v[114:117], v151 offset:7488
	s_mov_b32 s2, 0x68000
	v_add_co_u32_e32 v18, vcc, s2, v152
	s_mov_b32 s2, 0x6c000
	s_nop 0
	v_addc_co_u32_e32 v19, vcc, 0, v153, vcc
	global_load_dwordx4 v[54:57], v[18:19], off sc1
	global_load_dwordx4 v[66:69], v[18:19], off offset:256 sc1
	v_add_co_u32_e32 v18, vcc, s2, v152
	s_waitcnt lgkmcnt(0)
	v_mfma_f32_16x16x32_f16 v[38:41], v[30:33], v[114:117], v[38:41]
	v_addc_co_u32_e32 v19, vcc, 0, v153, vcc
	global_load_dwordx4 v[30:33], v[18:19], off sc1
	s_nop 0
	global_load_dwordx4 v[18:21], v[18:19], off offset:256 sc1
	v_mfma_f32_16x16x32_f16 v[22:25], v[10:13], v[114:117], v[22:25]
	ds_read_b128 v[10:13], v151 offset:256
	ds_read_b128 v[114:117], v151 offset:864
	s_waitcnt vmcnt(24) lgkmcnt(1)
	v_mfma_f32_16x16x32_f16 v[130:133], v[58:61], v[10:13], v[130:133]
	s_waitcnt vmcnt(23)
	v_mfma_f32_16x16x32_f16 v[50:53], v[62:65], v[10:13], v[50:53]
	ds_read_b128 v[10:13], v151 offset:1472
	s_waitcnt lgkmcnt(1)
	v_mfma_f32_16x16x32_f16 v[142:145], v[58:61], v[114:117], v[158:161]
	v_mfma_f32_16x16x32_f16 v[158:161], v[62:65], v[114:117], v[178:181]
	s_waitcnt lgkmcnt(0)
	v_mfma_f32_16x16x32_f16 v[178:181], v[58:61], v[10:13], v[182:185]
	v_mfma_f32_16x16x32_f16 v[182:185], v[62:65], v[10:13], v[198:201]
	v_add_u32_e32 v10, 0x9d9c0, v244
	v_min_u32_e32 v10, v10, v157
	global_load_dwordx4 v[10:13], v10, s[8:9] nt
	s_waitcnt vmcnt(21)
	v_cvt_pk_f16_f32 v115, v148, v149
	v_cvt_pk_f16_f32 v114, v146, v147
	ds_write_b16 v238, v114 offset:4256
	ds_write_b16_d16_hi v239, v114 offset:4256
	ds_write_b16 v240, v115 offset:4256
	ds_write_b16_d16_hi v241, v115 offset:4256
	ds_read_b128 v[114:117], v151 offset:2080
	ds_read_b128 v[146:149], v151 offset:2688
	s_waitcnt lgkmcnt(1)
	v_mfma_f32_16x16x32_f16 v[198:201], v[58:61], v[114:117], v[202:205]
	v_mfma_f32_16x16x32_f16 v[202:205], v[62:65], v[114:117], v[210:213]
	s_waitcnt lgkmcnt(0)
	v_mfma_f32_16x16x32_f16 v[134:137], v[58:61], v[146:149], v[134:137]
	v_mfma_f32_16x16x32_f16 v[146:149], v[62:65], v[146:149], v[190:193]
	ds_read_b128 v[114:117], v151 offset:3296
	s_nop 1
	ds_read_b128 v[190:193], v151 offset:3904
	s_waitcnt lgkmcnt(1)
	v_mfma_f32_16x16x32_f16 v[206:209], v[58:61], v[114:117], v[206:209]
	v_mfma_f32_16x16x32_f16 v[122:125], v[62:65], v[114:117], v[122:125]
	s_waitcnt lgkmcnt(0)
	v_mfma_f32_16x16x32_f16 v[210:213], v[58:61], v[190:193], v[214:217]
	v_mfma_f32_16x16x32_f16 v[190:193], v[62:65], v[190:193], v[218:221]
	v_add_u32_e32 v114, 0xb4000, v150
	v_min_u32_e32 v114, v114, v157
	global_load_dwordx4 v[114:117], v114, s[8:9] nt
	s_waitcnt vmcnt(21)
	v_cvt_pk_f16_f32 v113, v112, v113
	v_cvt_pk_f16_f32 v112, v110, v111
	ds_write_b16 v234, v112 offset:4864
	ds_write_b16_d16_hi v235, v112 offset:4864
	ds_write_b16 v236, v113 offset:4864
	ds_write_b16_d16_hi v237, v113 offset:4864
	s_mov_b32 s2, 0xb4000
	ds_read_b128 v[110:113], v151 offset:4512
	ds_read_b128 v[214:217], v151 offset:6336
	s_waitcnt lgkmcnt(1)
	v_mfma_f32_16x16x32_f16 v[166:169], v[58:61], v[110:113], v[166:169]
	v_mfma_f32_16x16x32_f16 v[162:165], v[62:65], v[110:113], v[162:165]
	ds_read_b128 v[110:113], v151 offset:5120
	ds_read_b128 v[218:221], v151 offset:5728
	s_waitcnt lgkmcnt(1)
	v_mfma_f32_16x16x32_f16 v[138:141], v[58:61], v[110:113], v[138:141]
	v_mfma_f32_16x16x32_f16 v[170:173], v[62:65], v[110:113], v[170:173]
	s_waitcnt lgkmcnt(0)
	v_mfma_f32_16x16x32_f16 v[174:177], v[58:61], v[218:221], v[174:177]
	v_mfma_f32_16x16x32_f16 v[126:129], v[62:65], v[218:221], v[126:129]
	v_mfma_f32_16x16x32_f16 v[118:121], v[58:61], v[214:217], v[118:121]
	v_mfma_f32_16x16x32_f16 v[214:217], v[62:65], v[214:217], v[222:225]
	v_add_u32_e32 v110, 0xca640, v244
	v_min_u32_e32 v110, v110, v157
	global_load_dwordx4 v[110:113], v110, s[8:9] nt
	s_waitcnt vmcnt(21)
	v_cvt_pk_f16_f32 v9, v8, v9
	v_cvt_pk_f16_f32 v8, v6, v7
	ds_write_b16 v238, v8 offset:5472
	ds_write_b16_d16_hi v239, v8 offset:5472
	ds_write_b16 v240, v9 offset:5472
	ds_write_b16_d16_hi v241, v9 offset:5472
	ds_read_b128 v[6:9], v151 offset:6944
	ds_read_b128 v[218:221], v151 offset:7552
	s_waitcnt lgkmcnt(1)
	v_mfma_f32_16x16x32_f16 v[186:189], v[58:61], v[6:9], v[186:189]
	v_mfma_f32_16x16x32_f16 v[6:9], v[62:65], v[6:9], v[194:197]
	s_waitcnt lgkmcnt(0)
	v_mfma_f32_16x16x32_f16 v[58:61], v[58:61], v[218:221], v[38:41]
	v_mfma_f32_16x16x32_f16 v[194:197], v[62:65], v[218:221], v[22:25]
	s_nop 2
	ds_read_b128 v[22:25], v151 offset:320
	ds_read_b128 v[38:41], v151 offset:928
	s_waitcnt lgkmcnt(1)
	v_mfma_f32_16x16x32_f16 v[130:133], v[34:37], v[22:25], v[130:133]
	v_mfma_f32_16x16x32_f16 v[218:221], v[14:17], v[22:25], v[50:53]
	s_waitcnt lgkmcnt(0)
	v_mfma_f32_16x16x32_f16 v[142:145], v[34:37], v[38:41], v[142:145]
	v_mfma_f32_16x16x32_f16 v[158:161], v[14:17], v[38:41], v[158:161]
	v_add_u32_e32 v22, 0xe0c80, v150
	v_min_u32_e32 v22, v22, v157
	global_load_dwordx4 v[62:65], v22, s[8:9] nt
	s_waitcnt vmcnt(21)
	v_cvt_pk_f16_f32 v23, v72, v73
	v_cvt_pk_f16_f32 v22, v70, v71
	ds_write_b16 v234, v22 offset:6080
	ds_write_b16_d16_hi v235, v22 offset:6080
	ds_write_b16 v236, v23 offset:6080
	ds_write_b16_d16_hi v237, v23 offset:6080
	ds_read_b128 v[22:25], v151 offset:1536
	ds_read_b128 v[38:41], v151 offset:2144
	s_waitcnt lgkmcnt(1)
	v_mfma_f32_16x16x32_f16 v[178:181], v[34:37], v[22:25], v[178:181]
	v_mfma_f32_16x16x32_f16 v[182:185], v[14:17], v[22:25], v[182:185]
	s_waitcnt lgkmcnt(0)
	v_mfma_f32_16x16x32_f16 v[198:201], v[34:37], v[38:41], v[198:201]
	v_mfma_f32_16x16x32_f16 v[202:205], v[14:17], v[38:41], v[202:205]
	ds_read_b128 v[22:25], v151 offset:2752
	ds_read_b128 v[38:41], v151 offset:3360
	s_waitcnt lgkmcnt(1)
	v_mfma_f32_16x16x32_f16 v[134:137], v[34:37], v[22:25], v[134:137]
	v_mfma_f32_16x16x32_f16 v[146:149], v[14:17], v[22:25], v[146:149]
	s_waitcnt lgkmcnt(0)
	v_mfma_f32_16x16x32_f16 v[206:209], v[34:37], v[38:41], v[206:209]
	v_mfma_f32_16x16x32_f16 v[122:125], v[14:17], v[38:41], v[122:125]
	v_add_u32_e32 v22, 0xf72c0, v244
	v_min_u32_e32 v22, v22, v157
	global_load_dwordx4 v[70:73], v22, s[8:9] nt
	s_waitcnt vmcnt(21)
	v_cvt_pk_f16_f32 v23, v76, v77
	v_cvt_pk_f16_f32 v22, v74, v75
	ds_write_b16 v238, v22 offset:6688
	ds_write_b16_d16_hi v239, v22 offset:6688
	ds_write_b16 v240, v23 offset:6688
	ds_write_b16_d16_hi v241, v23 offset:6688
	ds_read_b128 v[22:25], v151 offset:3968
	ds_read_b128 v[38:41], v151 offset:4576
	s_waitcnt lgkmcnt(1)
	v_mfma_f32_16x16x32_f16 v[210:213], v[34:37], v[22:25], v[210:213]
	v_mfma_f32_16x16x32_f16 v[190:193], v[14:17], v[22:25], v[190:193]
	s_waitcnt lgkmcnt(0)
	v_mfma_f32_16x16x32_f16 v[166:169], v[34:37], v[38:41], v[166:169]
	v_mfma_f32_16x16x32_f16 v[162:165], v[14:17], v[38:41], v[162:165]
	ds_read_b128 v[22:25], v151 offset:5184
	ds_read_b128 v[38:41], v151 offset:5792
	s_waitcnt lgkmcnt(1)
	v_mfma_f32_16x16x32_f16 v[138:141], v[34:37], v[22:25], v[138:141]
	v_mfma_f32_16x16x32_f16 v[170:173], v[14:17], v[22:25], v[170:173]
	s_waitcnt lgkmcnt(0)
	v_mfma_f32_16x16x32_f16 v[174:177], v[34:37], v[38:41], v[174:177]
	v_mfma_f32_16x16x32_f16 v[126:129], v[14:17], v[38:41], v[126:129]
	v_add_u32_e32 v22, 0x10d900, v150
	v_min_u32_e32 v22, v22, v157
	v_cndmask_b32_e64 v22, 0, v22, s[0:1]
	global_load_dwordx4 v[74:77], v22, s[8:9] nt
	s_waitcnt vmcnt(21)
	v_cvt_pk_f16_f32 v23, v80, v81
	v_cvt_pk_f16_f32 v22, v78, v79
	ds_write_b16 v234, v22 offset:7296
	ds_write_b16_d16_hi v235, v22 offset:7296
	ds_write_b16 v236, v23 offset:7296
	ds_write_b16_d16_hi v237, v23 offset:7296
	ds_read_b128 v[22:25], v151 offset:6400
	ds_read_b128 v[38:41], v151 offset:7008
	s_mov_b32 s3, 0x70000
	ds_read_b128 v[78:81], v151 offset:7616
	s_waitcnt lgkmcnt(0)
	v_mfma_f32_16x16x32_f16 v[118:121], v[34:37], v[22:25], v[118:121]
	s_barrier
	v_sub_u32_e32 v245, v234, v243
	v_add_u32_e32 v246, 0xfffffdc0, v245
	v_min_u32_e32 v245, v245, v246
	v_add_u32_e32 v234, v242, v245
	v_sub_u32_e32 v245, v235, v243
	v_add_u32_e32 v246, 0xfffffdc0, v245
	v_min_u32_e32 v245, v245, v246
	v_add_u32_e32 v235, v242, v245
	v_sub_u32_e32 v245, v236, v243
	v_add_u32_e32 v246, 0xfffffdc0, v245
	v_min_u32_e32 v245, v245, v246
	v_add_u32_e32 v236, v242, v245
	v_sub_u32_e32 v245, v237, v243
	v_add_u32_e32 v246, 0xfffffdc0, v245
	v_min_u32_e32 v245, v245, v246
	v_add_u32_e32 v237, v242, v245
	v_sub_u32_e32 v245, v238, v243
	v_add_u32_e32 v246, 0xfffffdc0, v245
	v_min_u32_e32 v245, v245, v246
	v_add_u32_e32 v238, v242, v245
	v_sub_u32_e32 v245, v239, v243
	v_add_u32_e32 v246, 0xfffffdc0, v245
	v_min_u32_e32 v245, v245, v246
	v_add_u32_e32 v239, v242, v245
	v_sub_u32_e32 v245, v240, v243
	v_add_u32_e32 v246, 0xfffffdc0, v245
	v_min_u32_e32 v245, v245, v246
	v_add_u32_e32 v240, v242, v245
	v_sub_u32_e32 v245, v241, v243
	v_add_u32_e32 v246, 0xfffffdc0, v245
	v_min_u32_e32 v245, v245, v246
	v_add_u32_e32 v241, v242, v245
	v_mfma_f32_16x16x32_f16 v[214:217], v[14:17], v[22:25], v[214:217]
	v_add_co_u32_e32 v22, vcc, s3, v152
	s_mov_b32 s3, 0x74000
	s_nop 0
	v_addc_co_u32_e32 v23, vcc, 0, v153, vcc
	v_mfma_f32_16x16x32_f16 v[222:225], v[14:17], v[38:41], v[6:9]
	s_nop 2
	v_add_co_u32_e32 v6, vcc, s3, v152
	v_mfma_f32_16x16x32_f16 v[186:189], v[34:37], v[38:41], v[186:189]
	s_nop 0
	v_addc_co_u32_e32 v7, vcc, 0, v153, vcc
	global_load_dwordx4 v[38:41], v[22:23], off sc1
	global_load_dwordx4 v[50:53], v[22:23], off offset:256 sc1
	s_nop 0
	global_load_dwordx4 v[22:25], v[6:7], off sc1
	s_nop 0
	global_load_dwordx4 v[6:9], v[6:7], off offset:256 sc1
	v_mfma_f32_16x16x32_f16 v[34:37], v[34:37], v[78:81], v[58:61]
	v_mfma_f32_16x16x32_f16 v[14:17], v[14:17], v[78:81], v[194:197]
	v_add_u32_e32 v157, 0x111524dc, v154
	s_nop 0
	ds_read_b128 v[58:61], v151 offset:384
	v_add_u32_e32 v78, 0x1000, v150
	s_waitcnt vmcnt(24) lgkmcnt(0)
	v_mfma_f32_16x16x32_f16 v[130:133], v[42:45], v[58:61], v[130:133]
	s_waitcnt vmcnt(23)
	v_mfma_f32_16x16x32_f16 v[58:61], v[46:49], v[58:61], v[218:221]
	v_min_u32_e32 v78, v78, v157
	global_load_dwordx4 v[78:81], v78, s[8:9] nt
	s_waitcnt vmcnt(21)
	v_cvt_pk_f16_f32 v85, v84, v85
	v_cvt_pk_f16_f32 v84, v82, v83
	ds_write_b16 v234, v84 offset:0
	ds_write_b16_d16_hi v235, v84 offset:0
	ds_write_b16 v236, v85 offset:0
	ds_write_b16_d16_hi v237, v85 offset:0
	ds_read_b128 v[82:85], v151 offset:992
	ds_read_b128 v[194:197], v151 offset:1600
	s_waitcnt lgkmcnt(1)
	v_mfma_f32_16x16x32_f16 v[142:145], v[42:45], v[82:85], v[142:145]
	v_mfma_f32_16x16x32_f16 v[158:161], v[46:49], v[82:85], v[158:161]
	s_waitcnt lgkmcnt(0)
	v_mfma_f32_16x16x32_f16 v[178:181], v[42:45], v[194:197], v[178:181]
	v_mfma_f32_16x16x32_f16 v[182:185], v[46:49], v[194:197], v[182:185]
	ds_read_b128 v[82:85], v151 offset:2208
	ds_read_b128 v[194:197], v151 offset:2816
	s_waitcnt lgkmcnt(1)
	v_mfma_f32_16x16x32_f16 v[198:201], v[42:45], v[82:85], v[198:201]
	v_mfma_f32_16x16x32_f16 v[202:205], v[46:49], v[82:85], v[202:205]
	s_waitcnt lgkmcnt(0)
	v_mfma_f32_16x16x32_f16 v[134:137], v[42:45], v[194:197], v[134:137]
	v_mfma_f32_16x16x32_f16 v[146:149], v[46:49], v[194:197], v[146:149]
	v_add_u32_e32 v82, 0x17640, v244
	v_min_u32_e32 v82, v82, v157
	global_load_dwordx4 v[82:85], v82, s[8:9] nt
	s_waitcnt vmcnt(21)
	v_cvt_pk_f16_f32 v89, v88, v89
	v_cvt_pk_f16_f32 v88, v86, v87
	ds_write_b16 v238, v88 offset:608
	ds_write_b16_d16_hi v239, v88 offset:608
	ds_write_b16 v240, v89 offset:608
	ds_write_b16_d16_hi v241, v89 offset:608
	ds_read_b128 v[86:89], v151 offset:3424
	ds_read_b128 v[194:197], v151 offset:5248
	s_waitcnt lgkmcnt(1)
	v_mfma_f32_16x16x32_f16 v[206:209], v[42:45], v[86:89], v[206:209]
	v_mfma_f32_16x16x32_f16 v[122:125], v[46:49], v[86:89], v[122:125]
	ds_read_b128 v[86:89], v151 offset:4032
	ds_read_b128 v[218:221], v151 offset:4640
	s_waitcnt lgkmcnt(1)
	v_mfma_f32_16x16x32_f16 v[210:213], v[42:45], v[86:89], v[210:213]
	v_mfma_f32_16x16x32_f16 v[190:193], v[46:49], v[86:89], v[190:193]
	s_waitcnt lgkmcnt(0)
	v_mfma_f32_16x16x32_f16 v[166:169], v[42:45], v[218:221], v[166:169]
	v_mfma_f32_16x16x32_f16 v[162:165], v[46:49], v[218:221], v[162:165]
	v_mfma_f32_16x16x32_f16 v[138:141], v[42:45], v[194:197], v[138:141]
	v_mfma_f32_16x16x32_f16 v[170:173], v[46:49], v[194:197], v[170:173]
	v_add_u32_e32 v86, 0x2dc80, v150
	v_min_u32_e32 v86, v86, v157
	global_load_dwordx4 v[86:89], v86, s[8:9] nt
	s_waitcnt vmcnt(21)
	v_cvt_pk_f16_f32 v93, v92, v93
	v_cvt_pk_f16_f32 v92, v90, v91
	ds_write_b16 v234, v92 offset:1216
	ds_write_b16_d16_hi v235, v92 offset:1216
	ds_write_b16 v236, v93 offset:1216
	ds_write_b16_d16_hi v237, v93 offset:1216
	ds_read_b128 v[90:93], v151 offset:5856
	ds_read_b128 v[194:197], v151 offset:6464
	s_waitcnt lgkmcnt(1)
	v_mfma_f32_16x16x32_f16 v[174:177], v[42:45], v[90:93], v[174:177]
	v_mfma_f32_16x16x32_f16 v[126:129], v[46:49], v[90:93], v[126:129]
	s_waitcnt lgkmcnt(0)
	v_mfma_f32_16x16x32_f16 v[118:121], v[42:45], v[194:197], v[118:121]
	v_mfma_f32_16x16x32_f16 v[194:197], v[46:49], v[194:197], v[214:217]
	ds_read_b128 v[90:93], v151 offset:7072
	s_nop 1
	ds_read_b128 v[214:217], v151 offset:7680
	s_waitcnt lgkmcnt(1)
	v_mfma_f32_16x16x32_f16 v[186:189], v[42:45], v[90:93], v[186:189]
	v_mfma_f32_16x16x32_f16 v[218:221], v[46:49], v[90:93], v[222:225]
	s_waitcnt lgkmcnt(0)
	v_mfma_f32_16x16x32_f16 v[34:37], v[42:45], v[214:217], v[34:37]
	v_mfma_f32_16x16x32_f16 v[46:49], v[46:49], v[214:217], v[14:17]
	s_nop 2
	v_add_u32_e32 v14, 0x442c0, v244
	v_min_u32_e32 v14, v14, v157
	global_load_dwordx4 v[90:93], v14, s[8:9] nt
	s_waitcnt vmcnt(21)
	v_cvt_pk_f16_f32 v15, v96, v97
	v_cvt_pk_f16_f32 v14, v94, v95
	ds_write_b16 v238, v14 offset:1824
	ds_write_b16_d16_hi v239, v14 offset:1824
	ds_write_b16 v240, v15 offset:1824
	ds_write_b16_d16_hi v241, v15 offset:1824
	ds_read_b128 v[14:17], v151 offset:448
	ds_read_b128 v[42:45], v151 offset:1056
	s_waitcnt lgkmcnt(1)
	v_mfma_f32_16x16x32_f16 v[130:133], v[26:29], v[14:17], v[130:133]
	v_mfma_f32_16x16x32_f16 v[214:217], v[2:5], v[14:17], v[58:61]
	s_waitcnt lgkmcnt(0)
	v_mfma_f32_16x16x32_f16 v[142:145], v[26:29], v[42:45], v[142:145]
	v_mfma_f32_16x16x32_f16 v[158:161], v[2:5], v[42:45], v[158:161]
	ds_read_b128 v[14:17], v151 offset:1664
	ds_read_b128 v[42:45], v151 offset:2272
	s_waitcnt lgkmcnt(1)
	v_mfma_f32_16x16x32_f16 v[178:181], v[26:29], v[14:17], v[178:181]
	v_mfma_f32_16x16x32_f16 v[182:185], v[2:5], v[14:17], v[182:185]
	s_waitcnt lgkmcnt(0)
	v_mfma_f32_16x16x32_f16 v[198:201], v[26:29], v[42:45], v[198:201]
	v_mfma_f32_16x16x32_f16 v[202:205], v[2:5], v[42:45], v[202:205]
	v_add_u32_e32 v14, 0x5a900, v150
	v_min_u32_e32 v14, v14, v157
	global_load_dwordx4 v[94:97], v14, s[8:9] nt
	s_waitcnt vmcnt(21)
	v_cvt_pk_f16_f32 v15, v100, v101
	v_cvt_pk_f16_f32 v14, v98, v99
	ds_write_b16 v234, v14 offset:2432
	ds_write_b16_d16_hi v235, v14 offset:2432
	ds_write_b16 v236, v15 offset:2432
	ds_write_b16_d16_hi v237, v15 offset:2432
	ds_read_b128 v[14:17], v151 offset:2880
	ds_read_b128 v[42:45], v151 offset:3488
	s_waitcnt lgkmcnt(1)
	v_mfma_f32_16x16x32_f16 v[134:137], v[26:29], v[14:17], v[134:137]
	v_mfma_f32_16x16x32_f16 v[146:149], v[2:5], v[14:17], v[146:149]
	s_waitcnt lgkmcnt(0)
	v_mfma_f32_16x16x32_f16 v[206:209], v[26:29], v[42:45], v[206:209]
	v_mfma_f32_16x16x32_f16 v[122:125], v[2:5], v[42:45], v[122:125]
	ds_read_b128 v[14:17], v151 offset:4096
	ds_read_b128 v[42:45], v151 offset:4704
	s_waitcnt lgkmcnt(1)
	v_mfma_f32_16x16x32_f16 v[210:213], v[26:29], v[14:17], v[210:213]
	v_mfma_f32_16x16x32_f16 v[190:193], v[2:5], v[14:17], v[190:193]
	s_waitcnt lgkmcnt(0)
	v_mfma_f32_16x16x32_f16 v[166:169], v[26:29], v[42:45], v[166:169]
	v_mfma_f32_16x16x32_f16 v[162:165], v[2:5], v[42:45], v[162:165]
	v_add_u32_e32 v14, 0x70f40, v244
	v_min_u32_e32 v14, v14, v157
	global_load_dwordx4 v[98:101], v14, s[8:9] nt
	s_waitcnt vmcnt(21)
	v_cvt_pk_f16_f32 v15, v104, v105
	v_cvt_pk_f16_f32 v14, v102, v103
	ds_write_b16 v238, v14 offset:3040
	ds_write_b16_d16_hi v239, v14 offset:3040
	ds_write_b16 v240, v15 offset:3040
	ds_write_b16_d16_hi v241, v15 offset:3040
	ds_read_b128 v[14:17], v151 offset:5312
	ds_read_b128 v[42:45], v151 offset:5920
	s_waitcnt lgkmcnt(1)
	v_mfma_f32_16x16x32_f16 v[138:141], v[26:29], v[14:17], v[138:141]
	v_mfma_f32_16x16x32_f16 v[170:173], v[2:5], v[14:17], v[170:173]
	s_waitcnt lgkmcnt(0)
	v_mfma_f32_16x16x32_f16 v[174:177], v[26:29], v[42:45], v[174:177]
	v_mfma_f32_16x16x32_f16 v[126:129], v[2:5], v[42:45], v[126:129]
	ds_read_b128 v[14:17], v151 offset:6528
	ds_read_b128 v[42:45], v151 offset:7136
	s_waitcnt lgkmcnt(1)
	v_mfma_f32_16x16x32_f16 v[118:121], v[26:29], v[14:17], v[118:121]
	v_mfma_f32_16x16x32_f16 v[194:197], v[2:5], v[14:17], v[194:197]
	s_waitcnt lgkmcnt(0)
	v_mfma_f32_16x16x32_f16 v[186:189], v[26:29], v[42:45], v[186:189]
	v_mfma_f32_16x16x32_f16 v[218:221], v[2:5], v[42:45], v[218:221]
	v_add_u32_e32 v14, 0x87580, v150
	v_min_u32_e32 v14, v14, v157
	global_load_dwordx4 v[102:105], v14, s[8:9] nt
	s_waitcnt vmcnt(21)
	v_cvt_pk_f16_f32 v15, v108, v109
	v_cvt_pk_f16_f32 v14, v106, v107
	ds_write_b16 v234, v14 offset:3648
	ds_write_b16_d16_hi v235, v14 offset:3648
	ds_write_b16 v236, v15 offset:3648
	ds_write_b16_d16_hi v237, v15 offset:3648
	ds_read_b128 v[106:109], v151 offset:7744
	s_mov_b32 s3, 0x78000
	v_add_co_u32_e32 v14, vcc, s3, v152
	s_mov_b32 s3, 0x7c000
	s_nop 0
	v_addc_co_u32_e32 v15, vcc, 0, v153, vcc
	global_load_dwordx4 v[42:45], v[14:15], off sc1
	global_load_dwordx4 v[58:61], v[14:15], off offset:256 sc1
	v_add_co_u32_e32 v14, vcc, s3, v152
	s_waitcnt lgkmcnt(0)
	v_mfma_f32_16x16x32_f16 v[26:29], v[26:29], v[106:109], v[34:37]
	v_addc_co_u32_e32 v15, vcc, 0, v153, vcc
	s_nop 1
	global_load_dwordx4 v[34:37], v[14:15], off sc1
	s_nop 0
	global_load_dwordx4 v[14:17], v[14:15], off offset:256 sc1
	v_mfma_f32_16x16x32_f16 v[46:49], v[2:5], v[106:109], v[46:49]
	ds_read_b128 v[2:5], v151 offset:512
	ds_read_b128 v[106:109], v151 offset:1120
	s_waitcnt vmcnt(24) lgkmcnt(1)
	v_mfma_f32_16x16x32_f16 v[130:133], v[54:57], v[2:5], v[130:133]
	s_waitcnt vmcnt(23)
	v_mfma_f32_16x16x32_f16 v[214:217], v[66:69], v[2:5], v[214:217]
	ds_read_b128 v[2:5], v151 offset:1728
	s_waitcnt lgkmcnt(1)
	v_mfma_f32_16x16x32_f16 v[142:145], v[54:57], v[106:109], v[142:145]
	v_mfma_f32_16x16x32_f16 v[158:161], v[66:69], v[106:109], v[158:161]
	s_waitcnt lgkmcnt(0)
	v_mfma_f32_16x16x32_f16 v[178:181], v[54:57], v[2:5], v[178:181]
	v_mfma_f32_16x16x32_f16 v[182:185], v[66:69], v[2:5], v[182:185]
	v_add_u32_e32 v2, 0x9dbc0, v244
	v_min_u32_e32 v2, v2, v157
	global_load_dwordx4 v[2:5], v2, s[8:9] nt
	s_waitcnt vmcnt(21)
	v_cvt_pk_f16_f32 v13, v12, v13
	v_cvt_pk_f16_f32 v12, v10, v11
	ds_write_b16 v238, v12 offset:4256
	ds_write_b16_d16_hi v239, v12 offset:4256
	ds_write_b16 v240, v13 offset:4256
	ds_write_b16_d16_hi v241, v13 offset:4256
	ds_read_b128 v[10:13], v151 offset:2336
	ds_read_b128 v[106:109], v151 offset:2944
	s_waitcnt lgkmcnt(1)
	v_mfma_f32_16x16x32_f16 v[198:201], v[54:57], v[10:13], v[198:201]
	v_mfma_f32_16x16x32_f16 v[10:13], v[66:69], v[10:13], v[202:205]
	s_waitcnt lgkmcnt(0)
	v_mfma_f32_16x16x32_f16 v[134:137], v[54:57], v[106:109], v[134:137]
	v_mfma_f32_16x16x32_f16 v[146:149], v[66:69], v[106:109], v[146:149]
	ds_read_b128 v[106:109], v151 offset:3552
	ds_read_b128 v[202:205], v151 offset:4160
	s_waitcnt lgkmcnt(1)
	v_mfma_f32_16x16x32_f16 v[206:209], v[54:57], v[106:109], v[206:209]
	v_mfma_f32_16x16x32_f16 v[122:125], v[66:69], v[106:109], v[122:125]
	s_waitcnt lgkmcnt(0)
	v_mfma_f32_16x16x32_f16 v[210:213], v[54:57], v[202:205], v[210:213]
	v_mfma_f32_16x16x32_f16 v[190:193], v[66:69], v[202:205], v[190:193]
	v_add_u32_e32 v106, 0xb4200, v150
	v_min_u32_e32 v106, v106, v157
	global_load_dwordx4 v[106:109], v106, s[8:9] nt
	s_waitcnt vmcnt(21)
	v_cvt_pk_f16_f32 v117, v116, v117
	v_cvt_pk_f16_f32 v116, v114, v115
	ds_write_b16 v234, v116 offset:4864
	ds_write_b16_d16_hi v235, v116 offset:4864
	ds_write_b16 v236, v117 offset:4864
	ds_write_b16_d16_hi v237, v117 offset:4864
	ds_read_b128 v[114:117], v151 offset:4768
	ds_read_b128 v[202:205], v151 offset:6592
	s_waitcnt lgkmcnt(1)
	v_mfma_f32_16x16x32_f16 v[166:169], v[54:57], v[114:117], v[166:169]
	v_mfma_f32_16x16x32_f16 v[162:165], v[66:69], v[114:117], v[162:165]
	ds_read_b128 v[114:117], v151 offset:5376
	ds_read_b128 v[222:225], v151 offset:5984
	s_waitcnt lgkmcnt(1)
	v_mfma_f32_16x16x32_f16 v[138:141], v[54:57], v[114:117], v[138:141]
	v_mfma_f32_16x16x32_f16 v[170:173], v[66:69], v[114:117], v[170:173]
	s_waitcnt lgkmcnt(0)
	v_mfma_f32_16x16x32_f16 v[174:177], v[54:57], v[222:225], v[174:177]
	v_mfma_f32_16x16x32_f16 v[126:129], v[66:69], v[222:225], v[126:129]
	v_mfma_f32_16x16x32_f16 v[222:225], v[54:57], v[202:205], v[118:121]
	v_mfma_f32_16x16x32_f16 v[194:197], v[66:69], v[202:205], v[194:197]
	v_add_u32_e32 v114, 0xca840, v244
	v_min_u32_e32 v114, v114, v157
	global_load_dwordx4 v[114:117], v114, s[8:9] nt
	s_waitcnt vmcnt(21)
	v_cvt_pk_f16_f32 v113, v112, v113
	v_cvt_pk_f16_f32 v112, v110, v111
	ds_write_b16 v238, v112 offset:5472
	ds_write_b16_d16_hi v239, v112 offset:5472
	ds_write_b16 v240, v113 offset:5472
	ds_write_b16_d16_hi v241, v113 offset:5472
	ds_read_b128 v[110:113], v151 offset:7200
	ds_read_b128 v[118:121], v151 offset:7808
	s_waitcnt lgkmcnt(1)
	v_mfma_f32_16x16x32_f16 v[186:189], v[54:57], v[110:113], v[186:189]
	v_mfma_f32_16x16x32_f16 v[202:205], v[66:69], v[110:113], v[218:221]
	s_waitcnt lgkmcnt(0)
	v_mfma_f32_16x16x32_f16 v[26:29], v[54:57], v[118:121], v[26:29]
	v_mfma_f32_16x16x32_f16 v[66:69], v[66:69], v[118:121], v[46:49]
	s_nop 2
	ds_read_b128 v[46:49], v151 offset:0
	ds_read_b128 v[54:57], v151 offset:608
	s_waitcnt lgkmcnt(1)
	v_mfma_f32_16x16x32_f16 v[130:133], v[30:33], v[46:49], v[130:133]
	v_mfma_f32_16x16x32_f16 v[214:217], v[18:21], v[46:49], v[214:217]
	s_waitcnt lgkmcnt(0)
	v_mfma_f32_16x16x32_f16 v[142:145], v[30:33], v[54:57], v[142:145]
	v_mfma_f32_16x16x32_f16 v[158:161], v[18:21], v[54:57], v[158:161]
	v_add_u32_e32 v46, 0xe0e80, v150
	v_min_u32_e32 v46, v46, v157
	global_load_dwordx4 v[110:113], v46, s[8:9] nt
	s_waitcnt vmcnt(21)
	v_cvt_pk_f16_f32 v47, v64, v65
	v_cvt_pk_f16_f32 v46, v62, v63
	ds_write_b16 v234, v46 offset:6080
	ds_write_b16_d16_hi v235, v46 offset:6080
	ds_write_b16 v236, v47 offset:6080
	ds_write_b16_d16_hi v237, v47 offset:6080
	ds_read_b128 v[46:49], v151 offset:1216
	ds_read_b128 v[54:57], v151 offset:1824
	s_waitcnt lgkmcnt(1)
	v_mfma_f32_16x16x32_f16 v[62:65], v[30:33], v[46:49], v[178:181]
	v_mfma_f32_16x16x32_f16 v[178:181], v[18:21], v[46:49], v[182:185]
	s_waitcnt lgkmcnt(0)
	v_mfma_f32_16x16x32_f16 v[182:185], v[30:33], v[54:57], v[198:201]
	v_mfma_f32_16x16x32_f16 v[198:201], v[18:21], v[54:57], v[10:13]
	s_nop 2
	ds_read_b128 v[10:13], v151 offset:2432
	ds_read_b128 v[46:49], v151 offset:3040
	s_waitcnt lgkmcnt(1)
	v_mfma_f32_16x16x32_f16 v[134:137], v[30:33], v[10:13], v[134:137]
	v_mfma_f32_16x16x32_f16 v[146:149], v[18:21], v[10:13], v[146:149]
	s_waitcnt lgkmcnt(0)
	v_mfma_f32_16x16x32_f16 v[206:209], v[30:33], v[46:49], v[206:209]
	v_mfma_f32_16x16x32_f16 v[122:125], v[18:21], v[46:49], v[122:125]
	v_add_u32_e32 v10, 0xf74c0, v244
	v_min_u32_e32 v10, v10, v157
	global_load_dwordx4 v[118:121], v10, s[8:9] nt
	s_waitcnt vmcnt(21)
	v_cvt_pk_f16_f32 v11, v72, v73
	v_cvt_pk_f16_f32 v10, v70, v71
	ds_write_b16 v238, v10 offset:6688
	ds_write_b16_d16_hi v239, v10 offset:6688
	ds_write_b16 v240, v11 offset:6688
	ds_write_b16_d16_hi v241, v11 offset:6688
	ds_read_b128 v[10:13], v151 offset:3648
	ds_read_b128 v[46:49], v151 offset:4256
	s_waitcnt lgkmcnt(1)
	v_mfma_f32_16x16x32_f16 v[210:213], v[30:33], v[10:13], v[210:213]
	v_mfma_f32_16x16x32_f16 v[190:193], v[18:21], v[10:13], v[190:193]
	s_waitcnt lgkmcnt(0)
	v_mfma_f32_16x16x32_f16 v[166:169], v[30:33], v[46:49], v[166:169]
	v_mfma_f32_16x16x32_f16 v[162:165], v[18:21], v[46:49], v[162:165]
	ds_read_b128 v[10:13], v151 offset:4864
	ds_read_b128 v[46:49], v151 offset:5472
	s_waitcnt lgkmcnt(1)
	v_mfma_f32_16x16x32_f16 v[138:141], v[30:33], v[10:13], v[138:141]
	v_mfma_f32_16x16x32_f16 v[170:173], v[18:21], v[10:13], v[170:173]
	s_waitcnt lgkmcnt(0)
	v_mfma_f32_16x16x32_f16 v[174:177], v[30:33], v[46:49], v[174:177]
	v_mfma_f32_16x16x32_f16 v[126:129], v[18:21], v[46:49], v[126:129]
	v_add_u32_e32 v10, 0x10db00, v150
	v_min_u32_e32 v10, v10, v157
	v_cndmask_b32_e64 v10, 0, v10, s[0:1]
	global_load_dwordx4 v[70:73], v10, s[8:9] nt
	s_waitcnt vmcnt(21)
	v_cvt_pk_f16_f32 v11, v76, v77
	v_cvt_pk_f16_f32 v10, v74, v75
	ds_write_b16 v234, v10 offset:7296
	ds_write_b16_d16_hi v235, v10 offset:7296
	ds_write_b16 v236, v11 offset:7296
	ds_write_b16_d16_hi v237, v11 offset:7296
	ds_read_b128 v[10:13], v151 offset:6080
	ds_read_b128 v[46:49], v151 offset:6688
	ds_read_b128 v[74:77], v151 offset:7296
	s_mov_b32 s3, 0x80000
	s_waitcnt lgkmcnt(0)
	v_mfma_f32_16x16x32_f16 v[218:221], v[30:33], v[10:13], v[222:225]
	s_barrier
	v_sub_u32_e32 v245, v234, v243
	v_add_u32_e32 v246, 0xfffffdc0, v245
	v_min_u32_e32 v245, v245, v246
	v_add_u32_e32 v234, v242, v245
	v_sub_u32_e32 v245, v235, v243
	v_add_u32_e32 v246, 0xfffffdc0, v245
	v_min_u32_e32 v245, v245, v246
	v_add_u32_e32 v235, v242, v245
	v_sub_u32_e32 v245, v236, v243
	v_add_u32_e32 v246, 0xfffffdc0, v245
	v_min_u32_e32 v245, v245, v246
	v_add_u32_e32 v236, v242, v245
	v_sub_u32_e32 v245, v237, v243
	v_add_u32_e32 v246, 0xfffffdc0, v245
	v_min_u32_e32 v245, v245, v246
	v_add_u32_e32 v237, v242, v245
	v_sub_u32_e32 v245, v238, v243
	v_add_u32_e32 v246, 0xfffffdc0, v245
	v_min_u32_e32 v245, v245, v246
	v_add_u32_e32 v238, v242, v245
	v_sub_u32_e32 v245, v239, v243
	v_add_u32_e32 v246, 0xfffffdc0, v245
	v_min_u32_e32 v245, v245, v246
	v_add_u32_e32 v239, v242, v245
	v_sub_u32_e32 v245, v240, v243
	v_add_u32_e32 v246, 0xfffffdc0, v245
	v_min_u32_e32 v245, v245, v246
	v_add_u32_e32 v240, v242, v245
	v_sub_u32_e32 v245, v241, v243
	v_add_u32_e32 v246, 0xfffffdc0, v245
	v_min_u32_e32 v245, v245, v246
	v_add_u32_e32 v241, v242, v245
	v_mfma_f32_16x16x32_f16 v[194:197], v[18:21], v[10:13], v[194:197]
	v_add_co_u32_e32 v10, vcc, s3, v152
	s_mov_b32 s3, 0x84000
	s_nop 0
	v_addc_co_u32_e32 v11, vcc, 0, v153, vcc
	v_mfma_f32_16x16x32_f16 v[186:189], v[30:33], v[46:49], v[186:189]
	v_mfma_f32_16x16x32_f16 v[202:205], v[18:21], v[46:49], v[202:205]
	global_load_dwordx4 v[46:49], v[10:11], off sc1
	global_load_dwordx4 v[54:57], v[10:11], off offset:256 sc1
	v_add_co_u32_e32 v10, vcc, s3, v152
	v_mfma_f32_16x16x32_f16 v[30:33], v[30:33], v[74:77], v[26:29]
	s_nop 0
	v_addc_co_u32_e32 v11, vcc, 0, v153, vcc
	s_nop 0
	global_load_dwordx4 v[26:29], v[10:11], off sc1
	s_nop 0
	global_load_dwordx4 v[10:13], v[10:11], off offset:256 sc1
	v_mfma_f32_16x16x32_f16 v[18:21], v[18:21], v[74:77], v[66:69]
	v_add_u32_e32 v157, 0x111526dc, v154
	s_nop 1
	ds_read_b128 v[66:69], v151 offset:64
	v_add_u32_e32 v74, 0x1200, v150
	s_waitcnt vmcnt(24) lgkmcnt(0)
	v_mfma_f32_16x16x32_f16 v[130:133], v[38:41], v[66:69], v[130:133]
	s_waitcnt vmcnt(23)
	v_mfma_f32_16x16x32_f16 v[66:69], v[50:53], v[66:69], v[214:217]
	v_min_u32_e32 v74, v74, v157
	global_load_dwordx4 v[74:77], v74, s[8:9] nt
	s_waitcnt vmcnt(21)
	v_cvt_pk_f16_f32 v81, v80, v81
	v_cvt_pk_f16_f32 v80, v78, v79
	ds_write_b16 v234, v80 offset:0
	ds_write_b16_d16_hi v235, v80 offset:0
	ds_write_b16 v236, v81 offset:0
	ds_write_b16_d16_hi v237, v81 offset:0
	ds_read_b128 v[78:81], v151 offset:672
	ds_read_b128 v[214:217], v151 offset:1280
	s_waitcnt lgkmcnt(1)
	v_mfma_f32_16x16x32_f16 v[142:145], v[38:41], v[78:81], v[142:145]
	v_mfma_f32_16x16x32_f16 v[158:161], v[50:53], v[78:81], v[158:161]
	s_waitcnt lgkmcnt(0)
	v_mfma_f32_16x16x32_f16 v[62:65], v[38:41], v[214:217], v[62:65]
	v_mfma_f32_16x16x32_f16 v[178:181], v[50:53], v[214:217], v[178:181]
	ds_read_b128 v[78:81], v151 offset:1888
	ds_read_b128 v[214:217], v151 offset:2496
	s_waitcnt lgkmcnt(1)
	v_mfma_f32_16x16x32_f16 v[182:185], v[38:41], v[78:81], v[182:185]
	v_mfma_f32_16x16x32_f16 v[198:201], v[50:53], v[78:81], v[198:201]
	s_waitcnt lgkmcnt(0)
	v_mfma_f32_16x16x32_f16 v[134:137], v[38:41], v[214:217], v[134:137]
	v_mfma_f32_16x16x32_f16 v[146:149], v[50:53], v[214:217], v[146:149]
	v_add_u32_e32 v78, 0x17840, v244
	v_min_u32_e32 v78, v78, v157
	global_load_dwordx4 v[78:81], v78, s[8:9] nt
	s_waitcnt vmcnt(21)
	v_cvt_pk_f16_f32 v85, v84, v85
	v_cvt_pk_f16_f32 v84, v82, v83
	ds_write_b16 v238, v84 offset:608
	ds_write_b16_d16_hi v239, v84 offset:608
	ds_write_b16 v240, v85 offset:608
	ds_write_b16_d16_hi v241, v85 offset:608
	ds_read_b128 v[82:85], v151 offset:3104
	ds_read_b128 v[214:217], v151 offset:4928
	s_waitcnt lgkmcnt(1)
	v_mfma_f32_16x16x32_f16 v[206:209], v[38:41], v[82:85], v[206:209]
	v_mfma_f32_16x16x32_f16 v[122:125], v[50:53], v[82:85], v[122:125]
	ds_read_b128 v[82:85], v151 offset:3712
	ds_read_b128 v[222:225], v151 offset:4320
	s_waitcnt lgkmcnt(1)
	v_mfma_f32_16x16x32_f16 v[210:213], v[38:41], v[82:85], v[210:213]
	v_mfma_f32_16x16x32_f16 v[190:193], v[50:53], v[82:85], v[190:193]
	s_waitcnt lgkmcnt(0)
	v_mfma_f32_16x16x32_f16 v[166:169], v[38:41], v[222:225], v[166:169]
	v_mfma_f32_16x16x32_f16 v[162:165], v[50:53], v[222:225], v[162:165]
	v_mfma_f32_16x16x32_f16 v[138:141], v[38:41], v[214:217], v[138:141]
	v_mfma_f32_16x16x32_f16 v[170:173], v[50:53], v[214:217], v[170:173]
	v_add_u32_e32 v82, 0x2de80, v150
	v_min_u32_e32 v82, v82, v157
	global_load_dwordx4 v[82:85], v82, s[8:9] nt
	s_waitcnt vmcnt(21)
	v_cvt_pk_f16_f32 v89, v88, v89
	v_cvt_pk_f16_f32 v88, v86, v87
	ds_write_b16 v234, v88 offset:1216
	ds_write_b16_d16_hi v235, v88 offset:1216
	ds_write_b16 v236, v89 offset:1216
	ds_write_b16_d16_hi v237, v89 offset:1216
	ds_read_b128 v[86:89], v151 offset:5536
	ds_read_b128 v[214:217], v151 offset:6144
	s_waitcnt lgkmcnt(1)
	v_mfma_f32_16x16x32_f16 v[174:177], v[38:41], v[86:89], v[174:177]
	v_mfma_f32_16x16x32_f16 v[126:129], v[50:53], v[86:89], v[126:129]
	s_waitcnt lgkmcnt(0)
	v_mfma_f32_16x16x32_f16 v[218:221], v[38:41], v[214:217], v[218:221]
	v_mfma_f32_16x16x32_f16 v[194:197], v[50:53], v[214:217], v[194:197]
	ds_read_b128 v[86:89], v151 offset:6752
	ds_read_b128 v[214:217], v151 offset:7360
	s_waitcnt lgkmcnt(1)
	v_mfma_f32_16x16x32_f16 v[186:189], v[38:41], v[86:89], v[186:189]
	v_mfma_f32_16x16x32_f16 v[202:205], v[50:53], v[86:89], v[202:205]
	s_waitcnt lgkmcnt(0)
	v_mfma_f32_16x16x32_f16 v[30:33], v[38:41], v[214:217], v[30:33]
	v_mfma_f32_16x16x32_f16 v[38:41], v[50:53], v[214:217], v[18:21]
	s_nop 2
	v_add_u32_e32 v18, 0x444c0, v244
	v_min_u32_e32 v18, v18, v157
	global_load_dwordx4 v[50:53], v18, s[8:9] nt
	s_waitcnt vmcnt(21)
	v_cvt_pk_f16_f32 v19, v92, v93
	v_cvt_pk_f16_f32 v18, v90, v91
	ds_write_b16 v238, v18 offset:1824
	ds_write_b16_d16_hi v239, v18 offset:1824
	ds_write_b16 v240, v19 offset:1824
	ds_write_b16_d16_hi v241, v19 offset:1824
	ds_read_b128 v[18:21], v151 offset:128
	ds_read_b128 v[86:89], v151 offset:736
	s_waitcnt lgkmcnt(1)
	v_mfma_f32_16x16x32_f16 v[130:133], v[22:25], v[18:21], v[130:133]
	v_mfma_f32_16x16x32_f16 v[214:217], v[6:9], v[18:21], v[66:69]
	ds_read_b128 v[18:21], v151 offset:1344
	s_nop 1
	ds_read_b128 v[66:69], v151 offset:1952
	s_waitcnt lgkmcnt(2)
	v_mfma_f32_16x16x32_f16 v[142:145], v[22:25], v[86:89], v[142:145]
	v_mfma_f32_16x16x32_f16 v[158:161], v[6:9], v[86:89], v[158:161]
	s_waitcnt lgkmcnt(1)
	v_mfma_f32_16x16x32_f16 v[222:225], v[22:25], v[18:21], v[62:65]
	v_mfma_f32_16x16x32_f16 v[178:181], v[6:9], v[18:21], v[178:181]
	s_waitcnt lgkmcnt(0)
	v_mfma_f32_16x16x32_f16 v[182:185], v[22:25], v[66:69], v[182:185]
	v_mfma_f32_16x16x32_f16 v[198:201], v[6:9], v[66:69], v[198:201]
	v_add_u32_e32 v18, 0x5ab00, v150
	v_min_u32_e32 v18, v18, v157
	global_load_dwordx4 v[86:89], v18, s[8:9] nt
	s_waitcnt vmcnt(21)
	v_cvt_pk_f16_f32 v19, v96, v97
	v_cvt_pk_f16_f32 v18, v94, v95
	ds_write_b16 v234, v18 offset:2432
	ds_write_b16_d16_hi v235, v18 offset:2432
	ds_write_b16 v236, v19 offset:2432
	ds_write_b16_d16_hi v237, v19 offset:2432
	ds_read_b128 v[18:21], v151 offset:2560
	ds_read_b128 v[62:65], v151 offset:3168
	s_waitcnt lgkmcnt(1)
	v_mfma_f32_16x16x32_f16 v[134:137], v[22:25], v[18:21], v[134:137]
	v_mfma_f32_16x16x32_f16 v[146:149], v[6:9], v[18:21], v[146:149]
	s_waitcnt lgkmcnt(0)
	v_mfma_f32_16x16x32_f16 v[206:209], v[22:25], v[62:65], v[206:209]
	v_mfma_f32_16x16x32_f16 v[122:125], v[6:9], v[62:65], v[122:125]
	ds_read_b128 v[18:21], v151 offset:3776
	ds_read_b128 v[62:65], v151 offset:4384
	s_waitcnt lgkmcnt(1)
	v_mfma_f32_16x16x32_f16 v[210:213], v[22:25], v[18:21], v[210:213]
	v_mfma_f32_16x16x32_f16 v[190:193], v[6:9], v[18:21], v[190:193]
	s_waitcnt lgkmcnt(0)
	v_mfma_f32_16x16x32_f16 v[166:169], v[22:25], v[62:65], v[166:169]
	v_mfma_f32_16x16x32_f16 v[162:165], v[6:9], v[62:65], v[162:165]
	v_add_u32_e32 v18, 0x71140, v244
	v_min_u32_e32 v18, v18, v157
	global_load_dwordx4 v[90:93], v18, s[8:9] nt
	s_waitcnt vmcnt(21)
	v_cvt_pk_f16_f32 v19, v100, v101
	v_cvt_pk_f16_f32 v18, v98, v99
	ds_write_b16 v238, v18 offset:3040
	ds_write_b16_d16_hi v239, v18 offset:3040
	ds_write_b16 v240, v19 offset:3040
	ds_write_b16_d16_hi v241, v19 offset:3040
	ds_read_b128 v[18:21], v151 offset:4992
	ds_read_b128 v[62:65], v151 offset:5600
	s_waitcnt lgkmcnt(1)
	v_mfma_f32_16x16x32_f16 v[98:101], v[22:25], v[18:21], v[138:141]
	v_mfma_f32_16x16x32_f16 v[138:141], v[6:9], v[18:21], v[170:173]
	s_waitcnt lgkmcnt(0)
	v_mfma_f32_16x16x32_f16 v[170:173], v[22:25], v[62:65], v[174:177]
	v_mfma_f32_16x16x32_f16 v[126:129], v[6:9], v[62:65], v[126:129]
	ds_read_b128 v[18:21], v151 offset:6208
	ds_read_b128 v[62:65], v151 offset:6816
	s_waitcnt lgkmcnt(1)
	v_mfma_f32_16x16x32_f16 v[174:177], v[22:25], v[18:21], v[218:221]
	v_mfma_f32_16x16x32_f16 v[194:197], v[6:9], v[18:21], v[194:197]
	s_waitcnt lgkmcnt(0)
	v_mfma_f32_16x16x32_f16 v[186:189], v[22:25], v[62:65], v[186:189]
	v_mfma_f32_16x16x32_f16 v[202:205], v[6:9], v[62:65], v[202:205]
	v_add_u32_e32 v18, 0x87780, v150
	v_min_u32_e32 v18, v18, v157
	global_load_dwordx4 v[94:97], v18, s[8:9] nt
	s_waitcnt vmcnt(21)
	v_cvt_pk_f16_f32 v19, v104, v105
	v_cvt_pk_f16_f32 v18, v102, v103
	ds_write_b16 v234, v18 offset:3648
	ds_write_b16_d16_hi v235, v18 offset:3648
	ds_write_b16 v236, v19 offset:3648
	ds_write_b16_d16_hi v237, v19 offset:3648
	ds_read_b128 v[102:105], v151 offset:7424
	s_mov_b32 s3, 0x88000
	v_add_co_u32_e32 v18, vcc, s3, v152
	s_mov_b32 s3, 0x8c000
	s_nop 0
	v_addc_co_u32_e32 v19, vcc, 0, v153, vcc
	global_load_dwordx4 v[62:65], v[18:19], off sc1
	global_load_dwordx4 v[66:69], v[18:19], off offset:256 sc1
	v_add_co_u32_e32 v18, vcc, s3, v152
	s_waitcnt lgkmcnt(0)
	v_mfma_f32_16x16x32_f16 v[22:25], v[22:25], v[102:105], v[30:33]
	v_addc_co_u32_e32 v19, vcc, 0, v153, vcc
	s_nop 1
	global_load_dwordx4 v[30:33], v[18:19], off sc1
	s_nop 0
	global_load_dwordx4 v[18:21], v[18:19], off offset:256 sc1
	v_mfma_f32_16x16x32_f16 v[38:41], v[6:9], v[102:105], v[38:41]
	ds_read_b128 v[6:9], v151 offset:192
	ds_read_b128 v[102:105], v151 offset:800
	s_waitcnt vmcnt(24) lgkmcnt(1)
	v_mfma_f32_16x16x32_f16 v[130:133], v[42:45], v[6:9], v[130:133]
	s_waitcnt vmcnt(23)
	v_mfma_f32_16x16x32_f16 v[214:217], v[58:61], v[6:9], v[214:217]
	ds_read_b128 v[6:9], v151 offset:1408
	s_waitcnt lgkmcnt(1)
	v_mfma_f32_16x16x32_f16 v[142:145], v[42:45], v[102:105], v[142:145]
	v_mfma_f32_16x16x32_f16 v[158:161], v[58:61], v[102:105], v[158:161]
	s_waitcnt lgkmcnt(0)
	v_mfma_f32_16x16x32_f16 v[218:221], v[42:45], v[6:9], v[222:225]
	v_mfma_f32_16x16x32_f16 v[178:181], v[58:61], v[6:9], v[178:181]
	v_add_u32_e32 v6, 0x9ddc0, v244
	v_min_u32_e32 v6, v6, v157
	global_load_dwordx4 v[6:9], v6, s[8:9] nt
	s_waitcnt vmcnt(21)
	v_cvt_pk_f16_f32 v5, v4, v5
	v_cvt_pk_f16_f32 v4, v2, v3
	ds_write_b16 v238, v4 offset:4256
	ds_write_b16_d16_hi v239, v4 offset:4256
	ds_write_b16 v240, v5 offset:4256
	ds_write_b16_d16_hi v241, v5 offset:4256
	ds_read_b128 v[2:5], v151 offset:2016
	ds_read_b128 v[102:105], v151 offset:2624
	s_waitcnt lgkmcnt(1)
	v_mfma_f32_16x16x32_f16 v[182:185], v[42:45], v[2:5], v[182:185]
	v_mfma_f32_16x16x32_f16 v[2:5], v[58:61], v[2:5], v[198:201]
	s_waitcnt lgkmcnt(0)
	v_mfma_f32_16x16x32_f16 v[134:137], v[42:45], v[102:105], v[134:137]
	v_mfma_f32_16x16x32_f16 v[146:149], v[58:61], v[102:105], v[146:149]
	ds_read_b128 v[102:105], v151 offset:3232
	ds_read_b128 v[198:201], v151 offset:3840
	s_waitcnt lgkmcnt(1)
	v_mfma_f32_16x16x32_f16 v[206:209], v[42:45], v[102:105], v[206:209]
	v_mfma_f32_16x16x32_f16 v[122:125], v[58:61], v[102:105], v[122:125]
	s_waitcnt lgkmcnt(0)
	v_mfma_f32_16x16x32_f16 v[210:213], v[42:45], v[198:201], v[210:213]
	v_mfma_f32_16x16x32_f16 v[190:193], v[58:61], v[198:201], v[190:193]
	v_add_u32_e32 v102, 0xb4400, v150
	v_min_u32_e32 v102, v102, v157
	global_load_dwordx4 v[102:105], v102, s[8:9] nt
	s_waitcnt vmcnt(21)
	v_cvt_pk_f16_f32 v109, v108, v109
	v_cvt_pk_f16_f32 v108, v106, v107
	ds_write_b16 v234, v108 offset:4864
	ds_write_b16_d16_hi v235, v108 offset:4864
	ds_write_b16 v236, v109 offset:4864
	ds_write_b16_d16_hi v237, v109 offset:4864
	ds_read_b128 v[106:109], v151 offset:4448
	ds_read_b128 v[198:201], v151 offset:6272
	s_waitcnt lgkmcnt(1)
	v_mfma_f32_16x16x32_f16 v[166:169], v[42:45], v[106:109], v[166:169]
	v_mfma_f32_16x16x32_f16 v[162:165], v[58:61], v[106:109], v[162:165]
	ds_read_b128 v[106:109], v151 offset:5056
	ds_read_b128 v[222:225], v151 offset:5664
	s_waitcnt lgkmcnt(1)
	v_mfma_f32_16x16x32_f16 v[98:101], v[42:45], v[106:109], v[98:101]
	v_mfma_f32_16x16x32_f16 v[138:141], v[58:61], v[106:109], v[138:141]
	s_waitcnt lgkmcnt(0)
	v_mfma_f32_16x16x32_f16 v[170:173], v[42:45], v[222:225], v[170:173]
	v_mfma_f32_16x16x32_f16 v[126:129], v[58:61], v[222:225], v[126:129]
	v_mfma_f32_16x16x32_f16 v[174:177], v[42:45], v[198:201], v[174:177]
	v_mfma_f32_16x16x32_f16 v[194:197], v[58:61], v[198:201], v[194:197]
	v_add_u32_e32 v106, 0xcaa40, v244
	v_min_u32_e32 v106, v106, v157
	global_load_dwordx4 v[106:109], v106, s[8:9] nt
	s_waitcnt vmcnt(21)
	v_cvt_pk_f16_f32 v117, v116, v117
	v_cvt_pk_f16_f32 v116, v114, v115
	ds_write_b16 v238, v116 offset:5472
	ds_write_b16_d16_hi v239, v116 offset:5472
	ds_write_b16 v240, v117 offset:5472
	ds_write_b16_d16_hi v241, v117 offset:5472
	ds_read_b128 v[114:117], v151 offset:6880
	ds_read_b128 v[198:201], v151 offset:7488
	s_waitcnt lgkmcnt(1)
	v_mfma_f32_16x16x32_f16 v[186:189], v[42:45], v[114:117], v[186:189]
	v_mfma_f32_16x16x32_f16 v[202:205], v[58:61], v[114:117], v[202:205]
	s_waitcnt lgkmcnt(0)
	v_mfma_f32_16x16x32_f16 v[22:25], v[42:45], v[198:201], v[22:25]
	v_mfma_f32_16x16x32_f16 v[58:61], v[58:61], v[198:201], v[38:41]
	s_nop 2
	ds_read_b128 v[38:41], v151 offset:256
	ds_read_b128 v[42:45], v151 offset:864
	s_waitcnt lgkmcnt(1)
	v_mfma_f32_16x16x32_f16 v[130:133], v[34:37], v[38:41], v[130:133]
	v_mfma_f32_16x16x32_f16 v[198:201], v[14:17], v[38:41], v[214:217]
	s_waitcnt lgkmcnt(0)
	v_mfma_f32_16x16x32_f16 v[142:145], v[34:37], v[42:45], v[142:145]
	v_mfma_f32_16x16x32_f16 v[158:161], v[14:17], v[42:45], v[158:161]
	v_add_u32_e32 v38, 0xe1080, v150
	v_min_u32_e32 v38, v38, v157
	global_load_dwordx4 v[114:117], v38, s[8:9] nt
	s_waitcnt vmcnt(21)
	v_cvt_pk_f16_f32 v39, v112, v113
	v_cvt_pk_f16_f32 v38, v110, v111
	ds_write_b16 v234, v38 offset:6080
	ds_write_b16_d16_hi v235, v38 offset:6080
	ds_write_b16 v236, v39 offset:6080
	ds_write_b16_d16_hi v237, v39 offset:6080
	ds_read_b128 v[38:41], v151 offset:1472
	ds_read_b128 v[42:45], v151 offset:2080
	s_waitcnt lgkmcnt(1)
	v_mfma_f32_16x16x32_f16 v[214:217], v[34:37], v[38:41], v[218:221]
	v_mfma_f32_16x16x32_f16 v[178:181], v[14:17], v[38:41], v[178:181]
	s_waitcnt lgkmcnt(0)
	v_mfma_f32_16x16x32_f16 v[218:221], v[14:17], v[42:45], v[2:5]
	s_nop 2
	ds_read_b128 v[2:5], v151 offset:2688
	ds_read_b128 v[38:41], v151 offset:3296
	v_mfma_f32_16x16x32_f16 v[182:185], v[34:37], v[42:45], v[182:185]
	s_waitcnt lgkmcnt(1)
	v_mfma_f32_16x16x32_f16 v[134:137], v[34:37], v[2:5], v[134:137]
	v_mfma_f32_16x16x32_f16 v[146:149], v[14:17], v[2:5], v[146:149]
	s_waitcnt lgkmcnt(0)
	v_mfma_f32_16x16x32_f16 v[206:209], v[34:37], v[38:41], v[206:209]
	v_mfma_f32_16x16x32_f16 v[122:125], v[14:17], v[38:41], v[122:125]
	v_add_u32_e32 v2, 0xf76c0, v244
	v_min_u32_e32 v2, v2, v157
	global_load_dwordx4 v[110:113], v2, s[8:9] nt
	s_waitcnt vmcnt(21)
	v_cvt_pk_f16_f32 v3, v120, v121
	v_cvt_pk_f16_f32 v2, v118, v119
	ds_write_b16 v238, v2 offset:6688
	ds_write_b16_d16_hi v239, v2 offset:6688
	ds_write_b16 v240, v3 offset:6688
	ds_write_b16_d16_hi v241, v3 offset:6688
	ds_read_b128 v[2:5], v151 offset:3904
	ds_read_b128 v[38:41], v151 offset:4512
	s_waitcnt lgkmcnt(1)
	v_mfma_f32_16x16x32_f16 v[210:213], v[34:37], v[2:5], v[210:213]
	v_mfma_f32_16x16x32_f16 v[190:193], v[14:17], v[2:5], v[190:193]
	s_waitcnt lgkmcnt(0)
	v_mfma_f32_16x16x32_f16 v[166:169], v[34:37], v[38:41], v[166:169]
	v_mfma_f32_16x16x32_f16 v[162:165], v[14:17], v[38:41], v[162:165]
	ds_read_b128 v[2:5], v151 offset:5120
	ds_read_b128 v[38:41], v151 offset:5728
	s_waitcnt lgkmcnt(1)
	v_mfma_f32_16x16x32_f16 v[98:101], v[34:37], v[2:5], v[98:101]
	v_mfma_f32_16x16x32_f16 v[138:141], v[14:17], v[2:5], v[138:141]
	s_waitcnt lgkmcnt(0)
	v_mfma_f32_16x16x32_f16 v[170:173], v[34:37], v[38:41], v[170:173]
	v_mfma_f32_16x16x32_f16 v[126:129], v[14:17], v[38:41], v[126:129]
	v_add_u32_e32 v2, 0x10dd00, v150
	v_min_u32_e32 v2, v2, v157
	v_cndmask_b32_e64 v2, 0, v2, s[0:1]
	global_load_dwordx4 v[118:121], v2, s[8:9] nt
	s_waitcnt vmcnt(21)
	v_cvt_pk_f16_f32 v3, v72, v73
	v_cvt_pk_f16_f32 v2, v70, v71
	ds_write_b16 v234, v2 offset:7296
	ds_write_b16_d16_hi v235, v2 offset:7296
	ds_write_b16 v236, v3 offset:7296
	ds_write_b16_d16_hi v237, v3 offset:7296
	ds_read_b128 v[2:5], v151 offset:6336
	ds_read_b128 v[38:41], v151 offset:6944
	ds_read_b128 v[70:73], v151 offset:7552
	s_mov_b32 s3, 0x90000
	s_waitcnt lgkmcnt(0)
	v_mfma_f32_16x16x32_f16 v[174:177], v[34:37], v[2:5], v[174:177]
	s_barrier
	v_sub_u32_e32 v245, v234, v243
	v_add_u32_e32 v246, 0xfffffdc0, v245
	v_min_u32_e32 v245, v245, v246
	v_add_u32_e32 v234, v242, v245
	v_sub_u32_e32 v245, v235, v243
	v_add_u32_e32 v246, 0xfffffdc0, v245
	v_min_u32_e32 v245, v245, v246
	v_add_u32_e32 v235, v242, v245
	v_sub_u32_e32 v245, v236, v243
	v_add_u32_e32 v246, 0xfffffdc0, v245
	v_min_u32_e32 v245, v245, v246
	v_add_u32_e32 v236, v242, v245
	v_sub_u32_e32 v245, v237, v243
	v_add_u32_e32 v246, 0xfffffdc0, v245
	v_min_u32_e32 v245, v245, v246
	v_add_u32_e32 v237, v242, v245
	v_sub_u32_e32 v245, v238, v243
	v_add_u32_e32 v246, 0xfffffdc0, v245
	v_min_u32_e32 v245, v245, v246
	v_add_u32_e32 v238, v242, v245
	v_sub_u32_e32 v245, v239, v243
	v_add_u32_e32 v246, 0xfffffdc0, v245
	v_min_u32_e32 v245, v245, v246
	v_add_u32_e32 v239, v242, v245
	v_sub_u32_e32 v245, v240, v243
	v_add_u32_e32 v246, 0xfffffdc0, v245
	v_min_u32_e32 v245, v245, v246
	v_add_u32_e32 v240, v242, v245
	v_sub_u32_e32 v245, v241, v243
	v_add_u32_e32 v246, 0xfffffdc0, v245
	v_min_u32_e32 v245, v245, v246
	v_add_u32_e32 v241, v242, v245
	v_mfma_f32_16x16x32_f16 v[194:197], v[14:17], v[2:5], v[194:197]
	v_add_co_u32_e32 v2, vcc, s3, v152
	s_mov_b32 s3, 0x94000
	s_nop 0
	v_addc_co_u32_e32 v3, vcc, 0, v153, vcc
	v_mfma_f32_16x16x32_f16 v[186:189], v[34:37], v[38:41], v[186:189]
	v_mfma_f32_16x16x32_f16 v[202:205], v[14:17], v[38:41], v[202:205]
	global_load_dwordx4 v[38:41], v[2:3], off sc1
	global_load_dwordx4 v[42:45], v[2:3], off offset:256 sc1
	v_add_co_u32_e32 v2, vcc, s3, v152
	v_mfma_f32_16x16x32_f16 v[34:37], v[34:37], v[70:73], v[22:25]
	s_nop 0
	v_addc_co_u32_e32 v3, vcc, 0, v153, vcc
	s_nop 0
	global_load_dwordx4 v[22:25], v[2:3], off sc1
	s_nop 0
	global_load_dwordx4 v[2:5], v[2:3], off offset:256 sc1
	v_mfma_f32_16x16x32_f16 v[14:17], v[14:17], v[70:73], v[58:61]
	v_add_u32_e32 v157, 0x111528dc, v154
	s_nop 1
	ds_read_b128 v[58:61], v151 offset:320
	v_add_u32_e32 v70, 0x1400, v150
	s_waitcnt vmcnt(24) lgkmcnt(0)
	v_mfma_f32_16x16x32_f16 v[130:133], v[46:49], v[58:61], v[130:133]
	s_waitcnt vmcnt(23)
	v_mfma_f32_16x16x32_f16 v[198:201], v[54:57], v[58:61], v[198:201]
	v_min_u32_e32 v58, v70, v157
	global_load_dwordx4 v[58:61], v58, s[8:9] nt
	s_waitcnt vmcnt(21)
	v_cvt_pk_f16_f32 v71, v76, v77
	v_cvt_pk_f16_f32 v70, v74, v75
	ds_write_b16 v234, v70 offset:0
	ds_write_b16_d16_hi v235, v70 offset:0
	ds_write_b16 v236, v71 offset:0
	ds_write_b16_d16_hi v237, v71 offset:0
	ds_read_b128 v[70:73], v151 offset:928
	ds_read_b128 v[74:77], v151 offset:1536
	s_waitcnt lgkmcnt(1)
	v_mfma_f32_16x16x32_f16 v[142:145], v[46:49], v[70:73], v[142:145]
	v_mfma_f32_16x16x32_f16 v[158:161], v[54:57], v[70:73], v[158:161]
	s_waitcnt lgkmcnt(0)
	v_mfma_f32_16x16x32_f16 v[214:217], v[46:49], v[74:77], v[214:217]
	v_mfma_f32_16x16x32_f16 v[178:181], v[54:57], v[74:77], v[178:181]
	ds_read_b128 v[70:73], v151 offset:2144
	ds_read_b128 v[74:77], v151 offset:2752
	s_waitcnt lgkmcnt(1)
	v_mfma_f32_16x16x32_f16 v[182:185], v[46:49], v[70:73], v[182:185]
	v_mfma_f32_16x16x32_f16 v[218:221], v[54:57], v[70:73], v[218:221]
	s_waitcnt lgkmcnt(0)
	v_mfma_f32_16x16x32_f16 v[134:137], v[46:49], v[74:77], v[134:137]
	v_mfma_f32_16x16x32_f16 v[146:149], v[54:57], v[74:77], v[146:149]
	v_add_u32_e32 v70, 0x17a40, v244
	v_min_u32_e32 v70, v70, v157
	global_load_dwordx4 v[70:73], v70, s[8:9] nt
	s_waitcnt vmcnt(21)
	v_cvt_pk_f16_f32 v75, v80, v81
	v_cvt_pk_f16_f32 v74, v78, v79
	ds_write_b16 v238, v74 offset:608
	ds_write_b16_d16_hi v239, v74 offset:608
	ds_write_b16 v240, v75 offset:608
	ds_write_b16_d16_hi v241, v75 offset:608
	ds_read_b128 v[74:77], v151 offset:3360
	ds_read_b128 v[78:81], v151 offset:5184
	s_waitcnt lgkmcnt(1)
	v_mfma_f32_16x16x32_f16 v[206:209], v[46:49], v[74:77], v[206:209]
	v_mfma_f32_16x16x32_f16 v[122:125], v[54:57], v[74:77], v[122:125]
	ds_read_b128 v[74:77], v151 offset:3968
	ds_read_b128 v[222:225], v151 offset:4576
	s_waitcnt lgkmcnt(1)
	v_mfma_f32_16x16x32_f16 v[210:213], v[46:49], v[74:77], v[210:213]
	v_mfma_f32_16x16x32_f16 v[190:193], v[54:57], v[74:77], v[190:193]
	s_waitcnt lgkmcnt(0)
	v_mfma_f32_16x16x32_f16 v[166:169], v[46:49], v[222:225], v[166:169]
	v_mfma_f32_16x16x32_f16 v[162:165], v[54:57], v[222:225], v[162:165]
	v_mfma_f32_16x16x32_f16 v[98:101], v[46:49], v[78:81], v[98:101]
	v_mfma_f32_16x16x32_f16 v[138:141], v[54:57], v[78:81], v[138:141]
	v_add_u32_e32 v74, 0x2e080, v150
	v_min_u32_e32 v74, v74, v157
	global_load_dwordx4 v[74:77], v74, s[8:9] nt
	s_waitcnt vmcnt(21)
	v_cvt_pk_f16_f32 v79, v84, v85
	v_cvt_pk_f16_f32 v78, v82, v83
	ds_write_b16 v234, v78 offset:1216
	ds_write_b16_d16_hi v235, v78 offset:1216
	ds_write_b16 v236, v79 offset:1216
	ds_write_b16_d16_hi v237, v79 offset:1216
	ds_read_b128 v[78:81], v151 offset:5792
	ds_read_b128 v[82:85], v151 offset:6400
	s_waitcnt lgkmcnt(1)
	v_mfma_f32_16x16x32_f16 v[170:173], v[46:49], v[78:81], v[170:173]
	v_mfma_f32_16x16x32_f16 v[126:129], v[54:57], v[78:81], v[126:129]
	s_waitcnt lgkmcnt(0)
	v_mfma_f32_16x16x32_f16 v[174:177], v[46:49], v[82:85], v[174:177]
	v_mfma_f32_16x16x32_f16 v[194:197], v[54:57], v[82:85], v[194:197]
	ds_read_b128 v[78:81], v151 offset:7008
	ds_read_b128 v[82:85], v151 offset:7616
	s_waitcnt lgkmcnt(1)
	v_mfma_f32_16x16x32_f16 v[186:189], v[46:49], v[78:81], v[186:189]
	v_mfma_f32_16x16x32_f16 v[202:205], v[54:57], v[78:81], v[202:205]
	s_waitcnt lgkmcnt(0)
	v_mfma_f32_16x16x32_f16 v[34:37], v[46:49], v[82:85], v[34:37]
	v_mfma_f32_16x16x32_f16 v[46:49], v[54:57], v[82:85], v[14:17]
	s_nop 2
	v_add_u32_e32 v14, 0x446c0, v244
	v_min_u32_e32 v14, v14, v157
	global_load_dwordx4 v[78:81], v14, s[8:9] nt
	s_waitcnt vmcnt(21)
	v_cvt_pk_f16_f32 v15, v52, v53
	v_cvt_pk_f16_f32 v14, v50, v51
	ds_write_b16 v238, v14 offset:1824
	ds_write_b16_d16_hi v239, v14 offset:1824
	ds_write_b16 v240, v15 offset:1824
	ds_write_b16_d16_hi v241, v15 offset:1824
	ds_read_b128 v[14:17], v151 offset:384
	ds_read_b128 v[50:53], v151 offset:992
	s_waitcnt lgkmcnt(1)
	v_mfma_f32_16x16x32_f16 v[130:133], v[26:29], v[14:17], v[130:133]
	v_mfma_f32_16x16x32_f16 v[198:201], v[10:13], v[14:17], v[198:201]
	s_waitcnt lgkmcnt(0)
	v_mfma_f32_16x16x32_f16 v[142:145], v[26:29], v[50:53], v[142:145]
	v_mfma_f32_16x16x32_f16 v[158:161], v[10:13], v[50:53], v[158:161]
	ds_read_b128 v[14:17], v151 offset:1600
	ds_read_b128 v[50:53], v151 offset:2208
	s_waitcnt lgkmcnt(1)
	v_mfma_f32_16x16x32_f16 v[214:217], v[26:29], v[14:17], v[214:217]
	v_mfma_f32_16x16x32_f16 v[178:181], v[10:13], v[14:17], v[178:181]
	s_waitcnt lgkmcnt(0)
	v_mfma_f32_16x16x32_f16 v[182:185], v[26:29], v[50:53], v[182:185]
	v_mfma_f32_16x16x32_f16 v[218:221], v[10:13], v[50:53], v[218:221]
	v_add_u32_e32 v14, 0x5ad00, v150
	v_min_u32_e32 v14, v14, v157
	global_load_dwordx4 v[82:85], v14, s[8:9] nt
	s_waitcnt vmcnt(21)
	v_cvt_pk_f16_f32 v15, v88, v89
	v_cvt_pk_f16_f32 v14, v86, v87
	ds_write_b16 v234, v14 offset:2432
	ds_write_b16_d16_hi v235, v14 offset:2432
	ds_write_b16 v236, v15 offset:2432
	ds_write_b16_d16_hi v237, v15 offset:2432
	ds_read_b128 v[14:17], v151 offset:2816
	ds_read_b128 v[50:53], v151 offset:3424
	s_waitcnt lgkmcnt(1)
	v_mfma_f32_16x16x32_f16 v[134:137], v[26:29], v[14:17], v[134:137]
	v_mfma_f32_16x16x32_f16 v[146:149], v[10:13], v[14:17], v[146:149]
	s_waitcnt lgkmcnt(0)
	v_mfma_f32_16x16x32_f16 v[206:209], v[26:29], v[50:53], v[206:209]
	v_mfma_f32_16x16x32_f16 v[122:125], v[10:13], v[50:53], v[122:125]
	ds_read_b128 v[14:17], v151 offset:4032
	ds_read_b128 v[50:53], v151 offset:4640
	s_waitcnt lgkmcnt(1)
	v_mfma_f32_16x16x32_f16 v[210:213], v[26:29], v[14:17], v[210:213]
	v_mfma_f32_16x16x32_f16 v[190:193], v[10:13], v[14:17], v[190:193]
	s_waitcnt lgkmcnt(0)
	v_mfma_f32_16x16x32_f16 v[166:169], v[26:29], v[50:53], v[166:169]
	v_mfma_f32_16x16x32_f16 v[162:165], v[10:13], v[50:53], v[162:165]
	v_add_u32_e32 v14, 0x71340, v244
	v_min_u32_e32 v14, v14, v157
	global_load_dwordx4 v[86:89], v14, s[8:9] nt
	s_waitcnt vmcnt(21)
	v_cvt_pk_f16_f32 v15, v92, v93
	v_cvt_pk_f16_f32 v14, v90, v91
	ds_write_b16 v238, v14 offset:3040
	ds_write_b16_d16_hi v239, v14 offset:3040
	ds_write_b16 v240, v15 offset:3040
	ds_write_b16_d16_hi v241, v15 offset:3040
	ds_read_b128 v[14:17], v151 offset:5248
	ds_read_b128 v[50:53], v151 offset:5856
	s_waitcnt lgkmcnt(1)
	v_mfma_f32_16x16x32_f16 v[222:225], v[26:29], v[14:17], v[98:101]
	v_mfma_f32_16x16x32_f16 v[138:141], v[10:13], v[14:17], v[138:141]
	s_waitcnt lgkmcnt(0)
	v_mfma_f32_16x16x32_f16 v[170:173], v[26:29], v[50:53], v[170:173]
	v_mfma_f32_16x16x32_f16 v[126:129], v[10:13], v[50:53], v[126:129]
	ds_read_b128 v[14:17], v151 offset:6464
	ds_read_b128 v[50:53], v151 offset:7072
	s_waitcnt lgkmcnt(1)
	v_mfma_f32_16x16x32_f16 v[174:177], v[26:29], v[14:17], v[174:177]
	v_mfma_f32_16x16x32_f16 v[194:197], v[10:13], v[14:17], v[194:197]
	s_waitcnt lgkmcnt(0)
	v_mfma_f32_16x16x32_f16 v[186:189], v[26:29], v[50:53], v[186:189]
	v_mfma_f32_16x16x32_f16 v[202:205], v[10:13], v[50:53], v[202:205]
	v_add_u32_e32 v14, 0x87980, v150
	v_min_u32_e32 v14, v14, v157
	global_load_dwordx4 v[90:93], v14, s[8:9] nt
	s_waitcnt vmcnt(21)
	v_cvt_pk_f16_f32 v15, v96, v97
	v_cvt_pk_f16_f32 v14, v94, v95
	ds_write_b16 v234, v14 offset:3648
	ds_write_b16_d16_hi v235, v14 offset:3648
	ds_write_b16 v236, v15 offset:3648
	ds_write_b16_d16_hi v237, v15 offset:3648
	ds_read_b128 v[94:97], v151 offset:7680
	s_mov_b32 s3, 0x98000
	v_add_co_u32_e32 v14, vcc, s3, v152
	s_mov_b32 s3, 0x9c000
	s_nop 0
	v_addc_co_u32_e32 v15, vcc, 0, v153, vcc
	global_load_dwordx4 v[50:53], v[14:15], off sc1
	global_load_dwordx4 v[54:57], v[14:15], off offset:256 sc1
	v_add_co_u32_e32 v14, vcc, s3, v152
	s_waitcnt lgkmcnt(0)
	v_mfma_f32_16x16x32_f16 v[34:37], v[26:29], v[94:97], v[34:37]
	v_addc_co_u32_e32 v15, vcc, 0, v153, vcc
	global_load_dwordx4 v[26:29], v[14:15], off sc1
	s_nop 0
	global_load_dwordx4 v[14:17], v[14:15], off offset:256 sc1
	v_mfma_f32_16x16x32_f16 v[10:13], v[10:13], v[94:97], v[46:49]
	s_nop 2
	ds_read_b128 v[46:49], v151 offset:448
	ds_read_b128 v[94:97], v151 offset:1056
	s_waitcnt vmcnt(24) lgkmcnt(1)
	v_mfma_f32_16x16x32_f16 v[130:133], v[62:65], v[46:49], v[130:133]
	s_waitcnt lgkmcnt(0)
	v_mfma_f32_16x16x32_f16 v[142:145], v[62:65], v[94:97], v[142:145]
	s_waitcnt vmcnt(23)
	v_mfma_f32_16x16x32_f16 v[158:161], v[66:69], v[94:97], v[158:161]
	ds_read_b128 v[94:97], v151 offset:1664
	v_mfma_f32_16x16x32_f16 v[46:49], v[66:69], v[46:49], v[198:201]
	s_waitcnt lgkmcnt(0)
	v_mfma_f32_16x16x32_f16 v[198:201], v[62:65], v[94:97], v[214:217]
	v_mfma_f32_16x16x32_f16 v[178:181], v[66:69], v[94:97], v[178:181]
	v_add_u32_e32 v94, 0x9dfc0, v244
	v_min_u32_e32 v94, v94, v157
	global_load_dwordx4 v[94:97], v94, s[8:9] nt
	s_waitcnt vmcnt(21)
	v_cvt_pk_f16_f32 v9, v8, v9
	v_cvt_pk_f16_f32 v8, v6, v7
	ds_write_b16 v238, v8 offset:4256
	ds_write_b16_d16_hi v239, v8 offset:4256
	ds_write_b16 v240, v9 offset:4256
	ds_write_b16_d16_hi v241, v9 offset:4256
	ds_read_b128 v[6:9], v151 offset:2272
	ds_read_b128 v[98:101], v151 offset:2880
	s_waitcnt lgkmcnt(1)
	v_mfma_f32_16x16x32_f16 v[182:185], v[62:65], v[6:9], v[182:185]
	s_waitcnt lgkmcnt(0)
	v_mfma_f32_16x16x32_f16 v[134:137], v[62:65], v[98:101], v[134:137]
	v_mfma_f32_16x16x32_f16 v[146:149], v[66:69], v[98:101], v[146:149]
	ds_read_b128 v[98:101], v151 offset:3488
	ds_read_b128 v[214:217], v151 offset:4096
	v_mfma_f32_16x16x32_f16 v[6:9], v[66:69], v[6:9], v[218:221]
	s_waitcnt lgkmcnt(1)
	v_mfma_f32_16x16x32_f16 v[206:209], v[62:65], v[98:101], v[206:209]
	v_mfma_f32_16x16x32_f16 v[122:125], v[66:69], v[98:101], v[122:125]
	s_waitcnt lgkmcnt(0)
	v_mfma_f32_16x16x32_f16 v[210:213], v[62:65], v[214:217], v[210:213]
	v_mfma_f32_16x16x32_f16 v[190:193], v[66:69], v[214:217], v[190:193]
	v_add_u32_e32 v98, 0xb4600, v150
	v_min_u32_e32 v98, v98, v157
	global_load_dwordx4 v[98:101], v98, s[8:9] nt
	s_waitcnt vmcnt(21)
	v_cvt_pk_f16_f32 v105, v104, v105
	v_cvt_pk_f16_f32 v104, v102, v103
	ds_write_b16 v234, v104 offset:4864
	ds_write_b16_d16_hi v235, v104 offset:4864
	ds_write_b16 v236, v105 offset:4864
	ds_write_b16_d16_hi v237, v105 offset:4864
	ds_read_b128 v[102:105], v151 offset:4704
	ds_read_b128 v[214:217], v151 offset:6528
	s_waitcnt lgkmcnt(1)
	v_mfma_f32_16x16x32_f16 v[166:169], v[62:65], v[102:105], v[166:169]
	v_mfma_f32_16x16x32_f16 v[162:165], v[66:69], v[102:105], v[162:165]
	ds_read_b128 v[102:105], v151 offset:5312
	ds_read_b128 v[218:221], v151 offset:5920
	s_waitcnt lgkmcnt(1)
	v_mfma_f32_16x16x32_f16 v[222:225], v[62:65], v[102:105], v[222:225]
	v_mfma_f32_16x16x32_f16 v[138:141], v[66:69], v[102:105], v[138:141]
	s_waitcnt lgkmcnt(0)
	v_mfma_f32_16x16x32_f16 v[170:173], v[62:65], v[218:221], v[170:173]
	v_mfma_f32_16x16x32_f16 v[126:129], v[66:69], v[218:221], v[126:129]
	v_mfma_f32_16x16x32_f16 v[174:177], v[62:65], v[214:217], v[174:177]
	v_mfma_f32_16x16x32_f16 v[194:197], v[66:69], v[214:217], v[194:197]
	v_add_u32_e32 v102, 0xcac40, v244
	v_min_u32_e32 v102, v102, v157
	global_load_dwordx4 v[102:105], v102, s[8:9] nt
	s_waitcnt vmcnt(21)
	v_cvt_pk_f16_f32 v109, v108, v109
	v_cvt_pk_f16_f32 v108, v106, v107
	ds_write_b16 v238, v108 offset:5472
	ds_write_b16_d16_hi v239, v108 offset:5472
	ds_write_b16 v240, v109 offset:5472
	ds_write_b16_d16_hi v241, v109 offset:5472
	ds_read_b128 v[106:109], v151 offset:7136
	ds_read_b128 v[214:217], v151 offset:7744
	s_waitcnt lgkmcnt(1)
	v_mfma_f32_16x16x32_f16 v[186:189], v[62:65], v[106:109], v[186:189]
	s_waitcnt lgkmcnt(0)
	v_mfma_f32_16x16x32_f16 v[218:221], v[62:65], v[214:217], v[34:37]
	v_mfma_f32_16x16x32_f16 v[214:217], v[66:69], v[214:217], v[10:13]
	s_nop 2
	ds_read_b128 v[10:13], v151 offset:512
	ds_read_b128 v[34:37], v151 offset:1120
	v_mfma_f32_16x16x32_f16 v[202:205], v[66:69], v[106:109], v[202:205]
	s_waitcnt lgkmcnt(1)
	v_mfma_f32_16x16x32_f16 v[130:133], v[30:33], v[10:13], v[130:133]
	v_mfma_f32_16x16x32_f16 v[226:229], v[18:21], v[10:13], v[46:49]
	s_waitcnt lgkmcnt(0)
	v_mfma_f32_16x16x32_f16 v[142:145], v[30:33], v[34:37], v[142:145]
	v_mfma_f32_16x16x32_f16 v[158:161], v[18:21], v[34:37], v[158:161]
	v_add_u32_e32 v10, 0xe1280, v150
	v_min_u32_e32 v10, v10, v157
	global_load_dwordx4 v[62:65], v10, s[8:9] nt
	s_waitcnt vmcnt(21)
	v_cvt_pk_f16_f32 v11, v116, v117
	v_cvt_pk_f16_f32 v10, v114, v115
	ds_write_b16 v234, v10 offset:6080
	ds_write_b16_d16_hi v235, v10 offset:6080
	ds_write_b16 v236, v11 offset:6080
	ds_write_b16_d16_hi v237, v11 offset:6080
	ds_read_b128 v[10:13], v151 offset:1728
	ds_read_b128 v[34:37], v151 offset:2336
	s_waitcnt lgkmcnt(1)
	v_mfma_f32_16x16x32_f16 v[114:117], v[30:33], v[10:13], v[198:201]
	v_mfma_f32_16x16x32_f16 v[178:181], v[18:21], v[10:13], v[178:181]
	s_waitcnt lgkmcnt(0)
	v_mfma_f32_16x16x32_f16 v[198:201], v[18:21], v[34:37], v[6:9]
	s_nop 2
	ds_read_b128 v[6:9], v151 offset:2944
	ds_read_b128 v[10:13], v151 offset:3552
	v_mfma_f32_16x16x32_f16 v[182:185], v[30:33], v[34:37], v[182:185]
	s_waitcnt lgkmcnt(1)
	v_mfma_f32_16x16x32_f16 v[134:137], v[30:33], v[6:9], v[134:137]
	v_mfma_f32_16x16x32_f16 v[146:149], v[18:21], v[6:9], v[146:149]
	s_waitcnt lgkmcnt(0)
	v_mfma_f32_16x16x32_f16 v[206:209], v[30:33], v[10:13], v[206:209]
	v_mfma_f32_16x16x32_f16 v[122:125], v[18:21], v[10:13], v[122:125]
	v_add_u32_e32 v6, 0xf78c0, v244
	v_min_u32_e32 v6, v6, v157
	global_load_dwordx4 v[66:69], v6, s[8:9] nt
	s_waitcnt vmcnt(21)
	v_cvt_pk_f16_f32 v7, v112, v113
	v_cvt_pk_f16_f32 v6, v110, v111
	ds_write_b16 v238, v6 offset:6688
	ds_write_b16_d16_hi v239, v6 offset:6688
	ds_write_b16 v240, v7 offset:6688
	ds_write_b16_d16_hi v241, v7 offset:6688
	ds_read_b128 v[6:9], v151 offset:4160
	ds_read_b128 v[10:13], v151 offset:4768
	s_waitcnt lgkmcnt(1)
	v_mfma_f32_16x16x32_f16 v[210:213], v[30:33], v[6:9], v[210:213]
	v_mfma_f32_16x16x32_f16 v[190:193], v[18:21], v[6:9], v[190:193]
	s_waitcnt lgkmcnt(0)
	v_mfma_f32_16x16x32_f16 v[166:169], v[30:33], v[10:13], v[166:169]
	v_mfma_f32_16x16x32_f16 v[162:165], v[18:21], v[10:13], v[162:165]
	ds_read_b128 v[6:9], v151 offset:5376
	ds_read_b128 v[10:13], v151 offset:5984
	s_waitcnt lgkmcnt(1)
	v_mfma_f32_16x16x32_f16 v[222:225], v[30:33], v[6:9], v[222:225]
	v_mfma_f32_16x16x32_f16 v[138:141], v[18:21], v[6:9], v[138:141]
	s_waitcnt lgkmcnt(0)
	v_mfma_f32_16x16x32_f16 v[170:173], v[30:33], v[10:13], v[170:173]
	v_mfma_f32_16x16x32_f16 v[126:129], v[18:21], v[10:13], v[126:129]
	v_add_u32_e32 v6, 0x10df00, v150
	v_min_u32_e32 v6, v6, v157
	v_cndmask_b32_e64 v6, 0, v6, s[0:1]
	global_load_dwordx4 v[106:109], v6, s[8:9] nt
	s_waitcnt vmcnt(21)
	v_cvt_pk_f16_f32 v7, v120, v121
	v_cvt_pk_f16_f32 v6, v118, v119
	ds_write_b16 v234, v6 offset:7296
	ds_write_b16_d16_hi v235, v6 offset:7296
	ds_write_b16 v236, v7 offset:7296
	ds_write_b16_d16_hi v237, v7 offset:7296
	ds_read_b128 v[6:9], v151 offset:6592
	ds_read_b128 v[10:13], v151 offset:7200
	s_mov_b32 s3, 0xa0000
	ds_read_b128 v[110:113], v151 offset:7808
	s_waitcnt lgkmcnt(0)
	v_mfma_f32_16x16x32_f16 v[118:121], v[30:33], v[6:9], v[174:177]
	s_barrier
	v_sub_u32_e32 v245, v234, v243
	v_add_u32_e32 v246, 0xfffffdc0, v245
	v_min_u32_e32 v245, v245, v246
	v_add_u32_e32 v234, v242, v245
	v_sub_u32_e32 v245, v235, v243
	v_add_u32_e32 v246, 0xfffffdc0, v245
	v_min_u32_e32 v245, v245, v246
	v_add_u32_e32 v235, v242, v245
	v_sub_u32_e32 v245, v236, v243
	v_add_u32_e32 v246, 0xfffffdc0, v245
	v_min_u32_e32 v245, v245, v246
	v_add_u32_e32 v236, v242, v245
	v_sub_u32_e32 v245, v237, v243
	v_add_u32_e32 v246, 0xfffffdc0, v245
	v_min_u32_e32 v245, v245, v246
	v_add_u32_e32 v237, v242, v245
	v_sub_u32_e32 v245, v238, v243
	v_add_u32_e32 v246, 0xfffffdc0, v245
	v_min_u32_e32 v245, v245, v246
	v_add_u32_e32 v238, v242, v245
	v_sub_u32_e32 v245, v239, v243
	v_add_u32_e32 v246, 0xfffffdc0, v245
	v_min_u32_e32 v245, v245, v246
	v_add_u32_e32 v239, v242, v245
	v_sub_u32_e32 v245, v240, v243
	v_add_u32_e32 v246, 0xfffffdc0, v245
	v_min_u32_e32 v245, v245, v246
	v_add_u32_e32 v240, v242, v245
	v_sub_u32_e32 v245, v241, v243
	v_add_u32_e32 v246, 0xfffffdc0, v245
	v_min_u32_e32 v245, v245, v246
	v_add_u32_e32 v241, v242, v245
	v_mfma_f32_16x16x32_f16 v[174:177], v[18:21], v[6:9], v[194:197]
	v_add_co_u32_e32 v6, vcc, s3, v152
	s_mov_b32 s3, 0xa4000
	s_nop 0
	v_addc_co_u32_e32 v7, vcc, 0, v153, vcc
	global_load_dwordx4 v[34:37], v[6:7], off sc1
	global_load_dwordx4 v[46:49], v[6:7], off offset:256 sc1
	v_add_co_u32_e32 v6, vcc, s3, v152
	v_mfma_f32_16x16x32_f16 v[186:189], v[30:33], v[10:13], v[186:189]
	s_nop 0
	v_addc_co_u32_e32 v7, vcc, 0, v153, vcc
	v_mfma_f32_16x16x32_f16 v[194:197], v[18:21], v[10:13], v[202:205]
	global_load_dwordx4 v[10:13], v[6:7], off sc1
	s_nop 0
	global_load_dwordx4 v[6:9], v[6:7], off offset:256 sc1
	v_mfma_f32_16x16x32_f16 v[30:33], v[30:33], v[110:113], v[218:221]
	v_mfma_f32_16x16x32_f16 v[18:21], v[18:21], v[110:113], v[214:217]
	v_min_u32_e32 v110, 0x54, v154
	v_add_u32_e32 v154, 0x11152adc, v110
	ds_read_b128 v[110:113], v151 offset:0
	v_add_u32_e32 v157, 0x1600, v250
	s_waitcnt vmcnt(24) lgkmcnt(0)
	v_mfma_f32_16x16x32_f16 v[130:133], v[38:41], v[110:113], v[130:133]
	s_waitcnt vmcnt(23)
	v_mfma_f32_16x16x32_f16 v[202:205], v[42:45], v[110:113], v[226:229]
	v_min_u32_e32 v110, v157, v154
	global_load_dwordx4 v[110:113], v110, s[8:9] nt
	s_waitcnt vmcnt(21)
	v_cvt_pk_f16_f32 v61, v60, v61
	v_cvt_pk_f16_f32 v60, v58, v59
	ds_write_b16 v234, v60 offset:0
	ds_write_b16_d16_hi v235, v60 offset:0
	ds_write_b16 v236, v61 offset:0
	ds_write_b16_d16_hi v237, v61 offset:0
	ds_read_b128 v[58:61], v151 offset:608
	ds_read_b128 v[214:217], v151 offset:1216
	s_waitcnt lgkmcnt(1)
	v_mfma_f32_16x16x32_f16 v[142:145], v[38:41], v[58:61], v[142:145]
	v_mfma_f32_16x16x32_f16 v[158:161], v[42:45], v[58:61], v[158:161]
	s_waitcnt lgkmcnt(0)
	v_mfma_f32_16x16x32_f16 v[114:117], v[38:41], v[214:217], v[114:117]
	v_mfma_f32_16x16x32_f16 v[178:181], v[42:45], v[214:217], v[178:181]
	ds_read_b128 v[58:61], v151 offset:1824
	ds_read_b128 v[214:217], v151 offset:2432
	s_waitcnt lgkmcnt(1)
	v_mfma_f32_16x16x32_f16 v[182:185], v[38:41], v[58:61], v[182:185]
	v_mfma_f32_16x16x32_f16 v[198:201], v[42:45], v[58:61], v[198:201]
	s_waitcnt lgkmcnt(0)
	v_mfma_f32_16x16x32_f16 v[134:137], v[38:41], v[214:217], v[134:137]
	v_mfma_f32_16x16x32_f16 v[146:149], v[42:45], v[214:217], v[146:149]
	v_add_u32_e32 v58, 0x17c40, v251
	v_min_u32_e32 v58, v58, v154
	global_load_dwordx4 v[58:61], v58, s[8:9] nt
	s_waitcnt vmcnt(21)
	v_cvt_pk_f16_f32 v73, v72, v73
	v_cvt_pk_f16_f32 v72, v70, v71
	ds_write_b16 v238, v72 offset:608
	ds_write_b16_d16_hi v239, v72 offset:608
	ds_write_b16 v240, v73 offset:608
	ds_write_b16_d16_hi v241, v73 offset:608
	ds_read_b128 v[70:73], v151 offset:3040
	ds_read_b128 v[214:217], v151 offset:4864
	s_waitcnt lgkmcnt(1)
	v_mfma_f32_16x16x32_f16 v[206:209], v[38:41], v[70:73], v[206:209]
	v_mfma_f32_16x16x32_f16 v[122:125], v[42:45], v[70:73], v[122:125]
	ds_read_b128 v[70:73], v151 offset:3648
	ds_read_b128 v[218:221], v151 offset:4256
	s_waitcnt lgkmcnt(1)
	v_mfma_f32_16x16x32_f16 v[210:213], v[38:41], v[70:73], v[210:213]
	v_mfma_f32_16x16x32_f16 v[190:193], v[42:45], v[70:73], v[190:193]
	s_waitcnt lgkmcnt(0)
	v_mfma_f32_16x16x32_f16 v[166:169], v[38:41], v[218:221], v[166:169]
	v_mfma_f32_16x16x32_f16 v[162:165], v[42:45], v[218:221], v[162:165]
	v_mfma_f32_16x16x32_f16 v[218:221], v[38:41], v[214:217], v[222:225]
	v_mfma_f32_16x16x32_f16 v[138:141], v[42:45], v[214:217], v[138:141]
	v_add_u32_e32 v70, 0x2e280, v250
	v_min_u32_e32 v70, v70, v154
	global_load_dwordx4 v[70:73], v70, s[8:9] nt
	s_waitcnt vmcnt(21)
	v_cvt_pk_f16_f32 v77, v76, v77
	v_cvt_pk_f16_f32 v76, v74, v75
	ds_write_b16 v234, v76 offset:1216
	ds_write_b16_d16_hi v235, v76 offset:1216
	ds_write_b16 v236, v77 offset:1216
	ds_write_b16_d16_hi v237, v77 offset:1216
	ds_read_b128 v[74:77], v151 offset:5472
	ds_read_b128 v[214:217], v151 offset:6080
	s_waitcnt lgkmcnt(1)
	v_mfma_f32_16x16x32_f16 v[170:173], v[38:41], v[74:77], v[170:173]
	v_mfma_f32_16x16x32_f16 v[126:129], v[42:45], v[74:77], v[126:129]
	s_waitcnt lgkmcnt(0)
	v_mfma_f32_16x16x32_f16 v[118:121], v[38:41], v[214:217], v[118:121]
	v_mfma_f32_16x16x32_f16 v[174:177], v[42:45], v[214:217], v[174:177]
	ds_read_b128 v[74:77], v151 offset:6688
	ds_read_b128 v[214:217], v151 offset:7296
	s_waitcnt lgkmcnt(1)
	v_mfma_f32_16x16x32_f16 v[186:189], v[38:41], v[74:77], v[186:189]
	v_mfma_f32_16x16x32_f16 v[194:197], v[42:45], v[74:77], v[194:197]
	s_waitcnt lgkmcnt(0)
	v_mfma_f32_16x16x32_f16 v[30:33], v[38:41], v[214:217], v[30:33]
	v_mfma_f32_16x16x32_f16 v[214:217], v[42:45], v[214:217], v[18:21]
	s_nop 2
	v_add_u32_e32 v18, 0x448c0, v251
	v_min_u32_e32 v18, v18, v154
	global_load_dwordx4 v[42:45], v18, s[8:9] nt
	s_waitcnt vmcnt(21)
	v_cvt_pk_f16_f32 v19, v80, v81
	v_cvt_pk_f16_f32 v18, v78, v79
	ds_write_b16 v238, v18 offset:1824
	ds_write_b16_d16_hi v239, v18 offset:1824
	ds_write_b16 v240, v19 offset:1824
	ds_write_b16_d16_hi v241, v19 offset:1824
	ds_read_b128 v[18:21], v151 offset:64
	ds_read_b128 v[38:41], v151 offset:672
	s_waitcnt lgkmcnt(1)
	v_mfma_f32_16x16x32_f16 v[130:133], v[22:25], v[18:21], v[130:133]
	v_mfma_f32_16x16x32_f16 v[202:205], v[2:5], v[18:21], v[202:205]
	s_waitcnt lgkmcnt(0)
	v_mfma_f32_16x16x32_f16 v[142:145], v[22:25], v[38:41], v[142:145]
	v_mfma_f32_16x16x32_f16 v[158:161], v[2:5], v[38:41], v[158:161]
	ds_read_b128 v[18:21], v151 offset:1280
	ds_read_b128 v[38:41], v151 offset:1888
	s_waitcnt lgkmcnt(1)
	v_mfma_f32_16x16x32_f16 v[114:117], v[22:25], v[18:21], v[114:117]
	v_mfma_f32_16x16x32_f16 v[178:181], v[2:5], v[18:21], v[178:181]
	s_waitcnt lgkmcnt(0)
	v_mfma_f32_16x16x32_f16 v[182:185], v[22:25], v[38:41], v[182:185]
	v_mfma_f32_16x16x32_f16 v[198:201], v[2:5], v[38:41], v[198:201]
	v_add_u32_e32 v18, 0x5af00, v250
	v_min_u32_e32 v18, v18, v154
	global_load_dwordx4 v[74:77], v18, s[8:9] nt
	s_waitcnt vmcnt(21)
	v_cvt_pk_f16_f32 v19, v84, v85
	v_cvt_pk_f16_f32 v18, v82, v83
	ds_write_b16 v234, v18 offset:2432
	ds_write_b16_d16_hi v235, v18 offset:2432
	ds_write_b16 v236, v19 offset:2432
	ds_write_b16_d16_hi v237, v19 offset:2432
	ds_read_b128 v[18:21], v151 offset:2496
	ds_read_b128 v[38:41], v151 offset:3104
	s_waitcnt lgkmcnt(1)
	v_mfma_f32_16x16x32_f16 v[134:137], v[22:25], v[18:21], v[134:137]
	v_mfma_f32_16x16x32_f16 v[146:149], v[2:5], v[18:21], v[146:149]
	s_waitcnt lgkmcnt(0)
	v_mfma_f32_16x16x32_f16 v[206:209], v[22:25], v[38:41], v[206:209]
	v_mfma_f32_16x16x32_f16 v[122:125], v[2:5], v[38:41], v[122:125]
	ds_read_b128 v[18:21], v151 offset:3712
	ds_read_b128 v[38:41], v151 offset:4320
	s_waitcnt lgkmcnt(1)
	v_mfma_f32_16x16x32_f16 v[210:213], v[22:25], v[18:21], v[210:213]
	v_mfma_f32_16x16x32_f16 v[190:193], v[2:5], v[18:21], v[190:193]
	s_waitcnt lgkmcnt(0)
	v_mfma_f32_16x16x32_f16 v[166:169], v[22:25], v[38:41], v[166:169]
	v_mfma_f32_16x16x32_f16 v[162:165], v[2:5], v[38:41], v[162:165]
	v_add_u32_e32 v18, 0x71540, v251
	v_min_u32_e32 v18, v18, v154
	global_load_dwordx4 v[78:81], v18, s[8:9] nt
	s_waitcnt vmcnt(21)
	v_cvt_pk_f16_f32 v19, v88, v89
	v_cvt_pk_f16_f32 v18, v86, v87
	ds_write_b16 v238, v18 offset:3040
	ds_write_b16_d16_hi v239, v18 offset:3040
	ds_write_b16 v240, v19 offset:3040
	ds_write_b16_d16_hi v241, v19 offset:3040
	ds_read_b128 v[18:21], v151 offset:4928
	ds_read_b128 v[38:41], v151 offset:5536
	s_waitcnt lgkmcnt(1)
	v_mfma_f32_16x16x32_f16 v[218:221], v[22:25], v[18:21], v[218:221]
	v_mfma_f32_16x16x32_f16 v[138:141], v[2:5], v[18:21], v[138:141]
	s_waitcnt lgkmcnt(0)
	v_mfma_f32_16x16x32_f16 v[170:173], v[22:25], v[38:41], v[170:173]
	v_mfma_f32_16x16x32_f16 v[126:129], v[2:5], v[38:41], v[126:129]
	ds_read_b128 v[18:21], v151 offset:6144
	ds_read_b128 v[38:41], v151 offset:6752
	s_waitcnt lgkmcnt(1)
	v_mfma_f32_16x16x32_f16 v[118:121], v[22:25], v[18:21], v[118:121]
	v_mfma_f32_16x16x32_f16 v[174:177], v[2:5], v[18:21], v[174:177]
	s_waitcnt lgkmcnt(0)
	v_mfma_f32_16x16x32_f16 v[186:189], v[22:25], v[38:41], v[186:189]
	v_mfma_f32_16x16x32_f16 v[194:197], v[2:5], v[38:41], v[194:197]
	v_add_u32_e32 v18, 0x87b80, v250
	v_min_u32_e32 v18, v18, v154
	global_load_dwordx4 v[82:85], v18, s[8:9] nt
	s_waitcnt vmcnt(21)
	v_cvt_pk_f16_f32 v19, v92, v93
	v_cvt_pk_f16_f32 v18, v90, v91
	ds_write_b16 v234, v18 offset:3648
	ds_write_b16_d16_hi v235, v18 offset:3648
	ds_write_b16 v236, v19 offset:3648
	ds_write_b16_d16_hi v237, v19 offset:3648
	ds_read_b128 v[86:89], v151 offset:7360
	s_mov_b32 s3, 0xa8000
	v_add_co_u32_e32 v18, vcc, s3, v152
	s_mov_b32 s3, 0xac000
	s_nop 0
	v_addc_co_u32_e32 v19, vcc, 0, v153, vcc
	s_waitcnt lgkmcnt(0)
	v_mfma_f32_16x16x32_f16 v[222:225], v[22:25], v[86:89], v[30:33]
	s_nop 2
	global_load_dwordx4 v[30:33], v[18:19], off sc1
	global_load_dwordx4 v[38:41], v[18:19], off offset:256 sc1
	v_add_co_u32_e32 v18, vcc, s3, v152
	v_mfma_f32_16x16x32_f16 v[2:5], v[2:5], v[86:89], v[214:217]
	s_nop 0
	v_addc_co_u32_e32 v19, vcc, 0, v153, vcc
	global_load_dwordx4 v[22:25], v[18:19], off sc1
	s_nop 0
	global_load_dwordx4 v[18:21], v[18:19], off offset:256 sc1
	ds_read_b128 v[86:89], v151 offset:128
	ds_read_b128 v[90:93], v151 offset:736
	s_waitcnt vmcnt(24) lgkmcnt(1)
	v_mfma_f32_16x16x32_f16 v[130:133], v[50:53], v[86:89], v[130:133]
	s_waitcnt vmcnt(23)
	v_mfma_f32_16x16x32_f16 v[202:205], v[54:57], v[86:89], v[202:205]
	ds_read_b128 v[86:89], v151 offset:1344
	s_waitcnt lgkmcnt(0)
	v_mfma_f32_16x16x32_f16 v[114:117], v[50:53], v[86:89], v[114:117]
	v_mfma_f32_16x16x32_f16 v[142:145], v[50:53], v[90:93], v[142:145]
	v_mfma_f32_16x16x32_f16 v[158:161], v[54:57], v[90:93], v[158:161]
	v_mfma_f32_16x16x32_f16 v[178:181], v[54:57], v[86:89], v[178:181]
	v_add_u32_e32 v86, 0x9e1c0, v251
	v_min_u32_e32 v86, v86, v154
	global_load_dwordx4 v[86:89], v86, s[8:9] nt
	s_waitcnt vmcnt(21)
	v_cvt_pk_f16_f32 v91, v96, v97
	v_cvt_pk_f16_f32 v90, v94, v95
	ds_write_b16 v238, v90 offset:4256
	ds_write_b16_d16_hi v239, v90 offset:4256
	ds_write_b16 v240, v91 offset:4256
	ds_write_b16_d16_hi v241, v91 offset:4256
	ds_read_b128 v[90:93], v151 offset:1952
	ds_read_b128 v[94:97], v151 offset:2560
	s_waitcnt lgkmcnt(1)
	v_mfma_f32_16x16x32_f16 v[182:185], v[50:53], v[90:93], v[182:185]
	v_mfma_f32_16x16x32_f16 v[198:201], v[54:57], v[90:93], v[198:201]
	s_waitcnt lgkmcnt(0)
	v_mfma_f32_16x16x32_f16 v[134:137], v[50:53], v[94:97], v[134:137]
	v_mfma_f32_16x16x32_f16 v[146:149], v[54:57], v[94:97], v[146:149]
	ds_read_b128 v[90:93], v151 offset:3168
	ds_read_b128 v[94:97], v151 offset:3776
	s_waitcnt lgkmcnt(1)
	v_mfma_f32_16x16x32_f16 v[206:209], v[50:53], v[90:93], v[206:209]
	v_mfma_f32_16x16x32_f16 v[122:125], v[54:57], v[90:93], v[122:125]
	s_waitcnt lgkmcnt(0)
	v_mfma_f32_16x16x32_f16 v[210:213], v[50:53], v[94:97], v[210:213]
	v_mfma_f32_16x16x32_f16 v[190:193], v[54:57], v[94:97], v[190:193]
	v_add_u32_e32 v90, 0xb4800, v250
	v_min_u32_e32 v90, v90, v154
	global_load_dwordx4 v[90:93], v90, s[8:9] nt
	s_waitcnt vmcnt(21)
	v_cvt_pk_f16_f32 v95, v100, v101
	v_cvt_pk_f16_f32 v94, v98, v99
	ds_write_b16 v234, v94 offset:4864
	ds_write_b16_d16_hi v235, v94 offset:4864
	ds_write_b16 v236, v95 offset:4864
	ds_write_b16_d16_hi v237, v95 offset:4864
	ds_read_b128 v[94:97], v151 offset:4384
	ds_read_b128 v[98:101], v151 offset:6208
	s_waitcnt lgkmcnt(1)
	v_mfma_f32_16x16x32_f16 v[166:169], v[50:53], v[94:97], v[166:169]
	v_mfma_f32_16x16x32_f16 v[162:165], v[54:57], v[94:97], v[162:165]
	ds_read_b128 v[94:97], v151 offset:4992
	ds_read_b128 v[214:217], v151 offset:5600
	s_waitcnt lgkmcnt(1)
	v_mfma_f32_16x16x32_f16 v[218:221], v[50:53], v[94:97], v[218:221]
	v_mfma_f32_16x16x32_f16 v[138:141], v[54:57], v[94:97], v[138:141]
	s_waitcnt lgkmcnt(0)
	v_mfma_f32_16x16x32_f16 v[170:173], v[50:53], v[214:217], v[170:173]
	v_mfma_f32_16x16x32_f16 v[126:129], v[54:57], v[214:217], v[126:129]
	v_mfma_f32_16x16x32_f16 v[118:121], v[50:53], v[98:101], v[118:121]
	v_mfma_f32_16x16x32_f16 v[174:177], v[54:57], v[98:101], v[174:177]
	v_add_u32_e32 v94, 0xcae40, v251
	v_min_u32_e32 v94, v94, v154
	global_load_dwordx4 v[94:97], v94, s[8:9] nt
	s_waitcnt vmcnt(21)
	v_cvt_pk_f16_f32 v99, v104, v105
	v_cvt_pk_f16_f32 v98, v102, v103
	ds_write_b16 v238, v98 offset:5472
	ds_write_b16_d16_hi v239, v98 offset:5472
	ds_write_b16 v240, v99 offset:5472
	ds_write_b16_d16_hi v241, v99 offset:5472
	ds_read_b128 v[98:101], v151 offset:6816
	ds_read_b128 v[102:105], v151 offset:7424
	s_waitcnt lgkmcnt(1)
	v_mfma_f32_16x16x32_f16 v[186:189], v[50:53], v[98:101], v[186:189]
	s_waitcnt lgkmcnt(0)
	v_mfma_f32_16x16x32_f16 v[214:217], v[50:53], v[102:105], v[222:225]
	v_mfma_f32_16x16x32_f16 v[102:105], v[54:57], v[102:105], v[2:5]
	s_nop 2
	ds_read_b128 v[2:5], v151 offset:192
	ds_read_b128 v[50:53], v151 offset:800
	v_mfma_f32_16x16x32_f16 v[194:197], v[54:57], v[98:101], v[194:197]
	s_waitcnt lgkmcnt(1)
	v_mfma_f32_16x16x32_f16 v[130:133], v[26:29], v[2:5], v[130:133]
	v_mfma_f32_16x16x32_f16 v[202:205], v[14:17], v[2:5], v[202:205]
	s_waitcnt lgkmcnt(0)
	v_mfma_f32_16x16x32_f16 v[142:145], v[26:29], v[50:53], v[142:145]
	v_mfma_f32_16x16x32_f16 v[158:161], v[14:17], v[50:53], v[158:161]
	v_add_u32_e32 v2, 0xe1480, v250
	v_min_u32_e32 v2, v2, v154
	global_load_dwordx4 v[98:101], v2, s[8:9] nt
	s_waitcnt vmcnt(21)
	v_cvt_pk_f16_f32 v3, v64, v65
	v_cvt_pk_f16_f32 v2, v62, v63
	ds_write_b16 v234, v2 offset:6080
	ds_write_b16_d16_hi v235, v2 offset:6080
	ds_write_b16 v236, v3 offset:6080
	ds_write_b16_d16_hi v237, v3 offset:6080
	ds_read_b128 v[2:5], v151 offset:1408
	ds_read_b128 v[50:53], v151 offset:2016
	s_waitcnt lgkmcnt(1)
	v_mfma_f32_16x16x32_f16 v[222:225], v[26:29], v[2:5], v[114:117]
	v_mfma_f32_16x16x32_f16 v[178:181], v[14:17], v[2:5], v[178:181]
	s_waitcnt lgkmcnt(0)
	v_mfma_f32_16x16x32_f16 v[182:185], v[26:29], v[50:53], v[182:185]
	v_mfma_f32_16x16x32_f16 v[198:201], v[14:17], v[50:53], v[198:201]
	ds_read_b128 v[2:5], v151 offset:2624
	ds_read_b128 v[50:53], v151 offset:3232
	s_waitcnt lgkmcnt(1)
	v_mfma_f32_16x16x32_f16 v[134:137], v[26:29], v[2:5], v[134:137]
	v_mfma_f32_16x16x32_f16 v[146:149], v[14:17], v[2:5], v[146:149]
	s_waitcnt lgkmcnt(0)
	v_mfma_f32_16x16x32_f16 v[206:209], v[26:29], v[50:53], v[206:209]
	v_mfma_f32_16x16x32_f16 v[122:125], v[14:17], v[50:53], v[122:125]
	v_add_u32_e32 v2, 0xf7ac0, v251
	v_min_u32_e32 v2, v2, v154
	global_load_dwordx4 v[62:65], v2, s[8:9] nt
	s_waitcnt vmcnt(21)
	v_cvt_pk_f16_f32 v3, v68, v69
	v_cvt_pk_f16_f32 v2, v66, v67
	ds_write_b16 v238, v2 offset:6688
	ds_write_b16_d16_hi v239, v2 offset:6688
	ds_write_b16 v240, v3 offset:6688
	ds_write_b16_d16_hi v241, v3 offset:6688
	ds_read_b128 v[2:5], v151 offset:3840
	ds_read_b128 v[50:53], v151 offset:4448
	s_waitcnt lgkmcnt(1)
	v_mfma_f32_16x16x32_f16 v[210:213], v[26:29], v[2:5], v[210:213]
	v_mfma_f32_16x16x32_f16 v[190:193], v[14:17], v[2:5], v[190:193]
	s_waitcnt lgkmcnt(0)
	v_mfma_f32_16x16x32_f16 v[166:169], v[26:29], v[50:53], v[166:169]
	v_mfma_f32_16x16x32_f16 v[162:165], v[14:17], v[50:53], v[162:165]
	ds_read_b128 v[2:5], v151 offset:5056
	ds_read_b128 v[50:53], v151 offset:5664
	s_waitcnt lgkmcnt(1)
	v_mfma_f32_16x16x32_f16 v[218:221], v[26:29], v[2:5], v[218:221]
	v_mfma_f32_16x16x32_f16 v[138:141], v[14:17], v[2:5], v[138:141]
	s_waitcnt lgkmcnt(0)
	v_mfma_f32_16x16x32_f16 v[170:173], v[26:29], v[50:53], v[170:173]
	v_mfma_f32_16x16x32_f16 v[126:129], v[14:17], v[50:53], v[126:129]
	v_add_u32_e32 v2, 0x10e100, v250
	v_min_u32_e32 v2, v2, v154
	v_cndmask_b32_e64 v2, 0, v2, s[0:1]
	global_load_dwordx4 v[66:69], v2, s[8:9] nt
	s_waitcnt vmcnt(21)
	v_cvt_pk_f16_f32 v3, v108, v109
	v_cvt_pk_f16_f32 v2, v106, v107
	ds_write_b16 v234, v2 offset:7296
	ds_write_b16_d16_hi v235, v2 offset:7296
	ds_write_b16 v236, v3 offset:7296
	ds_write_b16_d16_hi v237, v3 offset:7296
	ds_read_b128 v[2:5], v151 offset:6272
	ds_read_b128 v[50:53], v151 offset:6880
	ds_read_b128 v[106:109], v151 offset:7488
	s_mov_b32 s3, 0xb0000
	s_waitcnt lgkmcnt(0)
	v_mfma_f32_16x16x32_f16 v[116:119], v[26:29], v[2:5], v[118:121]
	s_barrier
	v_sub_u32_e32 v245, v234, v243
	v_add_u32_e32 v246, 0xfffffdc0, v245
	v_min_u32_e32 v245, v245, v246
	v_add_u32_e32 v234, v242, v245
	v_sub_u32_e32 v245, v235, v243
	v_add_u32_e32 v246, 0xfffffdc0, v245
	v_min_u32_e32 v245, v245, v246
	v_add_u32_e32 v235, v242, v245
	v_sub_u32_e32 v245, v236, v243
	v_add_u32_e32 v246, 0xfffffdc0, v245
	v_min_u32_e32 v245, v245, v246
	v_add_u32_e32 v236, v242, v245
	v_sub_u32_e32 v245, v237, v243
	v_add_u32_e32 v246, 0xfffffdc0, v245
	v_min_u32_e32 v245, v245, v246
	v_add_u32_e32 v237, v242, v245
	v_sub_u32_e32 v245, v238, v243
	v_add_u32_e32 v246, 0xfffffdc0, v245
	v_min_u32_e32 v245, v245, v246
	v_add_u32_e32 v238, v242, v245
	v_sub_u32_e32 v245, v239, v243
	v_add_u32_e32 v246, 0xfffffdc0, v245
	v_min_u32_e32 v245, v245, v246
	v_add_u32_e32 v239, v242, v245
	v_sub_u32_e32 v245, v240, v243
	v_add_u32_e32 v246, 0xfffffdc0, v245
	v_min_u32_e32 v245, v245, v246
	v_add_u32_e32 v240, v242, v245
	v_sub_u32_e32 v245, v241, v243
	v_add_u32_e32 v246, 0xfffffdc0, v245
	v_min_u32_e32 v245, v245, v246
	v_add_u32_e32 v241, v242, v245
	v_mfma_f32_16x16x32_f16 v[174:177], v[14:17], v[2:5], v[174:177]
	v_add_co_u32_e32 v2, vcc, s3, v152
	s_nop 1
	v_addc_co_u32_e32 v3, vcc, 0, v153, vcc
	v_mfma_f32_16x16x32_f16 v[186:189], v[26:29], v[50:53], v[186:189]
	v_mfma_f32_16x16x32_f16 v[214:217], v[26:29], v[106:109], v[214:217]
	v_add_co_u32_e32 v26, vcc, s2, v152
	s_nop 1
	v_addc_co_u32_e32 v27, vcc, 0, v153, vcc
	v_mfma_f32_16x16x32_f16 v[194:197], v[14:17], v[50:53], v[194:197]
	global_load_dwordx4 v[50:53], v[2:3], off sc1
	global_load_dwordx4 v[54:57], v[2:3], off offset:256 sc1
	s_nop 0
	global_load_dwordx4 v[2:5], v[26:27], off sc1
	s_nop 0
	global_load_dwordx4 v[26:29], v[26:27], off offset:256 sc1
	v_mfma_f32_16x16x32_f16 v[14:17], v[14:17], v[106:109], v[102:105]
	v_mov_b32_e32 v114, 0
	s_nop 1
	ds_read_b128 v[102:105], v151 offset:256
	v_mov_b32_e32 v115, 0
	v_add_u32_e32 v106, 0x1800, v150
	s_waitcnt vmcnt(24) lgkmcnt(0)
	v_mfma_f32_16x16x32_f16 v[130:133], v[34:37], v[102:105], v[130:133]
	s_waitcnt vmcnt(23)
	v_mfma_f32_16x16x32_f16 v[202:205], v[46:49], v[102:105], v[202:205]
	v_min_u32_e32 v102, v106, v114
	global_load_dwordx4 v[102:105], v102, s[8:9] nt
	s_waitcnt vmcnt(21)
	v_cvt_pk_f16_f32 v107, v112, v113
	v_cvt_pk_f16_f32 v106, v110, v111
	ds_write_b16 v234, v106 offset:0
	ds_write_b16_d16_hi v235, v106 offset:0
	ds_write_b16 v236, v107 offset:0
	ds_write_b16_d16_hi v237, v107 offset:0
	ds_read_b128 v[106:109], v151 offset:864
	ds_read_b128 v[110:113], v151 offset:1472
	s_waitcnt lgkmcnt(1)
	v_mfma_f32_16x16x32_f16 v[142:145], v[34:37], v[106:109], v[142:145]
	v_mfma_f32_16x16x32_f16 v[158:161], v[46:49], v[106:109], v[158:161]
	s_waitcnt lgkmcnt(0)
	v_mfma_f32_16x16x32_f16 v[222:225], v[34:37], v[110:113], v[222:225]
	v_mfma_f32_16x16x32_f16 v[110:113], v[46:49], v[110:113], v[178:181]
	ds_read_b128 v[106:109], v151 offset:2080
	s_nop 1
	ds_read_b128 v[178:181], v151 offset:2688
	s_waitcnt lgkmcnt(1)
	v_mfma_f32_16x16x32_f16 v[182:185], v[34:37], v[106:109], v[182:185]
	v_mfma_f32_16x16x32_f16 v[198:201], v[46:49], v[106:109], v[198:201]
	s_waitcnt lgkmcnt(0)
	v_mfma_f32_16x16x32_f16 v[134:137], v[34:37], v[178:181], v[134:137]
	v_mfma_f32_16x16x32_f16 v[146:149], v[46:49], v[178:181], v[146:149]
	v_add_u32_e32 v106, 0x17e40, v244
	v_min_u32_e32 v106, v106, v114
	global_load_dwordx4 v[106:109], v106, s[8:9] nt
	s_waitcnt vmcnt(21)
	v_cvt_pk_f16_f32 v61, v60, v61
	v_cvt_pk_f16_f32 v60, v58, v59
	ds_write_b16 v238, v60 offset:608
	ds_write_b16_d16_hi v239, v60 offset:608
	ds_write_b16 v240, v61 offset:608
	ds_write_b16_d16_hi v241, v61 offset:608
	ds_read_b128 v[58:61], v151 offset:3296
	ds_read_b128 v[178:181], v151 offset:5120
	s_waitcnt lgkmcnt(1)
	v_mfma_f32_16x16x32_f16 v[206:209], v[34:37], v[58:61], v[206:209]
	v_mfma_f32_16x16x32_f16 v[120:123], v[46:49], v[58:61], v[122:125]
	ds_read_b128 v[58:61], v151 offset:3904
	ds_read_b128 v[226:229], v151 offset:4512
	s_waitcnt lgkmcnt(1)
	v_mfma_f32_16x16x32_f16 v[210:213], v[34:37], v[58:61], v[210:213]
	v_mfma_f32_16x16x32_f16 v[190:193], v[46:49], v[58:61], v[190:193]
	s_waitcnt lgkmcnt(0)
	v_mfma_f32_16x16x32_f16 v[166:169], v[34:37], v[226:229], v[166:169]
	v_mfma_f32_16x16x32_f16 v[162:165], v[46:49], v[226:229], v[162:165]
	v_mfma_f32_16x16x32_f16 v[218:221], v[34:37], v[178:181], v[218:221]
	v_mfma_f32_16x16x32_f16 v[138:141], v[46:49], v[178:181], v[138:141]
	v_add_u32_e32 v58, 0x2e480, v150
	v_min_u32_e32 v58, v58, v114
	global_load_dwordx4 v[58:61], v58, s[8:9] nt
	s_waitcnt vmcnt(21)
	v_cvt_pk_f16_f32 v73, v72, v73
	v_cvt_pk_f16_f32 v72, v70, v71
	ds_write_b16 v234, v72 offset:1216
	ds_write_b16_d16_hi v235, v72 offset:1216
	ds_write_b16 v236, v73 offset:1216
	ds_write_b16_d16_hi v237, v73 offset:1216
	ds_read_b128 v[70:73], v151 offset:5728
	ds_read_b128 v[178:181], v151 offset:6336
	s_waitcnt lgkmcnt(1)
	v_mfma_f32_16x16x32_f16 v[170:173], v[34:37], v[70:73], v[170:173]
	v_mfma_f32_16x16x32_f16 v[124:127], v[46:49], v[70:73], v[126:129]
	s_waitcnt lgkmcnt(0)
	v_mfma_f32_16x16x32_f16 v[116:119], v[34:37], v[178:181], v[116:119]
	v_mfma_f32_16x16x32_f16 v[174:177], v[46:49], v[178:181], v[174:177]
	ds_read_b128 v[70:73], v151 offset:6944
	ds_read_b128 v[178:181], v151 offset:7552
	s_waitcnt lgkmcnt(1)
	v_mfma_f32_16x16x32_f16 v[186:189], v[34:37], v[70:73], v[186:189]
	v_mfma_f32_16x16x32_f16 v[194:197], v[46:49], v[70:73], v[194:197]
	s_waitcnt lgkmcnt(0)
	v_mfma_f32_16x16x32_f16 v[214:217], v[34:37], v[178:181], v[214:217]
	v_mfma_f32_16x16x32_f16 v[178:181], v[46:49], v[178:181], v[14:17]
	s_nop 2
	v_add_u32_e32 v14, 0x44ac0, v244
	v_min_u32_e32 v14, v14, v114
	global_load_dwordx4 v[34:37], v14, s[8:9] nt
	s_waitcnt vmcnt(21)
	v_cvt_pk_f16_f32 v15, v44, v45
	v_cvt_pk_f16_f32 v14, v42, v43
	ds_write_b16 v238, v14 offset:1824
	ds_write_b16_d16_hi v239, v14 offset:1824
	ds_write_b16 v240, v15 offset:1824
	ds_write_b16_d16_hi v241, v15 offset:1824
	ds_read_b128 v[14:17], v151 offset:320
	ds_read_b128 v[42:45], v151 offset:928
	s_waitcnt lgkmcnt(1)
	v_mfma_f32_16x16x32_f16 v[128:131], v[10:13], v[14:17], v[130:133]
	v_mfma_f32_16x16x32_f16 v[202:205], v[6:9], v[14:17], v[202:205]
	s_waitcnt lgkmcnt(0)
	v_mfma_f32_16x16x32_f16 v[142:145], v[10:13], v[42:45], v[142:145]
	v_mfma_f32_16x16x32_f16 v[158:161], v[6:9], v[42:45], v[158:161]
	ds_read_b128 v[14:17], v151 offset:1536
	ds_read_b128 v[42:45], v151 offset:2144
	s_waitcnt lgkmcnt(1)
	v_mfma_f32_16x16x32_f16 v[222:225], v[10:13], v[14:17], v[222:225]
	v_mfma_f32_16x16x32_f16 v[110:113], v[6:9], v[14:17], v[110:113]
	s_waitcnt lgkmcnt(0)
	v_mfma_f32_16x16x32_f16 v[182:185], v[10:13], v[42:45], v[182:185]
	v_mfma_f32_16x16x32_f16 v[198:201], v[6:9], v[42:45], v[198:201]
	v_add_u32_e32 v14, 0x5b100, v150
	v_min_u32_e32 v14, v14, v114
	global_load_dwordx4 v[70:73], v14, s[8:9] nt
	s_waitcnt vmcnt(21)
	v_cvt_pk_f16_f32 v15, v76, v77
	v_cvt_pk_f16_f32 v14, v74, v75
	ds_write_b16 v234, v14 offset:2432
	ds_write_b16_d16_hi v235, v14 offset:2432
	ds_write_b16 v236, v15 offset:2432
	ds_write_b16_d16_hi v237, v15 offset:2432
	ds_read_b128 v[14:17], v151 offset:2752
	ds_read_b128 v[42:45], v151 offset:3360
	s_waitcnt lgkmcnt(1)
	v_mfma_f32_16x16x32_f16 v[132:135], v[10:13], v[14:17], v[134:137]
	v_mfma_f32_16x16x32_f16 v[146:149], v[6:9], v[14:17], v[146:149]
	s_waitcnt lgkmcnt(0)
	v_mfma_f32_16x16x32_f16 v[206:209], v[10:13], v[42:45], v[206:209]
	v_mfma_f32_16x16x32_f16 v[120:123], v[6:9], v[42:45], v[120:123]
	ds_read_b128 v[14:17], v151 offset:3968
	ds_read_b128 v[42:45], v151 offset:4576
	s_waitcnt lgkmcnt(1)
	v_mfma_f32_16x16x32_f16 v[210:213], v[10:13], v[14:17], v[210:213]
	v_mfma_f32_16x16x32_f16 v[190:193], v[6:9], v[14:17], v[190:193]
	s_waitcnt lgkmcnt(0)
	v_mfma_f32_16x16x32_f16 v[166:169], v[10:13], v[42:45], v[166:169]
	v_mfma_f32_16x16x32_f16 v[162:165], v[6:9], v[42:45], v[162:165]
	v_add_u32_e32 v14, 0x71740, v244
	v_min_u32_e32 v14, v14, v114
	global_load_dwordx4 v[74:77], v14, s[8:9] nt
	s_waitcnt vmcnt(21)
	v_cvt_pk_f16_f32 v15, v80, v81
	v_cvt_pk_f16_f32 v14, v78, v79
	ds_write_b16 v238, v14 offset:3040
	ds_write_b16_d16_hi v239, v14 offset:3040
	ds_write_b16 v240, v15 offset:3040
	ds_write_b16_d16_hi v241, v15 offset:3040
	ds_read_b128 v[14:17], v151 offset:5184
	ds_read_b128 v[42:45], v151 offset:5792
	s_waitcnt lgkmcnt(1)
	v_mfma_f32_16x16x32_f16 v[218:221], v[10:13], v[14:17], v[218:221]
	v_mfma_f32_16x16x32_f16 v[136:139], v[6:9], v[14:17], v[138:141]
	s_waitcnt lgkmcnt(0)
	v_mfma_f32_16x16x32_f16 v[170:173], v[10:13], v[42:45], v[170:173]
	v_mfma_f32_16x16x32_f16 v[124:127], v[6:9], v[42:45], v[124:127]
	ds_read_b128 v[14:17], v151 offset:6400
	ds_read_b128 v[42:45], v151 offset:7008
	s_waitcnt lgkmcnt(1)
	v_mfma_f32_16x16x32_f16 v[116:119], v[10:13], v[14:17], v[116:119]
	v_mfma_f32_16x16x32_f16 v[174:177], v[6:9], v[14:17], v[174:177]
	s_waitcnt lgkmcnt(0)
	v_mfma_f32_16x16x32_f16 v[186:189], v[10:13], v[42:45], v[186:189]
	v_mfma_f32_16x16x32_f16 v[194:197], v[6:9], v[42:45], v[194:197]
	v_add_u32_e32 v14, 0x87d80, v150
	v_min_u32_e32 v14, v14, v114
	global_load_dwordx4 v[78:81], v14, s[8:9] nt
	s_waitcnt vmcnt(21)
	v_cvt_pk_f16_f32 v15, v84, v85
	v_cvt_pk_f16_f32 v14, v82, v83
	ds_write_b16 v234, v14 offset:3648
	ds_write_b16_d16_hi v235, v14 offset:3648
	ds_write_b16 v236, v15 offset:3648
	ds_write_b16_d16_hi v237, v15 offset:3648
	ds_read_b128 v[82:85], v151 offset:7616
	s_mov_b32 s2, 0xb8000
	v_add_co_u32_e32 v14, vcc, s2, v152
	s_mov_b32 s2, 0xbc000
	s_nop 0
	v_addc_co_u32_e32 v15, vcc, 0, v153, vcc
	v_add_co_u32_e32 v42, vcc, s2, v152
	s_waitcnt lgkmcnt(0)
	v_mfma_f32_16x16x32_f16 v[214:217], v[10:13], v[82:85], v[214:217]
	v_addc_co_u32_e32 v43, vcc, 0, v153, vcc
	global_load_dwordx4 v[10:13], v[14:15], off sc1
	s_nop 0
	global_load_dwordx4 v[14:17], v[14:15], off offset:256 sc1
	s_nop 0
	global_load_dwordx4 v[46:49], v[42:43], off sc1
	s_nop 0
	global_load_dwordx4 v[42:45], v[42:43], off offset:256 sc1
	v_mfma_f32_16x16x32_f16 v[178:181], v[6:9], v[82:85], v[178:181]
	ds_read_b128 v[6:9], v151 offset:384
	ds_read_b128 v[82:85], v151 offset:992
	s_waitcnt vmcnt(24) lgkmcnt(1)
	v_mfma_f32_16x16x32_f16 v[128:131], v[30:33], v[6:9], v[128:131]
	s_waitcnt vmcnt(23)
	v_mfma_f32_16x16x32_f16 v[202:205], v[38:41], v[6:9], v[202:205]
	ds_read_b128 v[6:9], v151 offset:1600
	s_waitcnt lgkmcnt(1)
	v_mfma_f32_16x16x32_f16 v[140:143], v[30:33], v[82:85], v[142:145]
	v_mfma_f32_16x16x32_f16 v[158:161], v[38:41], v[82:85], v[158:161]
	s_waitcnt lgkmcnt(0)
	v_mfma_f32_16x16x32_f16 v[222:225], v[30:33], v[6:9], v[222:225]
	v_mfma_f32_16x16x32_f16 v[110:113], v[38:41], v[6:9], v[110:113]
	v_add_u32_e32 v6, 0x9e3c0, v244
	v_min_u32_e32 v6, v6, v114
	global_load_dwordx4 v[6:9], v6, s[8:9] nt
	s_waitcnt vmcnt(21)
	v_cvt_pk_f16_f32 v83, v88, v89
	v_cvt_pk_f16_f32 v82, v86, v87
	ds_write_b16 v238, v82 offset:4256
	ds_write_b16_d16_hi v239, v82 offset:4256
	ds_write_b16 v240, v83 offset:4256
	ds_write_b16_d16_hi v241, v83 offset:4256
	ds_read_b128 v[82:85], v151 offset:2208
	ds_read_b128 v[86:89], v151 offset:2816
	s_waitcnt lgkmcnt(1)
	v_mfma_f32_16x16x32_f16 v[182:185], v[30:33], v[82:85], v[182:185]
	v_mfma_f32_16x16x32_f16 v[198:201], v[38:41], v[82:85], v[198:201]
	s_waitcnt lgkmcnt(0)
	v_mfma_f32_16x16x32_f16 v[132:135], v[30:33], v[86:89], v[132:135]
	v_mfma_f32_16x16x32_f16 v[144:147], v[38:41], v[86:89], v[146:149]
	ds_read_b128 v[82:85], v151 offset:3424
	ds_read_b128 v[86:89], v151 offset:4032
	s_waitcnt lgkmcnt(1)
	v_mfma_f32_16x16x32_f16 v[206:209], v[30:33], v[82:85], v[206:209]
	v_mfma_f32_16x16x32_f16 v[120:123], v[38:41], v[82:85], v[120:123]
	s_waitcnt lgkmcnt(0)
	v_mfma_f32_16x16x32_f16 v[210:213], v[30:33], v[86:89], v[210:213]
	v_mfma_f32_16x16x32_f16 v[190:193], v[38:41], v[86:89], v[190:193]
	v_add_u32_e32 v82, 0xb4a00, v150
	v_min_u32_e32 v82, v82, v114
	global_load_dwordx4 v[82:85], v82, s[8:9] nt
	s_waitcnt vmcnt(21)
	v_cvt_pk_f16_f32 v87, v92, v93
	v_cvt_pk_f16_f32 v86, v90, v91
	ds_write_b16 v234, v86 offset:4864
	ds_write_b16_d16_hi v235, v86 offset:4864
	ds_write_b16 v236, v87 offset:4864
	ds_write_b16_d16_hi v237, v87 offset:4864
	ds_read_b128 v[86:89], v151 offset:4640
	ds_read_b128 v[90:93], v151 offset:6464
	s_waitcnt lgkmcnt(1)
	v_mfma_f32_16x16x32_f16 v[166:169], v[30:33], v[86:89], v[166:169]
	v_mfma_f32_16x16x32_f16 v[162:165], v[38:41], v[86:89], v[162:165]
	ds_read_b128 v[86:89], v151 offset:5248
	ds_read_b128 v[226:229], v151 offset:5856
	s_waitcnt lgkmcnt(1)
	v_mfma_f32_16x16x32_f16 v[218:221], v[30:33], v[86:89], v[218:221]
	v_mfma_f32_16x16x32_f16 v[136:139], v[38:41], v[86:89], v[136:139]
	s_waitcnt lgkmcnt(0)
	v_mfma_f32_16x16x32_f16 v[170:173], v[30:33], v[226:229], v[170:173]
	v_mfma_f32_16x16x32_f16 v[124:127], v[38:41], v[226:229], v[124:127]
	v_mfma_f32_16x16x32_f16 v[116:119], v[30:33], v[90:93], v[116:119]
	v_mfma_f32_16x16x32_f16 v[90:93], v[38:41], v[90:93], v[174:177]
	v_add_u32_e32 v86, 0xcb040, v244
	v_min_u32_e32 v86, v86, v114
	global_load_dwordx4 v[86:89], v86, s[8:9] nt
	s_waitcnt vmcnt(21)
	v_cvt_pk_f16_f32 v97, v96, v97
	v_cvt_pk_f16_f32 v96, v94, v95
	ds_write_b16 v238, v96 offset:5472
	ds_write_b16_d16_hi v239, v96 offset:5472
	ds_write_b16 v240, v97 offset:5472
	ds_write_b16_d16_hi v241, v97 offset:5472
	ds_read_b128 v[94:97], v151 offset:7072
	ds_read_b128 v[174:177], v151 offset:7680
	s_waitcnt lgkmcnt(1)
	v_mfma_f32_16x16x32_f16 v[186:189], v[30:33], v[94:97], v[186:189]
	v_mfma_f32_16x16x32_f16 v[94:97], v[38:41], v[94:97], v[194:197]
	s_waitcnt lgkmcnt(0)
	v_mfma_f32_16x16x32_f16 v[194:197], v[30:33], v[174:177], v[214:217]
	v_mfma_f32_16x16x32_f16 v[174:177], v[38:41], v[174:177], v[178:181]
	ds_read_b128 v[30:33], v151 offset:448
	ds_read_b128 v[38:41], v151 offset:1056
	s_waitcnt lgkmcnt(1)
	v_mfma_f32_16x16x32_f16 v[128:131], v[22:25], v[30:33], v[128:131]
	v_mfma_f32_16x16x32_f16 v[178:181], v[18:21], v[30:33], v[202:205]
	s_waitcnt lgkmcnt(0)
	v_mfma_f32_16x16x32_f16 v[140:143], v[22:25], v[38:41], v[140:143]
	v_mfma_f32_16x16x32_f16 v[158:161], v[18:21], v[38:41], v[158:161]
	v_add_u32_e32 v30, 0xe1680, v150
	v_min_u32_e32 v30, v30, v114
	global_load_dwordx4 v[30:33], v30, s[8:9] nt
	s_waitcnt vmcnt(21)
	v_cvt_pk_f16_f32 v39, v100, v101
	v_cvt_pk_f16_f32 v38, v98, v99
	ds_write_b16 v234, v38 offset:6080
	ds_write_b16_d16_hi v235, v38 offset:6080
	ds_write_b16 v236, v39 offset:6080
	ds_write_b16_d16_hi v237, v39 offset:6080
	ds_read_b128 v[38:41], v151 offset:1664
	ds_read_b128 v[98:101], v151 offset:2272
	s_waitcnt lgkmcnt(1)
	v_mfma_f32_16x16x32_f16 v[202:205], v[22:25], v[38:41], v[222:225]
	v_mfma_f32_16x16x32_f16 v[214:217], v[18:21], v[38:41], v[110:113]
	ds_read_b128 v[38:41], v151 offset:2880
	s_nop 1
	ds_read_b128 v[110:113], v151 offset:3488
	s_waitcnt lgkmcnt(2)
	v_mfma_f32_16x16x32_f16 v[182:185], v[22:25], v[98:101], v[182:185]
	v_mfma_f32_16x16x32_f16 v[98:101], v[18:21], v[98:101], v[198:201]
	s_waitcnt lgkmcnt(1)
	v_mfma_f32_16x16x32_f16 v[132:135], v[22:25], v[38:41], v[132:135]
	v_mfma_f32_16x16x32_f16 v[144:147], v[18:21], v[38:41], v[144:147]
	s_waitcnt lgkmcnt(0)
	v_mfma_f32_16x16x32_f16 v[198:201], v[22:25], v[110:113], v[206:209]
	v_mfma_f32_16x16x32_f16 v[120:123], v[18:21], v[110:113], v[120:123]
	v_add_u32_e32 v38, 0xf7cc0, v244
	v_min_u32_e32 v38, v38, v114
	global_load_dwordx4 v[38:41], v38, s[8:9] nt
	s_waitcnt vmcnt(21)
	v_cvt_pk_f16_f32 v65, v64, v65
	v_cvt_pk_f16_f32 v64, v62, v63
	ds_write_b16 v238, v64 offset:6688
	ds_write_b16_d16_hi v239, v64 offset:6688
	ds_write_b16 v240, v65 offset:6688
	ds_write_b16_d16_hi v241, v65 offset:6688
	ds_read_b128 v[62:65], v151 offset:4096
	ds_read_b128 v[110:113], v151 offset:4704
	s_waitcnt lgkmcnt(1)
	v_mfma_f32_16x16x32_f16 v[206:209], v[22:25], v[62:65], v[210:213]
	v_mfma_f32_16x16x32_f16 v[62:65], v[18:21], v[62:65], v[190:193]
	s_waitcnt lgkmcnt(0)
	v_mfma_f32_16x16x32_f16 v[166:169], v[22:25], v[110:113], v[166:169]
	v_mfma_f32_16x16x32_f16 v[162:165], v[18:21], v[110:113], v[162:165]
	ds_read_b128 v[110:113], v151 offset:5312
	ds_read_b128 v[190:193], v151 offset:5920
	s_waitcnt lgkmcnt(1)
	v_mfma_f32_16x16x32_f16 v[210:213], v[22:25], v[110:113], v[218:221]
	v_mfma_f32_16x16x32_f16 v[136:139], v[18:21], v[110:113], v[136:139]
	s_waitcnt lgkmcnt(0)
	v_mfma_f32_16x16x32_f16 v[170:173], v[22:25], v[190:193], v[170:173]
	v_mfma_f32_16x16x32_f16 v[124:127], v[18:21], v[190:193], v[124:127]
	v_add_u32_e32 v110, 0x10e300, v150
	v_min_u32_e32 v110, v110, v114
	v_cndmask_b32_e64 v110, 0, v110, s[0:1]
	global_load_dwordx4 v[110:113], v110, s[8:9] nt
	s_waitcnt vmcnt(21)
	v_cvt_pk_f16_f32 v69, v68, v69
	v_cvt_pk_f16_f32 v68, v66, v67
	ds_write_b16 v234, v68 offset:7296
	ds_write_b16_d16_hi v235, v68 offset:7296
	ds_write_b16 v236, v69 offset:7296
	ds_write_b16_d16_hi v237, v69 offset:7296
	ds_read_b128 v[66:69], v151 offset:6528
	ds_read_b128 v[152:155], v151 offset:7136
	s_waitcnt lgkmcnt(1)
	v_mfma_f32_16x16x32_f16 v[116:119], v[22:25], v[66:69], v[116:119]
	v_mfma_f32_16x16x32_f16 v[66:69], v[18:21], v[66:69], v[90:93]
	s_waitcnt lgkmcnt(0)
	v_mfma_f32_16x16x32_f16 v[90:93], v[22:25], v[152:155], v[186:189]
	v_mfma_f32_16x16x32_f16 v[94:97], v[18:21], v[152:155], v[94:97]
	ds_read_b128 v[152:155], v151 offset:7744
	s_waitcnt lgkmcnt(0)
	s_barrier
	v_sub_u32_e32 v245, v234, v243
	v_add_u32_e32 v246, 0xfffffdc0, v245
	v_min_u32_e32 v245, v245, v246
	v_add_u32_e32 v234, v242, v245
	v_sub_u32_e32 v245, v235, v243
	v_add_u32_e32 v246, 0xfffffdc0, v245
	v_min_u32_e32 v245, v245, v246
	v_add_u32_e32 v235, v242, v245
	v_sub_u32_e32 v245, v236, v243
	v_add_u32_e32 v246, 0xfffffdc0, v245
	v_min_u32_e32 v245, v245, v246
	v_add_u32_e32 v236, v242, v245
	v_sub_u32_e32 v245, v237, v243
	v_add_u32_e32 v246, 0xfffffdc0, v245
	v_min_u32_e32 v245, v245, v246
	v_add_u32_e32 v237, v242, v245
	v_sub_u32_e32 v245, v238, v243
	v_add_u32_e32 v246, 0xfffffdc0, v245
	v_min_u32_e32 v245, v245, v246
	v_add_u32_e32 v238, v242, v245
	v_sub_u32_e32 v245, v239, v243
	v_add_u32_e32 v246, 0xfffffdc0, v245
	v_min_u32_e32 v245, v245, v246
	v_add_u32_e32 v239, v242, v245
	v_sub_u32_e32 v245, v240, v243
	v_add_u32_e32 v246, 0xfffffdc0, v245
	v_min_u32_e32 v245, v245, v246
	v_add_u32_e32 v240, v242, v245
	v_sub_u32_e32 v245, v241, v243
	v_add_u32_e32 v246, 0xfffffdc0, v245
	v_min_u32_e32 v245, v245, v246
	v_add_u32_e32 v241, v242, v245
	v_mfma_f32_16x16x32_f16 v[22:25], v[22:25], v[152:155], v[194:197]
	v_mfma_f32_16x16x32_f16 v[18:21], v[18:21], v[152:155], v[174:177]
	v_mov_b32_e32 v114, 0
	ds_read_b128 v[152:155], v151 offset:512
	s_waitcnt vmcnt(20) lgkmcnt(0)
	v_mfma_f32_16x16x32_f16 v[128:131], v[50:53], v[152:155], v[128:131]
	s_waitcnt vmcnt(19)
	v_mfma_f32_16x16x32_f16 v[152:155], v[54:57], v[152:155], v[178:181]
	s_waitcnt vmcnt(16)
	v_cvt_pk_f16_f32 v105, v104, v105
	v_cvt_pk_f16_f32 v104, v102, v103
	ds_write_b16 v234, v104 offset:0
	ds_write_b16_d16_hi v235, v104 offset:0
	ds_write_b16 v236, v105 offset:0
	ds_write_b16_d16_hi v237, v105 offset:0
	ds_read_b128 v[102:105], v151 offset:1120
	ds_read_b128 v[174:177], v151 offset:1728
	ds_read_b128 v[178:181], v151 offset:2336
	ds_read_b128 v[186:189], v151 offset:2944
	s_waitcnt lgkmcnt(3)
	v_mfma_f32_16x16x32_f16 v[140:143], v[50:53], v[102:105], v[140:143]
	v_mfma_f32_16x16x32_f16 v[102:105], v[54:57], v[102:105], v[158:161]
	s_waitcnt lgkmcnt(2)
	v_mfma_f32_16x16x32_f16 v[158:161], v[50:53], v[174:177], v[202:205]
	v_mfma_f32_16x16x32_f16 v[174:177], v[54:57], v[174:177], v[214:217]
	s_waitcnt lgkmcnt(1)
	v_mfma_f32_16x16x32_f16 v[182:185], v[50:53], v[178:181], v[182:185]
	v_mfma_f32_16x16x32_f16 v[98:101], v[54:57], v[178:181], v[98:101]
	s_waitcnt lgkmcnt(0)
	v_mfma_f32_16x16x32_f16 v[132:135], v[50:53], v[186:189], v[132:135]
	v_mfma_f32_16x16x32_f16 v[144:147], v[54:57], v[186:189], v[144:147]
	s_waitcnt vmcnt(15)
	v_cvt_pk_f16_f32 v109, v108, v109
	v_cvt_pk_f16_f32 v108, v106, v107
	ds_write_b16 v238, v108 offset:608
	ds_write_b16_d16_hi v239, v108 offset:608
	ds_write_b16 v240, v109 offset:608
	ds_write_b16_d16_hi v241, v109 offset:608
	ds_read_b128 v[106:109], v151 offset:3552
	ds_read_b128 v[178:181], v151 offset:5376
	s_waitcnt lgkmcnt(1)
	v_mfma_f32_16x16x32_f16 v[186:189], v[50:53], v[106:109], v[198:201]
	v_mfma_f32_16x16x32_f16 v[106:109], v[54:57], v[106:109], v[120:123]
	s_nop 2
	ds_read_b128 v[120:123], v151 offset:4160
	ds_read_b128 v[190:193], v151 offset:4768
	s_waitcnt lgkmcnt(1)
	v_mfma_f32_16x16x32_f16 v[194:197], v[50:53], v[120:123], v[206:209]
	v_mfma_f32_16x16x32_f16 v[62:65], v[54:57], v[120:123], v[62:65]
	s_waitcnt lgkmcnt(0)
	v_mfma_f32_16x16x32_f16 v[120:123], v[50:53], v[190:193], v[166:169]
	v_mfma_f32_16x16x32_f16 v[162:165], v[54:57], v[190:193], v[162:165]
	v_mfma_f32_16x16x32_f16 v[166:169], v[50:53], v[178:181], v[210:213]
	v_mfma_f32_16x16x32_f16 v[136:139], v[54:57], v[178:181], v[136:139]
	s_waitcnt vmcnt(14)
	v_cvt_pk_f16_f32 v61, v60, v61
	v_cvt_pk_f16_f32 v60, v58, v59
	ds_write_b16 v234, v60 offset:1216
	ds_write_b16_d16_hi v235, v60 offset:1216
	ds_write_b16 v236, v61 offset:1216
	ds_write_b16_d16_hi v237, v61 offset:1216
	ds_read_b128 v[58:61], v151 offset:5984
	ds_read_b128 v[178:181], v151 offset:6592
	s_waitcnt lgkmcnt(1)
	v_mfma_f32_16x16x32_f16 v[170:173], v[50:53], v[58:61], v[170:173]
	v_mfma_f32_16x16x32_f16 v[58:61], v[54:57], v[58:61], v[124:127]
	s_waitcnt lgkmcnt(0)
	v_mfma_f32_16x16x32_f16 v[116:119], v[50:53], v[178:181], v[116:119]
	v_mfma_f32_16x16x32_f16 v[66:69], v[54:57], v[178:181], v[66:69]
	ds_read_b128 v[124:127], v151 offset:7200
	ds_read_b128 v[178:181], v151 offset:7808
	s_waitcnt lgkmcnt(1)
	v_mfma_f32_16x16x32_f16 v[90:93], v[50:53], v[124:127], v[90:93]
	v_mfma_f32_16x16x32_f16 v[94:97], v[54:57], v[124:127], v[94:97]
	s_waitcnt lgkmcnt(0)
	v_mfma_f32_16x16x32_f16 v[22:25], v[50:53], v[178:181], v[22:25]
	v_mfma_f32_16x16x32_f16 v[18:21], v[54:57], v[178:181], v[18:21]
	s_waitcnt vmcnt(13)
	v_cvt_pk_f16_f32 v37, v36, v37
	v_cvt_pk_f16_f32 v36, v34, v35
	ds_write_b16 v238, v36 offset:1824
	ds_write_b16_d16_hi v239, v36 offset:1824
	ds_write_b16 v240, v37 offset:1824
	ds_write_b16_d16_hi v241, v37 offset:1824
	ds_read_b128 v[34:37], v151 offset:0
	ds_read_b128 v[50:53], v151 offset:608
	s_waitcnt lgkmcnt(1)
	v_mfma_f32_16x16x32_f16 v[54:57], v[2:5], v[34:37], v[128:131]
	s_waitcnt lgkmcnt(0)
	v_mfma_f32_16x16x32_f16 v[124:127], v[2:5], v[50:53], v[140:143]
	v_mfma_f32_16x16x32_f16 v[50:53], v[26:29], v[50:53], v[102:105]
	s_nop 2
	ds_read_b128 v[102:105], v151 offset:1216
	ds_read_b128 v[128:131], v151 offset:1824
	v_mfma_f32_16x16x32_f16 v[34:37], v[26:29], v[34:37], v[152:155]
	s_waitcnt lgkmcnt(1)
	v_mfma_f32_16x16x32_f16 v[140:143], v[2:5], v[102:105], v[158:161]
	v_mfma_f32_16x16x32_f16 v[102:105], v[26:29], v[102:105], v[174:177]
	s_waitcnt lgkmcnt(0)
	v_mfma_f32_16x16x32_f16 v[152:155], v[2:5], v[128:131], v[182:185]
	v_mfma_f32_16x16x32_f16 v[98:101], v[26:29], v[128:131], v[98:101]
	s_waitcnt vmcnt(12)
	v_cvt_pk_f16_f32 v73, v72, v73
	v_cvt_pk_f16_f32 v72, v70, v71
	ds_write_b16 v234, v72 offset:2432
	ds_write_b16_d16_hi v235, v72 offset:2432
	ds_write_b16 v236, v73 offset:2432
	ds_write_b16_d16_hi v237, v73 offset:2432
	ds_read_b128 v[70:73], v151 offset:2432
	ds_read_b128 v[128:131], v151 offset:3040
	s_waitcnt lgkmcnt(1)
	v_mfma_f32_16x16x32_f16 v[132:135], v[2:5], v[70:73], v[132:135]
	v_mfma_f32_16x16x32_f16 v[70:73], v[26:29], v[70:73], v[144:147]
	s_waitcnt lgkmcnt(0)
	v_mfma_f32_16x16x32_f16 v[144:147], v[2:5], v[128:131], v[186:189]
	v_mfma_f32_16x16x32_f16 v[106:109], v[26:29], v[128:131], v[106:109]
	ds_read_b128 v[128:131], v151 offset:3648
	ds_read_b128 v[158:161], v151 offset:4256
	s_waitcnt lgkmcnt(1)
	v_mfma_f32_16x16x32_f16 v[174:177], v[2:5], v[128:131], v[194:197]
	v_mfma_f32_16x16x32_f16 v[62:65], v[26:29], v[128:131], v[62:65]
	s_waitcnt lgkmcnt(0)
	v_mfma_f32_16x16x32_f16 v[120:123], v[2:5], v[158:161], v[120:123]
	v_mfma_f32_16x16x32_f16 v[128:131], v[26:29], v[158:161], v[162:165]
	s_waitcnt vmcnt(11)
	v_cvt_pk_f16_f32 v77, v76, v77
	v_cvt_pk_f16_f32 v76, v74, v75
	ds_write_b16 v238, v76 offset:3040
	ds_write_b16_d16_hi v239, v76 offset:3040
	ds_write_b16 v240, v77 offset:3040
	ds_write_b16_d16_hi v241, v77 offset:3040
	ds_read_b128 v[74:77], v151 offset:4864
	ds_read_b128 v[158:161], v151 offset:5472
	s_waitcnt lgkmcnt(1)
	v_mfma_f32_16x16x32_f16 v[162:165], v[2:5], v[74:77], v[166:169]
	v_mfma_f32_16x16x32_f16 v[74:77], v[26:29], v[74:77], v[136:139]
	s_waitcnt lgkmcnt(0)
	v_mfma_f32_16x16x32_f16 v[136:139], v[2:5], v[158:161], v[170:173]
	v_mfma_f32_16x16x32_f16 v[58:61], v[26:29], v[158:161], v[58:61]
	ds_read_b128 v[158:161], v151 offset:6080
	ds_read_b128 v[166:169], v151 offset:6688
	s_waitcnt lgkmcnt(1)
	v_mfma_f32_16x16x32_f16 v[116:119], v[2:5], v[158:161], v[116:119]
	v_mfma_f32_16x16x32_f16 v[66:69], v[26:29], v[158:161], v[66:69]
	s_waitcnt lgkmcnt(0)
	v_mfma_f32_16x16x32_f16 v[90:93], v[2:5], v[166:169], v[90:93]
	v_mfma_f32_16x16x32_f16 v[94:97], v[26:29], v[166:169], v[94:97]
	s_waitcnt vmcnt(10)
	v_cvt_pk_f16_f32 v81, v80, v81
	v_cvt_pk_f16_f32 v80, v78, v79
	ds_write_b16 v234, v80 offset:3648
	ds_write_b16_d16_hi v235, v80 offset:3648
	ds_write_b16 v236, v81 offset:3648
	ds_write_b16_d16_hi v237, v81 offset:3648
	ds_read_b128 v[78:81], v151 offset:7296
	s_waitcnt lgkmcnt(0)
	v_mfma_f32_16x16x32_f16 v[2:5], v[2:5], v[78:81], v[22:25]
	v_mfma_f32_16x16x32_f16 v[18:21], v[26:29], v[78:81], v[18:21]
	s_nop 1
	ds_read_b128 v[22:25], v151 offset:64
	ds_read_b128 v[26:29], v151 offset:672
	s_waitcnt vmcnt(9) lgkmcnt(1)
	v_mfma_f32_16x16x32_f16 v[54:57], v[10:13], v[22:25], v[54:57]
	s_waitcnt vmcnt(8)
	v_mfma_f32_16x16x32_f16 v[22:25], v[14:17], v[22:25], v[34:37]
	s_waitcnt lgkmcnt(0)
	v_mfma_f32_16x16x32_f16 v[34:37], v[10:13], v[26:29], v[124:127]
	v_mfma_f32_16x16x32_f16 v[26:29], v[14:17], v[26:29], v[50:53]
	s_nop 2
	ds_read_b128 v[50:53], v151 offset:1280
	s_waitcnt lgkmcnt(0)
	v_mfma_f32_16x16x32_f16 v[78:81], v[10:13], v[50:53], v[140:143]
	v_mfma_f32_16x16x32_f16 v[50:53], v[14:17], v[50:53], v[102:105]
	s_waitcnt vmcnt(5)
	v_cvt_pk_f16_f32 v9, v8, v9
	v_cvt_pk_f16_f32 v8, v6, v7
	ds_write_b16 v238, v8 offset:4256
	ds_write_b16_d16_hi v239, v8 offset:4256
	ds_write_b16 v240, v9 offset:4256
	ds_write_b16_d16_hi v241, v9 offset:4256
	ds_read_b128 v[6:9], v151 offset:1888
	ds_read_b128 v[102:105], v151 offset:2496
	s_waitcnt lgkmcnt(1)
	v_mfma_f32_16x16x32_f16 v[124:127], v[10:13], v[6:9], v[152:155]
	v_mfma_f32_16x16x32_f16 v[6:9], v[14:17], v[6:9], v[98:101]
	s_waitcnt lgkmcnt(0)
	v_mfma_f32_16x16x32_f16 v[132:135], v[10:13], v[102:105], v[132:135]
	v_mfma_f32_16x16x32_f16 v[70:73], v[14:17], v[102:105], v[70:73]
	ds_read_b128 v[98:101], v151 offset:3104
	ds_read_b128 v[102:105], v151 offset:3712
	s_waitcnt lgkmcnt(1)
	v_mfma_f32_16x16x32_f16 v[140:143], v[10:13], v[98:101], v[144:147]
	v_mfma_f32_16x16x32_f16 v[144:147], v[14:17], v[98:101], v[106:109]
	s_waitcnt lgkmcnt(0)
	v_mfma_f32_16x16x32_f16 v[152:155], v[10:13], v[102:105], v[174:177]
	v_mfma_f32_16x16x32_f16 v[158:161], v[14:17], v[102:105], v[62:65]
	s_waitcnt vmcnt(4)
	s_nop 1
	v_cvt_pk_f16_f32 v63, v84, v85
	v_cvt_pk_f16_f32 v62, v82, v83
	ds_write_b16 v234, v62 offset:4864
	ds_write_b16_d16_hi v235, v62 offset:4864
	ds_write_b16 v236, v63 offset:4864
	ds_write_b16_d16_hi v237, v63 offset:4864
	ds_read_b128 v[62:65], v151 offset:4320
	ds_read_b128 v[82:85], v151 offset:6144
	s_waitcnt lgkmcnt(1)
	v_mfma_f32_16x16x32_f16 v[120:123], v[10:13], v[62:65], v[120:123]
	v_mfma_f32_16x16x32_f16 v[128:131], v[14:17], v[62:65], v[128:131]
	ds_read_b128 v[62:65], v151 offset:4928
	ds_read_b128 v[98:101], v151 offset:5536
	s_waitcnt lgkmcnt(1)
	v_mfma_f32_16x16x32_f16 v[162:165], v[10:13], v[62:65], v[162:165]
	v_mfma_f32_16x16x32_f16 v[166:169], v[14:17], v[62:65], v[74:77]
	s_waitcnt lgkmcnt(0)
	v_mfma_f32_16x16x32_f16 v[136:139], v[10:13], v[98:101], v[136:139]
	v_mfma_f32_16x16x32_f16 v[170:173], v[14:17], v[98:101], v[58:61]
	v_mfma_f32_16x16x32_f16 v[116:119], v[10:13], v[82:85], v[116:119]
	v_mfma_f32_16x16x32_f16 v[174:177], v[14:17], v[82:85], v[66:69]
	s_waitcnt vmcnt(3)
	v_cvt_pk_f16_f32 v59, v88, v89
	v_cvt_pk_f16_f32 v58, v86, v87
	ds_write_b16 v238, v58 offset:5472
	ds_write_b16_d16_hi v239, v58 offset:5472
	ds_write_b16 v240, v59 offset:5472
	ds_write_b16_d16_hi v241, v59 offset:5472
	ds_read_b128 v[58:61], v151 offset:6752
	ds_read_b128 v[62:65], v151 offset:7360
	s_waitcnt lgkmcnt(1)
	v_mfma_f32_16x16x32_f16 v[178:181], v[10:13], v[58:61], v[90:93]
	v_mfma_f32_16x16x32_f16 v[182:185], v[14:17], v[58:61], v[94:97]
	s_waitcnt lgkmcnt(0)
	v_mfma_f32_16x16x32_f16 v[2:5], v[10:13], v[62:65], v[2:5]
	v_mfma_f32_16x16x32_f16 v[186:189], v[14:17], v[62:65], v[18:21]
	ds_read_b128 v[10:13], v151 offset:128
	ds_read_b128 v[14:17], v151 offset:736
	s_waitcnt lgkmcnt(1)
	v_mfma_f32_16x16x32_f16 v[148:151], v[46:49], v[10:13], v[54:57]
	v_mfma_f32_16x16x32_f16 v[106:109], v[42:45], v[10:13], v[22:25]
	s_waitcnt lgkmcnt(0)
	v_mfma_f32_16x16x32_f16 v[102:105], v[46:49], v[14:17], v[34:37]
	v_mfma_f32_16x16x32_f16 v[94:97], v[42:45], v[14:17], v[26:29]
	s_waitcnt vmcnt(2)
	v_cvt_pk_f16_f32 v11, v32, v33
	v_cvt_pk_f16_f32 v10, v30, v31
	ds_write_b16 v234, v10 offset:6080
	ds_write_b16_d16_hi v235, v10 offset:6080
	ds_write_b16 v236, v11 offset:6080
	ds_write_b16_d16_hi v237, v11 offset:6080
	ds_read_b128 v[10:13], v151 offset:1344
	ds_read_b128 v[14:17], v151 offset:1952
	s_waitcnt lgkmcnt(1)
	v_mfma_f32_16x16x32_f16 v[98:101], v[46:49], v[10:13], v[78:81]
	v_mfma_f32_16x16x32_f16 v[90:93], v[42:45], v[10:13], v[50:53]
	s_waitcnt lgkmcnt(0)
	v_mfma_f32_16x16x32_f16 v[82:85], v[42:45], v[14:17], v[6:9]
	s_nop 2
	ds_read_b128 v[6:9], v151 offset:2560
	ds_read_b128 v[10:13], v151 offset:3168
	v_mfma_f32_16x16x32_f16 v[86:89], v[46:49], v[14:17], v[124:127]
	s_waitcnt lgkmcnt(1)
	v_mfma_f32_16x16x32_f16 v[78:81], v[46:49], v[6:9], v[132:135]
	v_mfma_f32_16x16x32_f16 v[74:77], v[42:45], v[6:9], v[70:73]
	s_waitcnt lgkmcnt(0)
	v_mfma_f32_16x16x32_f16 v[70:73], v[46:49], v[10:13], v[140:143]
	v_mfma_f32_16x16x32_f16 v[62:65], v[42:45], v[10:13], v[144:147]
	s_waitcnt vmcnt(1)
	v_cvt_pk_f16_f32 v7, v40, v41
	v_cvt_pk_f16_f32 v6, v38, v39
	ds_write_b16 v238, v6 offset:6688
	ds_write_b16_d16_hi v239, v6 offset:6688
	ds_write_b16 v240, v7 offset:6688
	ds_write_b16_d16_hi v241, v7 offset:6688
	ds_read_b128 v[6:9], v151 offset:3776
	ds_read_b128 v[10:13], v151 offset:4384
	s_waitcnt lgkmcnt(1)
	v_mfma_f32_16x16x32_f16 v[66:69], v[46:49], v[6:9], v[152:155]
	v_mfma_f32_16x16x32_f16 v[58:61], v[42:45], v[6:9], v[158:161]
	s_waitcnt lgkmcnt(0)
	v_mfma_f32_16x16x32_f16 v[54:57], v[46:49], v[10:13], v[120:123]
	v_mfma_f32_16x16x32_f16 v[50:53], v[42:45], v[10:13], v[128:131]
	ds_read_b128 v[6:9], v151 offset:4992
	ds_read_b128 v[10:13], v151 offset:5600
	s_waitcnt lgkmcnt(1)
	v_mfma_f32_16x16x32_f16 v[38:41], v[46:49], v[6:9], v[162:165]
	v_mfma_f32_16x16x32_f16 v[34:37], v[42:45], v[6:9], v[166:169]
	s_waitcnt lgkmcnt(0)
	v_mfma_f32_16x16x32_f16 v[30:33], v[46:49], v[10:13], v[136:139]
	v_mfma_f32_16x16x32_f16 v[18:21], v[42:45], v[10:13], v[170:173]
	s_waitcnt vmcnt(0)
	v_cvt_pk_f16_f32 v7, v112, v113
	v_cvt_pk_f16_f32 v6, v110, v111
	ds_write_b16 v234, v6 offset:7296
	ds_write_b16_d16_hi v235, v6 offset:7296
	ds_write_b16 v236, v7 offset:7296
	ds_write_b16_d16_hi v237, v7 offset:7296
	ds_read_b128 v[6:9], v151 offset:6208
	ds_read_b128 v[10:13], v151 offset:6816
	ds_read_b128 v[110:113], v151 offset:7424
	s_waitcnt lgkmcnt(0)
	s_barrier
	v_mfma_f32_16x16x32_f16 v[22:25], v[46:49], v[6:9], v[116:119]
	s_barrier
	v_mfma_f32_16x16x32_f16 v[26:29], v[42:45], v[6:9], v[174:177]
	s_movk_i32 s0, 0xffe0
	v_lshrrev_b32_e32 v6, 2, v0
	v_and_b32_e32 v1, 15, v0
	v_ashrrev_i32_e32 v114, 1, v0
	v_and_b32_e32 v116, 12, v6
	v_mfma_f32_16x16x32_f16 v[14:17], v[46:49], v[10:13], v[178:181]
	v_and_or_b32 v120, v114, s0, v116
	v_lshlrev_b32_e32 v114, 3, v1
	v_lshlrev_b32_e32 v129, 1, v120
	v_mfma_f32_16x16x32_f16 v[6:9], v[46:49], v[110:113], v[2:5]
	v_mov_b32_e32 v46, 0x1f480
	v_lshl_add_u32 v128, v120, 2, v46
	v_or_b32_e32 v46, 0x1ee00, v114
	v_or_b32_e32 v47, 0x1ee80, v114
	v_or_b32_e32 v48, 0x1ef00, v114
	v_or_b32_e32 v49, 0x1ef80, v114
	v_mfma_f32_16x16x32_f16 v[10:13], v[42:45], v[10:13], v[182:185]
	s_movk_i32 s4, 0x210
	s_movk_i32 s0, 0x1880
	v_cmp_gt_i32_e32 vcc, s0, v0
	v_mfma_f32_16x16x32_f16 v[2:5], v[42:45], v[110:113], v[186:189]
	ds_read_b128 v[42:45], v128
	ds_read_b64 v[124:125], v46
	ds_read_b64 v[126:127], v47
	ds_read_b64 v[118:119], v48
	ds_read_b64 v[116:117], v49
	ds_read_b128 v[46:49], v128
	ds_read_b128 v[120:123], v128 offset:64
	s_waitcnt lgkmcnt(4)
	v_pk_fma_f32 v[104:105], v[126:127], v[44:45], v[104:105] op_sel_hi:[0,1,1]
	v_pk_fma_f32 v[102:103], v[126:127], v[42:43], v[102:103] op_sel_hi:[0,1,1]
	s_waitcnt lgkmcnt(0)
	v_pk_fma_f32 v[108:109], v[124:125], v[122:123], v[108:109] op_sel_hi:[0,1,1]
	v_pk_fma_f32 v[106:107], v[124:125], v[120:121], v[106:107] op_sel_hi:[0,1,1]
	v_pk_mul_f32 v[108:109], v[124:125], v[108:109] op_sel:[1,0]
	v_pk_mul_f32 v[106:107], v[124:125], v[106:107] op_sel:[1,0]
	v_cvt_pk_f16_f32 v109, v108, v109
	v_cvt_pk_f16_f32 v108, v106, v107
	v_or_b32_e32 v106, 32, v129
	v_mad_u32_u24 v107, v1, s4, v106
	ds_write_b64 v107, v[108:109]
	v_mov_b32_e32 v107, 0x2100
	v_pk_fma_f32 v[96:97], v[126:127], v[122:123], v[96:97] op_sel_hi:[0,1,1]
	v_pk_fma_f32 v[94:95], v[126:127], v[120:121], v[94:95] op_sel_hi:[0,1,1]
	v_mad_u32_u24 v107, v1, s4, v107
	v_pk_mul_f32 v[96:97], v[126:127], v[96:97] op_sel:[1,0]
	v_pk_mul_f32 v[94:95], v[126:127], v[94:95] op_sel:[1,0]
	v_pk_mul_f32 v[104:105], v[126:127], v[104:105] op_sel:[1,0]
	v_pk_mul_f32 v[102:103], v[126:127], v[102:103] op_sel:[1,0]
	v_cvt_pk_f16_f32 v97, v96, v97
	v_cvt_pk_f16_f32 v96, v94, v95
	v_add_u32_e32 v94, v107, v106
	v_cvt_pk_f16_f32 v105, v104, v105
	v_cvt_pk_f16_f32 v104, v102, v103
	v_add_u32_e32 v102, v107, v129
	ds_write_b64 v94, v[96:97]
	v_mov_b32_e32 v94, 0x4200
	v_pk_fma_f32 v[92:93], v[118:119], v[122:123], v[92:93] op_sel_hi:[0,1,1]
	v_pk_fma_f32 v[90:91], v[118:119], v[120:121], v[90:91] op_sel_hi:[0,1,1]
	ds_write_b64 v102, v[104:105]
	v_mad_u32_u24 v102, v1, s4, v94
	v_pk_mul_f32 v[92:93], v[118:119], v[92:93] op_sel:[1,0]
	v_pk_mul_f32 v[90:91], v[118:119], v[90:91] op_sel:[1,0]
	v_cvt_pk_f16_f32 v93, v92, v93
	v_cvt_pk_f16_f32 v92, v90, v91
	v_add_u32_e32 v90, v102, v106
	ds_write_b64 v90, v[92:93]
	v_mov_b32_e32 v90, 0x6300
	v_pk_fma_f32 v[84:85], v[116:117], v[122:123], v[84:85] op_sel_hi:[0,1,1]
	v_pk_fma_f32 v[82:83], v[116:117], v[120:121], v[82:83] op_sel_hi:[0,1,1]
	v_pk_fma_f32 v[110:111], v[124:125], v[44:45], v[150:151] op_sel_hi:[0,1,1]
	v_pk_fma_f32 v[112:113], v[124:125], v[42:43], v[148:149] op_sel_hi:[0,1,1]
	v_mad_u32_u24 v90, v1, s4, v90
	v_pk_mul_f32 v[84:85], v[116:117], v[84:85] op_sel:[1,0]
	v_pk_mul_f32 v[82:83], v[116:117], v[82:83] op_sel:[1,0]
	v_pk_mul_f32 v[110:111], v[124:125], v[110:111] op_sel:[1,0]
	v_pk_mul_f32 v[112:113], v[124:125], v[112:113] op_sel:[1,0]
	v_cvt_pk_f16_f32 v85, v84, v85
	v_cvt_pk_f16_f32 v84, v82, v83
	v_add_u32_e32 v82, v90, v106
	v_cvt_pk_f16_f32 v111, v110, v111
	v_cvt_pk_f16_f32 v110, v112, v113
	v_mad_u32_u24 v112, v1, s4, v129
	ds_write_b64 v82, v[84:85]
	v_or_b32_e32 v82, 0x1f000, v114
	ds_write_b64 v112, v[110:111]
	ds_read_b128 v[110:113], v128
	ds_read_b64 v[82:83], v82
	v_pk_fma_f32 v[94:95], v[118:119], v[44:45], v[100:101] op_sel_hi:[0,1,1]
	v_pk_fma_f32 v[96:97], v[118:119], v[42:43], v[98:99] op_sel_hi:[0,1,1]
	v_pk_fma_f32 v[88:89], v[116:117], v[44:45], v[88:89] op_sel_hi:[0,1,1]
	v_pk_fma_f32 v[86:87], v[116:117], v[42:43], v[86:87] op_sel_hi:[0,1,1]
	v_pk_mul_f32 v[94:95], v[118:119], v[94:95] op_sel:[1,0]
	v_pk_mul_f32 v[96:97], v[118:119], v[96:97] op_sel:[1,0]
	v_pk_mul_f32 v[88:89], v[116:117], v[88:89] op_sel:[1,0]
	v_pk_mul_f32 v[86:87], v[116:117], v[86:87] op_sel:[1,0]
	v_mov_b32_e32 v84, 0x8400
	s_waitcnt lgkmcnt(0)
	v_pk_fma_f32 v[44:45], v[82:83], v[44:45], v[80:81] op_sel_hi:[0,1,1]
	v_pk_fma_f32 v[42:43], v[82:83], v[42:43], v[78:79] op_sel_hi:[0,1,1]
	v_cvt_pk_f16_f32 v95, v94, v95
	v_cvt_pk_f16_f32 v94, v96, v97
	v_add_u32_e32 v96, v102, v129
	v_cvt_pk_f16_f32 v89, v88, v89
	v_cvt_pk_f16_f32 v88, v86, v87
	v_add_u32_e32 v86, v90, v129
	v_mad_u32_u24 v90, v1, s4, v84
	v_pk_mul_f32 v[44:45], v[82:83], v[44:45] op_sel:[1,0]
	v_pk_mul_f32 v[42:43], v[82:83], v[42:43] op_sel:[1,0]
	ds_write_b64 v96, v[94:95]
	ds_write_b64 v86, v[88:89]
	v_or_b32_e32 v84, 0x1f080, v114
	v_or_b32_e32 v86, 0x1f100, v114
	v_or_b32_e32 v88, 0x1f180, v114
	v_cvt_pk_f16_f32 v45, v44, v45
	v_cvt_pk_f16_f32 v44, v42, v43
	v_add_u32_e32 v42, v90, v129
	ds_read_b64 v[84:85], v84
	ds_read_b64 v[86:87], v86
	ds_read_b64 v[88:89], v88
	ds_write_b64 v42, v[44:45]
	v_pk_fma_f32 v[42:43], v[82:83], v[122:123], v[76:77] op_sel_hi:[0,1,1]
	v_pk_fma_f32 v[44:45], v[82:83], v[120:121], v[74:75] op_sel_hi:[0,1,1]
	v_pk_mul_f32 v[42:43], v[82:83], v[42:43] op_sel:[1,0]
	v_pk_mul_f32 v[44:45], v[82:83], v[44:45] op_sel:[1,0]
	v_cvt_pk_f16_f32 v43, v42, v43
	v_cvt_pk_f16_f32 v42, v44, v45
	v_add_u32_e32 v44, v90, v106
	ds_write_b64 v44, v[42:43]
	v_mov_b32_e32 v42, 0xa500
	v_mad_u32_u24 v74, v1, s4, v42
	s_waitcnt lgkmcnt(4)
	v_pk_fma_f32 v[42:43], v[84:85], v[48:49], v[72:73] op_sel_hi:[0,1,1]
	v_pk_fma_f32 v[44:45], v[84:85], v[46:47], v[70:71] op_sel_hi:[0,1,1]
	v_pk_mul_f32 v[42:43], v[84:85], v[42:43] op_sel:[1,0]
	v_pk_mul_f32 v[70:71], v[84:85], v[44:45] op_sel:[1,0]
	v_cvt_pk_f16_f32 v73, v42, v43
	ds_read_b128 v[42:45], v128 offset:64
	v_cvt_pk_f16_f32 v72, v70, v71
	v_add_u32_e32 v70, v74, v129
	ds_write_b64 v70, v[72:73]
	ds_read_b128 v[70:73], v128 offset:64
	s_waitcnt lgkmcnt(2)
	v_pk_fma_f32 v[64:65], v[84:85], v[44:45], v[64:65] op_sel_hi:[0,1,1]
	v_pk_fma_f32 v[62:63], v[84:85], v[42:43], v[62:63] op_sel_hi:[0,1,1]
	v_pk_mul_f32 v[64:65], v[84:85], v[64:65] op_sel:[1,0]
	v_pk_mul_f32 v[62:63], v[84:85], v[62:63] op_sel:[1,0]
	v_cvt_pk_f16_f32 v65, v64, v65
	v_cvt_pk_f16_f32 v64, v62, v63
	v_add_u32_e32 v62, v74, v106
	ds_write_b64 v62, v[64:65]
	v_mov_b32_e32 v62, 0xc600
	v_pk_fma_f32 v[60:61], v[86:87], v[44:45], v[60:61] op_sel_hi:[0,1,1]
	v_pk_fma_f32 v[58:59], v[86:87], v[42:43], v[58:59] op_sel_hi:[0,1,1]
	v_mad_u32_u24 v74, v1, s4, v62
	v_pk_mul_f32 v[60:61], v[86:87], v[60:61] op_sel:[1,0]
	v_pk_mul_f32 v[58:59], v[86:87], v[58:59] op_sel:[1,0]
	v_cvt_pk_f16_f32 v61, v60, v61
	v_cvt_pk_f16_f32 v60, v58, v59
	v_add_u32_e32 v58, v74, v106
	ds_write_b64 v58, v[60:61]
	v_mov_b32_e32 v58, 0xe700
	v_pk_fma_f32 v[52:53], v[88:89], v[44:45], v[52:53] op_sel_hi:[0,1,1]
	v_pk_fma_f32 v[50:51], v[88:89], v[42:43], v[50:51] op_sel_hi:[0,1,1]
	v_mad_u32_u24 v58, v1, s4, v58
	v_pk_mul_f32 v[52:53], v[88:89], v[52:53] op_sel:[1,0]
	v_pk_mul_f32 v[50:51], v[88:89], v[50:51] op_sel:[1,0]
	v_cvt_pk_f16_f32 v53, v52, v53
	v_cvt_pk_f16_f32 v52, v50, v51
	v_add_u32_e32 v50, v58, v106
	ds_write_b64 v50, v[52:53]
	v_or_b32_e32 v50, 0x1f200, v114
	ds_read_b64 v[50:51], v50
	v_pk_fma_f32 v[62:63], v[86:87], v[48:49], v[68:69] op_sel_hi:[0,1,1]
	v_pk_fma_f32 v[64:65], v[86:87], v[46:47], v[66:67] op_sel_hi:[0,1,1]
	v_pk_fma_f32 v[56:57], v[88:89], v[48:49], v[56:57] op_sel_hi:[0,1,1]
	v_pk_fma_f32 v[54:55], v[88:89], v[46:47], v[54:55] op_sel_hi:[0,1,1]
	v_pk_mul_f32 v[62:63], v[86:87], v[62:63] op_sel:[1,0]
	v_pk_mul_f32 v[64:65], v[86:87], v[64:65] op_sel:[1,0]
	v_pk_mul_f32 v[56:57], v[88:89], v[56:57] op_sel:[1,0]
	v_pk_mul_f32 v[54:55], v[88:89], v[54:55] op_sel:[1,0]
	v_cvt_pk_f16_f32 v63, v62, v63
	v_cvt_pk_f16_f32 v62, v64, v65
	v_add_u32_e32 v64, v74, v129
	v_cvt_pk_f16_f32 v57, v56, v57
	v_cvt_pk_f16_f32 v56, v54, v55
	v_add_u32_e32 v54, v58, v129
	v_mov_b32_e32 v52, 0x10800
	ds_write_b64 v64, v[62:63]
	ds_write_b64 v54, v[56:57]
	v_mad_u32_u24 v58, v1, s4, v52
	v_or_b32_e32 v52, 0x1f280, v114
	v_or_b32_e32 v54, 0x1f300, v114
	v_or_b32_e32 v56, 0x1f380, v114
	ds_read_b64 v[52:53], v52
	ds_read_b64 v[54:55], v54
	ds_read_b64 v[56:57], v56
	s_waitcnt lgkmcnt(5)
	v_pk_fma_f32 v[36:37], v[50:51], v[44:45], v[36:37] op_sel_hi:[0,1,1]
	v_pk_fma_f32 v[34:35], v[50:51], v[42:43], v[34:35] op_sel_hi:[0,1,1]
	v_pk_mul_f32 v[36:37], v[50:51], v[36:37] op_sel:[1,0]
	v_pk_mul_f32 v[34:35], v[50:51], v[34:35] op_sel:[1,0]
	v_cvt_pk_f16_f32 v37, v36, v37
	v_cvt_pk_f16_f32 v36, v34, v35
	v_add_u32_e32 v34, v58, v106
	v_pk_fma_f32 v[40:41], v[50:51], v[48:49], v[40:41] op_sel_hi:[0,1,1]
	v_pk_fma_f32 v[38:39], v[50:51], v[46:47], v[38:39] op_sel_hi:[0,1,1]
	ds_write_b64 v34, v[36:37]
	v_mov_b32_e32 v34, 0x12900
	s_waitcnt lgkmcnt(3)
	v_pk_fma_f32 v[20:21], v[52:53], v[44:45], v[20:21] op_sel_hi:[0,1,1]
	v_pk_fma_f32 v[18:19], v[52:53], v[42:43], v[18:19] op_sel_hi:[0,1,1]
	v_pk_mul_f32 v[40:41], v[50:51], v[40:41] op_sel:[1,0]
	v_pk_mul_f32 v[38:39], v[50:51], v[38:39] op_sel:[1,0]
	v_mad_u32_u24 v34, v1, s4, v34
	v_pk_fma_f32 v[32:33], v[52:53], v[48:49], v[32:33] op_sel_hi:[0,1,1]
	v_pk_fma_f32 v[30:31], v[52:53], v[46:47], v[30:31] op_sel_hi:[0,1,1]
	v_pk_mul_f32 v[20:21], v[52:53], v[20:21] op_sel:[1,0]
	v_pk_mul_f32 v[18:19], v[52:53], v[18:19] op_sel:[1,0]
	v_cvt_pk_f16_f32 v41, v40, v41
	v_cvt_pk_f16_f32 v40, v38, v39
	v_add_u32_e32 v38, v58, v129
	v_pk_mul_f32 v[32:33], v[52:53], v[32:33] op_sel:[1,0]
	v_pk_mul_f32 v[30:31], v[52:53], v[30:31] op_sel:[1,0]
	v_cvt_pk_f16_f32 v21, v20, v21
	v_cvt_pk_f16_f32 v20, v18, v19
	v_add_u32_e32 v18, v34, v106
	ds_write_b64 v38, v[40:41]
	v_cvt_pk_f16_f32 v33, v32, v33
	v_cvt_pk_f16_f32 v32, v30, v31
	v_add_u32_e32 v30, v34, v129
	ds_write_b64 v18, v[20:21]
	v_mov_b32_e32 v18, 0x14a00
	ds_write_b64 v30, v[32:33]
	v_mad_u32_u24 v30, v1, s4, v18
	s_waitcnt lgkmcnt(5)
	v_pk_fma_f32 v[18:19], v[54:55], v[112:113], v[24:25] op_sel_hi:[0,1,1]
	v_pk_fma_f32 v[20:21], v[54:55], v[110:111], v[22:23] op_sel_hi:[0,1,1]
	v_pk_mul_f32 v[18:19], v[54:55], v[18:19] op_sel:[1,0]
	v_pk_mul_f32 v[20:21], v[54:55], v[20:21] op_sel:[1,0]
	v_cvt_pk_f16_f32 v19, v18, v19
	v_cvt_pk_f16_f32 v18, v20, v21
	v_add_u32_e32 v20, v30, v129
	s_waitcnt lgkmcnt(4)
	v_pk_fma_f32 v[12:13], v[56:57], v[72:73], v[12:13] op_sel_hi:[0,1,1]
	v_pk_fma_f32 v[10:11], v[56:57], v[70:71], v[10:11] op_sel_hi:[0,1,1]
	ds_write_b64 v20, v[18:19]
	v_pk_fma_f32 v[18:19], v[54:55], v[72:73], v[28:29] op_sel_hi:[0,1,1]
	v_pk_fma_f32 v[20:21], v[54:55], v[70:71], v[26:27] op_sel_hi:[0,1,1]
	v_pk_mul_f32 v[12:13], v[56:57], v[12:13] op_sel:[1,0]
	v_pk_mul_f32 v[10:11], v[56:57], v[10:11] op_sel:[1,0]
	v_pk_mul_f32 v[18:19], v[54:55], v[18:19] op_sel:[1,0]
	v_pk_mul_f32 v[20:21], v[54:55], v[20:21] op_sel:[1,0]
	v_cvt_pk_f16_f32 v13, v12, v13
	v_cvt_pk_f16_f32 v12, v10, v11
	v_or_b32_e32 v10, 0x1f400, v114
	v_cvt_pk_f16_f32 v19, v18, v19
	v_cvt_pk_f16_f32 v18, v20, v21
	v_add_u32_e32 v20, v30, v106
	ds_read_b64 v[10:11], v10
	ds_write_b64 v20, v[18:19]
	v_mov_b32_e32 v18, 0x16b00
	v_pk_fma_f32 v[16:17], v[56:57], v[112:113], v[16:17] op_sel_hi:[0,1,1]
	v_pk_fma_f32 v[14:15], v[56:57], v[110:111], v[14:15] op_sel_hi:[0,1,1]
	v_mad_u32_u24 v18, v1, s4, v18
	v_pk_mul_f32 v[16:17], v[56:57], v[16:17] op_sel:[1,0]
	v_pk_mul_f32 v[14:15], v[56:57], v[14:15] op_sel:[1,0]
	v_cvt_pk_f16_f32 v17, v16, v17
	v_cvt_pk_f16_f32 v16, v14, v15
	v_add_u32_e32 v14, v18, v129
	ds_write_b64 v14, v[16:17]
	v_add_u32_e32 v14, v18, v106
	ds_write_b64 v14, v[12:13]
	v_mov_b32_e32 v12, 0x18c00
	s_waitcnt lgkmcnt(3)
	v_pk_fma_f32 v[8:9], v[10:11], v[112:113], v[8:9] op_sel_hi:[0,1,1]
	v_pk_fma_f32 v[6:7], v[10:11], v[110:111], v[6:7] op_sel_hi:[0,1,1]
	v_pk_fma_f32 v[4:5], v[10:11], v[72:73], v[4:5] op_sel_hi:[0,1,1]
	v_pk_fma_f32 v[2:3], v[10:11], v[70:71], v[2:3] op_sel_hi:[0,1,1]
	v_mad_u32_u24 v1, v1, s4, v12
	v_pk_mul_f32 v[8:9], v[10:11], v[8:9] op_sel:[1,0]
	v_pk_mul_f32 v[6:7], v[10:11], v[6:7] op_sel:[1,0]
	v_pk_mul_f32 v[4:5], v[10:11], v[4:5] op_sel:[1,0]
	v_pk_mul_f32 v[2:3], v[10:11], v[2:3] op_sel:[1,0]
	v_cvt_pk_f16_f32 v9, v8, v9
	v_cvt_pk_f16_f32 v8, v6, v7
	v_add_u32_e32 v6, v1, v129
	v_cvt_pk_f16_f32 v5, v4, v5
	v_cvt_pk_f16_f32 v4, v2, v3
	v_add_u32_e32 v1, v1, v106
	ds_write_b64 v6, v[8:9]
	ds_write_b64 v1, v[4:5]
	s_waitcnt lgkmcnt(0)
	s_barrier
	s_and_saveexec_b64 s[0:1], vcc
	s_cbranch_execz .LBB2_12
	v_lshlrev_b32_e32 v1, 4, v0
	v_and_b32_e32 v114, 0x70, v1
	v_lshl_add_u64 v[2:3], s[6:7], 0, v[114:115]
	s_mov_b64 s[0:1], 0
	s_mov_b32 s5, 0x5397829d
	s_movk_i32 s6, 0xf9e0
	s_mov_b32 s7, 0xc350
	s_movk_i32 s8, 0x167f
	s_branch .LBB2_10

	.amdhsa_kernel _Z6k_gemmPKfPKDv8_DF16_S0_S0_PDF16_
		.amdhsa_group_segment_fixed_size 129152
		.amdhsa_private_segment_fixed_size 0
		.amdhsa_kernarg_size 40
		.amdhsa_user_sgpr_count 2
		.amdhsa_user_sgpr_dispatch_ptr 0
		.amdhsa_user_sgpr_queue_ptr 0
		.amdhsa_user_sgpr_kernarg_segment_ptr 1
		.amdhsa_user_sgpr_dispatch_id 0
		.amdhsa_user_sgpr_kernarg_preload_length 0
		.amdhsa_user_sgpr_kernarg_preload_offset 0
		.amdhsa_user_sgpr_private_segment_size 0
		.amdhsa_uses_dynamic_stack 0
		.amdhsa_enable_private_segment 0
		.amdhsa_system_sgpr_workgroup_id_x 1
		.amdhsa_system_sgpr_workgroup_id_y 0
		.amdhsa_system_sgpr_workgroup_id_z 0
		.amdhsa_system_sgpr_workgroup_info 0
		.amdhsa_system_vgpr_workitem_id 0
		.amdhsa_next_free_vgpr 256
		.amdhsa_next_free_sgpr 96
		.amdhsa_accum_offset 256
		.amdhsa_reserve_vcc 1
		.amdhsa_float_round_mode_32 0
		.amdhsa_float_round_mode_16_64 0
		.amdhsa_float_denorm_mode_32 3
		.amdhsa_float_denorm_mode_16_64 3
		.amdhsa_dx10_clamp 1
		.amdhsa_ieee_mode 1
		.amdhsa_fp16_overflow 0
		.amdhsa_tg_split 0
		.amdhsa_exception_fp_ieee_invalid_op 0
		.amdhsa_exception_fp_denorm_src 0
		.amdhsa_exception_fp_ieee_div_zero 0
		.amdhsa_exception_fp_ieee_overflow 0
		.amdhsa_exception_fp_ieee_underflow 0
		.amdhsa_exception_fp_ieee_inexact 0
		.amdhsa_exception_int_div_zero 0
	.end_amdhsa_kernel

amdhsa.kernels:
  - .agpr_count:     0
    .args:
      - .actual_access:  read_only
        .address_space:  global
        .offset:         0
        .size:           8
        .value_kind:     global_buffer
      - .actual_access:  write_only
        .address_space:  global
        .offset:         8
        .size:           8
        .value_kind:     global_buffer
      - .actual_access:  write_only
        .address_space:  global
        .offset:         16
        .size:           8
        .value_kind:     global_buffer
      - .actual_access:  read_only
        .address_space:  global
        .offset:         24
        .size:           8
        .value_kind:     global_buffer
      - .actual_access:  write_only
        .address_space:  global
        .offset:         32
        .size:           8
        .value_kind:     global_buffer
      - .actual_access:  write_only
        .address_space:  global
        .offset:         40
        .size:           8
        .value_kind:     global_buffer
    .group_segment_fixed_size: 14576
    .kernarg_segment_align: 8
    .kernarg_segment_size: 48
    .language:       OpenCL C
    .language_version:
      - 2
      - 0
    .max_flat_workgroup_size: 256
    .name:           _Z5k_binPKiPiPjPKfPDv8_DF16_PDF16_
    .private_segment_fixed_size: 0
    .sgpr_count:     22
    .sgpr_spill_count: 0
    .symbol:         _Z5k_binPKiPiPjPKfPDv8_DF16_PDF16_.kd
    .uniform_work_group_size: 1
    .uses_dynamic_stack: false
    .vgpr_count:     75
    .vgpr_spill_count: 0
    .wavefront_size: 64
  - .agpr_count:     0
    .args:
      - .actual_access:  read_only
        .address_space:  global
        .offset:         0
        .size:           8
        .value_kind:     global_buffer
      - .actual_access:  read_only
        .address_space:  global
        .offset:         8
        .size:           8
        .value_kind:     global_buffer
      - .actual_access:  write_only
        .address_space:  global
        .offset:         16
        .size:           8
        .value_kind:     global_buffer
      - .actual_access:  write_only
        .address_space:  global
        .offset:         24
        .size:           8
        .value_kind:     global_buffer
      - .actual_access:  write_only
        .address_space:  global
        .offset:         32
        .size:           8
        .value_kind:     global_buffer
      - .actual_access:  write_only
        .address_space:  global
        .offset:         40
        .size:           8
        .value_kind:     global_buffer
    .group_segment_fixed_size: 18452
    .kernarg_segment_align: 8
    .kernarg_segment_size: 48
    .language:       OpenCL C
    .language_version:
      - 2
      - 0
    .max_flat_workgroup_size: 256
    .name:           _Z5k_csrPKiPKjP15HIP_vector_typeIiLj2EEPfPtS6_
    .private_segment_fixed_size: 0
    .sgpr_count:     94
    .sgpr_spill_count: 0
    .symbol:         _Z5k_csrPKiPKjP15HIP_vector_typeIiLj2EEPfPtS6_.kd
    .uniform_work_group_size: 1
    .uses_dynamic_stack: false
    .vgpr_count:     65
    .vgpr_spill_count: 0
    .wavefront_size: 64
  - .agpr_count:     0
    .args:
      - .actual_access:  read_only
        .address_space:  global
        .offset:         0
        .size:           8
        .value_kind:     global_buffer
      - .actual_access:  read_only
        .address_space:  global
        .offset:         8
        .size:           8
        .value_kind:     global_buffer
      - .actual_access:  read_only
        .address_space:  global
        .offset:         16
        .size:           8
        .value_kind:     global_buffer
      - .actual_access:  read_only
        .address_space:  global
        .offset:         24
        .size:           8
        .value_kind:     global_buffer
      - .actual_access:  write_only
        .address_space:  global
        .offset:         32
        .size:           8
        .value_kind:     global_buffer
    .group_segment_fixed_size: 129152
    .kernarg_segment_align: 8
    .kernarg_segment_size: 40
    .language:       OpenCL C
    .language_version:
      - 2
      - 0
    .max_flat_workgroup_size: 512
    .name:           _Z6k_gemmPKfPKDv8_DF16_S0_S0_PDF16_
    .private_segment_fixed_size: 0
    .sgpr_count:     22
    .sgpr_spill_count: 0
    .symbol:         _Z6k_gemmPKfPKDv8_DF16_S0_S0_PDF16_.kd
    .uniform_work_group_size: 1
    .uses_dynamic_stack: false
    .vgpr_count:     256
    .vgpr_spill_count: 0
    .wavefront_size: 64
  - .agpr_count:     0
    .args:
      - .actual_access:  read_only
        .address_space:  global
        .offset:         0
        .size:           8
        .value_kind:     global_buffer
      - .actual_access:  read_only
        .address_space:  global
        .offset:         8
        .size:           8
        .value_kind:     global_buffer
      - .actual_access:  read_only
        .address_space:  global
        .offset:         16
        .size:           8
        .value_kind:     global_buffer
      - .actual_access:  read_only
        .address_space:  global
        .offset:         24
        .size:           8
        .value_kind:     global_buffer
      - .actual_access:  read_only
        .address_space:  global
        .offset:         32
        .size:           8
        .value_kind:     global_buffer
      - .actual_access:  read_only
        .address_space:  global
        .offset:         40
        .size:           8
        .value_kind:     global_buffer
      - .address_space:  global
        .offset:         48
        .size:           8
        .value_kind:     global_buffer
    .group_segment_fixed_size: 2304
    .kernarg_segment_align: 8
    .kernarg_segment_size: 56
    .language:       OpenCL C
    .language_version:
      - 2
      - 0
    .max_flat_workgroup_size: 320
    .name:           _Z6k_agg1PKDF16_PK15HIP_vector_typeIiLj2EEPKtPKfS8_S8_Pf
    .private_segment_fixed_size: 0
    .sgpr_count:     40
    .sgpr_spill_count: 0
    .symbol:         _Z6k_agg1PKDF16_PK15HIP_vector_typeIiLj2EEPKtPKfS8_S8_Pf.kd
    .uniform_work_group_size: 1
    .uses_dynamic_stack: false
    .vgpr_count:     62
    .vgpr_spill_count: 0
    .wavefront_size: 64
  - .agpr_count:     0
    .args:
      - .actual_access:  read_only
        .address_space:  global
        .offset:         0
        .size:           8
        .value_kind:     global_buffer
      - .actual_access:  read_only
        .address_space:  global
        .offset:         8
        .size:           8
        .value_kind:     global_buffer
      - .actual_access:  read_only
        .address_space:  global
        .offset:         16
        .size:           8
        .value_kind:     global_buffer
      - .actual_access:  read_only
        .address_space:  global
        .offset:         24
        .size:           8
        .value_kind:     global_buffer
      - .actual_access:  read_only
        .address_space:  global
        .offset:         32
        .size:           8
        .value_kind:     global_buffer
      - .actual_access:  write_only
        .address_space:  global
        .offset:         40
        .size:           8
        .value_kind:     global_buffer
    .group_segment_fixed_size: 0
    .kernarg_segment_align: 8
    .kernarg_segment_size: 48
    .language:       OpenCL C
    .language_version:
      - 2
      - 0
    .max_flat_workgroup_size: 256
    .name:           _Z5k_outPKfPK15HIP_vector_typeIiLj2EEPKtS0_S0_Pf
    .private_segment_fixed_size: 0
    .sgpr_count:     18
    .sgpr_spill_count: 0
    .symbol:         _Z5k_outPKfPK15HIP_vector_typeIiLj2EEPKtS0_S0_Pf.kd
    .uniform_work_group_size: 1
    .uses_dynamic_stack: false
    .vgpr_count:     27
    .vgpr_spill_count: 0
    .wavefront_size: 64
